# v67 + non-temporal hint on the in-projection epilogue's output stores (145 MB per layer written while the GEMM relies on L2 for its A/B tiles)
# baseline (speedup 1.0000x reference)
; __device__ __forceinline__ u32x4 pack8(f32x4 a, f32x4 b) { u32x4 w; w.x = pk2(a[0], a[1]); w.y = pk2(a[2], a[3]); w.z = pk2(b[0], b[1]); w.w = pk2(b[2], b[3]); return w; }
; __device__ __forceinline__ float sq8(const f32x4& a, const f32x4& b) { return ((a[0] * a[0] + a[1] * a[1]) + (a[2] * a[2] + a[3] * a[3])) + ((b[0] * b[0] + b[1] * b[1]) + (b[2] * b[2] + b[3] * b[3])); }
;     __device__ __forceinline__ void operator()(const f32x4 (&acc)[2][2][4][2], const Unit& u, int ui, int wr, int wc, int fr, int fq, LAS unsigned char* lds) const {
;     ...
;                     const int c = bj * 128 + wc * 32 + fq * 8;
;                     f32x4 v0 = acc[ai][bj][m][0] * rs, v1 = acc[ai][bj][m][1] * rs;
;                     if (pn < 6) { if (pn < 2) { v0 = v0 * QS_SB; v1 = v1 * QS_SB; } *(u32x4*)(QKV + (size_t)row * 1536 + pn * 256 + c) = pack8(v0, v1); }
;                     else if (pn == 6) { *(u32x4*)(CKV + (size_t)row * 256 + c) = pack8(v0, v1); sq += sq8(v0, v1); }
;                     else if (pn == 7) { *(u32x4*)(CQ + (size_t)row * 384 + c) = pack8(v0, v1); sq += sq8(v0, v1); }
;                     else if (bj == 0) { *(u32x4*)(CQ + (size_t)row * 384 + 256 + c) = pack8(v0, v1); sq += sq8(v0, v1); }
.Lin_nopf:
	s_mov_b64 s[16:17], -1
	s_and_b64 vcc, exec, s[14:15]
	s_cbranch_vccz .LBB0_362
	v_cvt_pk_bf16_f32 v114, v130, v131
	v_cvt_pk_bf16_f32 v115, v132, v133
	v_cvt_pk_bf16_f32 v116, v126, v127
	v_cvt_pk_bf16_f32 v117, v128, v129
	s_cmp_lt_i32 s26, 7
	s_cbranch_scc1 .LBB0_359
	s_cmp_lg_u32 s26, 7
	s_cbranch_scc0 .LBB0_356
	v_lshl_add_u64 v[154:155], s[40:41], 0, v[142:143]
	v_lshlrev_b32_e32 v0, 1, v145
	v_lshl_add_u64 v[154:155], v[154:155], 0, v[0:1]
	v_mov_b32_e32 v156, v131
	v_mov_b32_e32 v157, v127
	global_store_dwordx4 v[154:155], v[114:117], off offset:512 nt
	v_mov_b32_e32 v154, v130
	v_mov_b32_e32 v155, v126
	v_pk_mul_f32 v[156:157], v[156:157], v[156:157]
	v_mov_b32_e32 v158, v133
	v_mov_b32_e32 v159, v129
	v_pk_fma_f32 v[154:155], v[154:155], v[154:155], v[156:157]
	v_mov_b32_e32 v156, v132
	v_mov_b32_e32 v157, v128
	v_pk_mul_f32 v[158:159], v[158:159], v[158:159]
	s_mov_b64 s[16:17], 0
	v_pk_fma_f32 v[156:157], v[156:157], v[156:157], v[158:159]
	s_nop 0
	v_pk_add_f32 v[154:155], v[154:155], v[156:157]
	s_nop 0
	v_add_f32_e32 v153, v154, v155
.LBB0_356:
	s_andn2_b64 vcc, exec, s[16:17]
	s_cbranch_vccnz .LBB0_358
	v_lshl_add_u64 v[154:155], s[40:41], 0, v[142:143]
	v_lshlrev_b32_e32 v0, 1, v145
	v_lshl_add_u64 v[154:155], v[154:155], 0, v[0:1]
	v_mov_b32_e32 v156, v131
	v_mov_b32_e32 v157, v127
	global_store_dwordx4 v[154:155], v[114:117], off nt
	v_mov_b32_e32 v154, v130
	v_mov_b32_e32 v155, v126
	v_pk_mul_f32 v[156:157], v[156:157], v[156:157]
	v_mov_b32_e32 v158, v133
	v_mov_b32_e32 v159, v129
	v_pk_fma_f32 v[154:155], v[154:155], v[154:155], v[156:157]
	v_mov_b32_e32 v156, v132
	v_mov_b32_e32 v157, v128
	v_pk_mul_f32 v[158:159], v[158:159], v[158:159]
	s_nop 0
	v_pk_fma_f32 v[156:157], v[156:157], v[156:157], v[158:159]
	s_nop 0
	v_pk_add_f32 v[154:155], v[154:155], v[156:157]
	s_nop 0
	v_add_f32_e32 v153, v154, v155

; __device__ __forceinline__ u32x4 pack8(f32x4 a, f32x4 b) { u32x4 w; w.x = pk2(a[0], a[1]); w.y = pk2(a[2], a[3]); w.z = pk2(b[0], b[1]); w.w = pk2(b[2], b[3]); return w; }
; __device__ __forceinline__ float sq8(const f32x4& a, const f32x4& b) { return ((a[0] * a[0] + a[1] * a[1]) + (a[2] * a[2] + a[3] * a[3])) + ((b[0] * b[0] + b[1] * b[1]) + (b[2] * b[2] + b[3] * b[3])); }
;     __device__ __forceinline__ void operator()(const f32x4 (&acc)[2][2][4][2], const Unit& u, int ui, int wr, int wc, int fr, int fq, LAS unsigned char* lds) const {
;     ...
;                 for (int bj = 0; bj < 2; ++bj) {
;                     const int c = bj * 128 + wc * 32 + fq * 8;
;                     f32x4 v0 = acc[ai][bj][m][0] * rs, v1 = acc[ai][bj][m][1] * rs;
;                     if (pn < 6) { if (pn < 2) { v0 = v0 * QS_SB; v1 = v1 * QS_SB; } *(u32x4*)(QKV + (size_t)row * 1536 + pn * 256 + c) = pack8(v0, v1); }
;                     else if (pn == 6) { *(u32x4*)(CKV + (size_t)row * 256 + c) = pack8(v0, v1); sq += sq8(v0, v1); }
.LBB0_359:
	s_andn2_b64 vcc, exec, s[16:17]
	s_cbranch_vccnz .LBB0_361
	v_lshl_add_u64 v[154:155], s[38:39], 0, v[140:141]
	v_lshlrev_b32_e32 v0, 1, v145
	v_lshl_add_u64 v[154:155], v[154:155], 0, v[0:1]
	global_store_dwordx4 v[154:155], v[114:117], off nt
	v_mov_b32_e32 v154, v133
	v_mov_b32_e32 v155, v129
	v_mov_b32_e32 v116, v131
	v_mov_b32_e32 v117, v127
	v_mov_b32_e32 v114, v130
	v_mov_b32_e32 v115, v126
	v_pk_mul_f32 v[116:117], v[116:117], v[116:117]
	v_pk_mul_f32 v[154:155], v[154:155], v[154:155]
	v_pk_fma_f32 v[114:115], v[114:115], v[114:115], v[116:117]
	v_mov_b32_e32 v116, v132
	v_mov_b32_e32 v117, v128
	v_pk_fma_f32 v[116:117], v[116:117], v[116:117], v[154:155]
	s_nop 0
	v_pk_add_f32 v[114:115], v[114:115], v[116:117]
	s_nop 0
	v_add_f32_e32 v153, v114, v115

; __device__ __forceinline__ float xor32(float x) { auto rr = __builtin_amdgcn_permlane32_swap(__float_as_uint(x), __float_as_uint(x), false, false); return __uint_as_float(((unsigned)(threadIdx.x & 32)) ? rr[0] : rr[1]); }
; __device__ __forceinline__ u32x4 pack8(f32x4 a, f32x4 b) { u32x4 w; w.x = pk2(a[0], a[1]); w.y = pk2(a[2], a[3]); w.z = pk2(b[0], b[1]); w.w = pk2(b[2], b[3]); return w; }
; __device__ __forceinline__ float sq8(const f32x4& a, const f32x4& b) { return ((a[0] * a[0] + a[1] * a[1]) + (a[2] * a[2] + a[3] * a[3])) + ((b[0] * b[0] + b[1] * b[1]) + (b[2] * b[2] + b[3] * b[3])); }
;     __device__ __forceinline__ void operator()(const f32x4 (&acc)[2][2][4][2], const Unit& u, int ui, int wr, int wc, int fr, int fq, LAS unsigned char* lds) const {
;     ...
;                     f32x4 v0 = acc[ai][bj][m][0] * rs, v1 = acc[ai][bj][m][1] * rs;
;                     if (pn < 6) { if (pn < 2) { v0 = v0 * QS_SB; v1 = v1 * QS_SB; } *(u32x4*)(QKV + (size_t)row * 1536 + pn * 256 + c) = pack8(v0, v1); }
;                     else if (pn == 6) { *(u32x4*)(CKV + (size_t)row * 256 + c) = pack8(v0, v1); sq += sq8(v0, v1); }
;                     else if (pn == 7) { *(u32x4*)(CQ + (size_t)row * 384 + c) = pack8(v0, v1); sq += sq8(v0, v1); }
;                     else if (bj == 0) { *(u32x4*)(CQ + (size_t)row * 384 + 256 + c) = pack8(v0, v1); sq += sq8(v0, v1); }
;                     else if (wc == 0) {
;                         const int ib = 8 * (fq & 1);
;                         const f32x4 c0 = *(const f32x4*)(COS + (size_t)row * 16 + ib), c1 = *(const f32x4*)(COS + (size_t)row * 16 + ib + 4);
;                         const f32x4 s0 = *(const f32x4*)(SIN + (size_t)row * 16 + ib), s1 = *(const f32x4*)(SIN + (size_t)row * 16 + ib + 4);
;                         f32x4 p0, p1;
; #pragma unroll
;                         for (int i = 0; i < 4; ++i) { p0[i] = xor32(v0[i]); p1[i] = xor32(v1[i]); }
;                         const float sg = (fq < 2) ? -1.f : 1.f;
;                         const f32x4 o0 = v0 * c0 + p0 * s0 * sg, o1 = v1 * c1 + p1 * s1 * sg;
;                         *(u32x4*)(KR + (size_t)row * 32 + fq * 8) = pack8(o0, o1);
.LBB0_362:
	s_movk_i32 s6, 0xc00
	s_lshl_b32 s62, s26, 8
	v_mad_i64_i32 v[114:115], s[6:7], v138, s6, 0
	s_ashr_i32 s63, s62, 31
	v_lshl_add_u64 v[114:115], s[36:37], 0, v[114:115]
	s_and_b64 vcc, exec, s[16:17]
	v_lshlrev_b32_e32 v0, 1, v145
	v_lshl_add_u64 v[116:117], s[62:63], 1, v[114:115]
	s_cbranch_vccz .LBB0_364
	v_pk_mul_f32 v[114:115], v[132:133], s[96:97] op_sel_hi:[1,0]
	v_pk_mul_f32 v[154:155], v[130:131], s[96:97] op_sel_hi:[1,0]
	v_pk_mul_f32 v[156:157], v[128:129], s[96:97] op_sel_hi:[1,0]
	v_pk_mul_f32 v[158:159], v[126:127], s[96:97] op_sel_hi:[1,0]
	v_cndmask_b32_e64 v129, v129, v157, s[12:13]
	v_cndmask_b32_e64 v145, v128, v156, s[12:13]
	v_cndmask_b32_e64 v128, v127, v159, s[12:13]
	v_cndmask_b32_e64 v153, v126, v158, s[12:13]
	v_cndmask_b32_e64 v115, v133, v115, s[12:13]
	v_cndmask_b32_e64 v114, v132, v114, s[12:13]
	v_cndmask_b32_e64 v126, v131, v155, s[12:13]
	v_cndmask_b32_e64 v127, v130, v154, s[12:13]
	v_cvt_pk_bf16_f32 v126, v127, v126
	v_cvt_pk_bf16_f32 v127, v114, v115
	v_cvt_pk_bf16_f32 v128, v153, v128
	v_cvt_pk_bf16_f32 v129, v145, v129
	v_lshl_add_u64 v[114:115], v[116:117], 0, v[0:1]
	v_mov_b32_e32 v153, 0
	global_store_dwordx4 v[114:115], v[126:129], off nt
.LBB0_364:
	v_cmp_gt_u32_e32 vcc, 2, v152
	v_mov_b32_e32 v145, v144
	v_mov_b32_e32 v130, v144
	v_cndmask_b32_e64 v114, 1.0, -1.0, vcc
	v_mov_b32_e32 v131, v144
	v_cndmask_b32_e64 v129, 0, 1, s[14:15]
	v_and_b32_e32 v128, 8, v149
	v_mov_b32_e32 v115, v114
	v_lshlrev_b64 v[126:127], 4, v[138:139]
	v_pk_mul_f32 v[124:125], v[124:125], v[130:131]
	v_pk_mul_f32 v[122:123], v[122:123], v[144:145]
	v_pk_mul_f32 v[120:121], v[120:121], v[130:131]
	v_pk_mul_f32 v[118:119], v[118:119], v[144:145]
	v_cmp_ne_u32_e64 s[18:19], 1, v129
	s_andn2_b64 vcc, exec, s[14:15]
	s_mov_b64 s[14:15], -1
	s_cbranch_vccnz .LBB0_376
	s_cmp_lt_i32 s26, 7
	s_cbranch_scc1 .LBB0_373
	s_cmp_lg_u32 s26, 7
	s_cbranch_scc0 .LBB0_370
	s_andn2_b64 vcc, exec, s[56:57]
	s_cbranch_vccnz .LBB0_369
	v_lshlrev_b64 v[158:159], 2, v[126:127]
	v_lshl_add_u64 v[130:131], s[44:45], 0, v[158:159]
	v_lshlrev_b32_e32 v160, 2, v128
	v_mov_b32_e32 v161, v1
	v_lshl_add_u64 v[158:159], s[46:47], 0, v[158:159]
	v_lshl_add_u64 v[154:155], v[130:131], 0, v[160:161]
	v_lshl_add_u64 v[162:163], v[158:159], 0, v[160:161]
	s_waitcnt vmcnt(5)
	v_mov_b32_e32 v130, v214
	v_mov_b32_e32 v131, v215
	v_mov_b32_e32 v132, v216
	v_mov_b32_e32 v133, v217
	v_mov_b32_e32 v154, v218
	v_mov_b32_e32 v155, v219
	v_mov_b32_e32 v156, v220
	v_mov_b32_e32 v157, v221
	v_mov_b32_e32 v158, v222
	v_mov_b32_e32 v159, v223
	v_mov_b32_e32 v160, v224
	v_mov_b32_e32 v161, v225
	v_mov_b32_e32 v162, v226
	v_mov_b32_e32 v163, v227
	v_mov_b32_e32 v164, v228
	v_mov_b32_e32 v165, v229
	global_load_dwordx4 v[214:217], v[202:203], off offset:2048
	global_load_dwordx4 v[218:221], v[202:203], off offset:2064
	global_load_dwordx4 v[222:225], v[204:205], off offset:2048
	global_load_dwordx4 v[226:229], v[204:205], off offset:2064
	v_mov_b32_e32 v129, v122
	v_mov_b32_e32 v166, v122
	s_nop 1
	v_permlane32_swap_b32_e32 v129, v166
	v_cndmask_b32_e64 v166, v129, v166, s[4:5]
	v_mov_b32_e32 v129, v118
	v_mov_b32_e32 v167, v118
	s_nop 1
	v_permlane32_swap_b32_e32 v129, v167
	v_cndmask_b32_e64 v168, v129, v167, s[4:5]
	v_mov_b32_e32 v129, v123
	v_mov_b32_e32 v167, v123
	s_nop 1
	v_permlane32_swap_b32_e32 v129, v167
	v_cndmask_b32_e64 v167, v129, v167, s[4:5]
	v_mov_b32_e32 v129, v119
	v_mov_b32_e32 v169, v119
	s_nop 1
	v_permlane32_swap_b32_e32 v129, v169
	v_cndmask_b32_e64 v169, v129, v169, s[4:5]
	v_mov_b32_e32 v129, v124
	v_mov_b32_e32 v170, v124
	s_nop 1
	v_permlane32_swap_b32_e32 v129, v170
	v_cndmask_b32_e64 v170, v129, v170, s[4:5]
	v_mov_b32_e32 v129, v120
	v_mov_b32_e32 v171, v120
	s_nop 1
	v_permlane32_swap_b32_e32 v129, v171
	v_cndmask_b32_e64 v172, v129, v171, s[4:5]
	v_mov_b32_e32 v129, v125
	v_mov_b32_e32 v171, v125
	s_nop 1
	v_permlane32_swap_b32_e32 v129, v171
	v_cndmask_b32_e64 v171, v129, v171, s[4:5]
	v_mov_b32_e32 v129, v121
	v_mov_b32_e32 v173, v121
	s_nop 1
	v_permlane32_swap_b32_e32 v129, v173
	v_cndmask_b32_e64 v173, v129, v173, s[4:5]
	v_lshlrev_b64 v[144:145], 6, v[138:139]
	v_lshl_add_u64 v[144:145], s[42:43], 0, v[144:145]
	s_waitcnt lgkmcnt(0)
	v_pk_mul_f32 v[160:161], v[160:161], v[170:171]
	v_pk_mul_f32 v[158:159], v[158:159], v[166:167]
	v_mov_b32_e32 v166, v114
	v_mov_b32_e32 v167, v114
	v_pk_mul_f32 v[160:161], v[166:167], v[160:161]
	v_pk_mul_f32 v[158:159], v[114:115], v[158:159]
	v_pk_fma_f32 v[132:133], v[124:125], v[132:133], v[160:161]
	v_pk_mul_f32 v[160:161], v[162:163], v[168:169]
	v_pk_fma_f32 v[130:131], v[122:123], v[130:131], v[158:159]
	v_pk_mul_f32 v[158:159], v[164:165], v[172:173]
	v_pk_mul_f32 v[160:161], v[114:115], v[160:161]
	v_pk_mul_f32 v[158:159], v[166:167], v[158:159]
	v_pk_fma_f32 v[154:155], v[118:119], v[154:155], v[160:161]
	v_pk_fma_f32 v[156:157], v[120:121], v[156:157], v[158:159]
	v_cvt_pk_bf16_f32 v130, v130, v131
	v_cvt_pk_bf16_f32 v131, v132, v133
	v_cvt_pk_bf16_f32 v132, v154, v155
	v_lshlrev_b32_e32 v154, 1, v149
	v_mov_b32_e32 v155, v1
	v_cvt_pk_bf16_f32 v133, v156, v157
	v_lshl_add_u64 v[144:145], v[144:145], 0, v[154:155]
	global_store_dwordx4 v[144:145], v[130:133], off nt

; __device__ __forceinline__ u32x4 pack8(f32x4 a, f32x4 b) { u32x4 w; w.x = pk2(a[0], a[1]); w.y = pk2(a[2], a[3]); w.z = pk2(b[0], b[1]); w.w = pk2(b[2], b[3]); return w; }
; __device__ __forceinline__ float sq8(const f32x4& a, const f32x4& b) { return ((a[0] * a[0] + a[1] * a[1]) + (a[2] * a[2] + a[3] * a[3])) + ((b[0] * b[0] + b[1] * b[1]) + (b[2] * b[2] + b[3] * b[3])); }
;     __device__ __forceinline__ void operator()(const f32x4 (&acc)[2][2][4][2], const Unit& u, int ui, int wr, int wc, int fr, int fq, LAS unsigned char* lds) const {
;     ...
;                 for (int bj = 0; bj < 2; ++bj) {
;                     const int c = bj * 128 + wc * 32 + fq * 8;
;                     f32x4 v0 = acc[ai][bj][m][0] * rs, v1 = acc[ai][bj][m][1] * rs;
;                     if (pn < 6) { if (pn < 2) { v0 = v0 * QS_SB; v1 = v1 * QS_SB; } *(u32x4*)(QKV + (size_t)row * 1536 + pn * 256 + c) = pack8(v0, v1); }
;                     else if (pn == 6) { *(u32x4*)(CKV + (size_t)row * 256 + c) = pack8(v0, v1); sq += sq8(v0, v1); }
;                     else if (pn == 7) { *(u32x4*)(CQ + (size_t)row * 384 + c) = pack8(v0, v1); sq += sq8(v0, v1); }
.LBB0_370:
	s_andn2_b64 vcc, exec, s[14:15]
	v_mov_b32_e32 v129, v153
	s_cbranch_vccnz .LBB0_372
	v_lshl_add_u64 v[142:143], s[40:41], 0, v[142:143]
	v_cvt_pk_bf16_f32 v130, v122, v123
	v_cvt_pk_bf16_f32 v131, v124, v125
	v_cvt_pk_bf16_f32 v132, v118, v119
	v_cvt_pk_bf16_f32 v133, v120, v121
	v_lshl_add_u64 v[142:143], v[142:143], 0, v[0:1]
	global_store_dwordx4 v[142:143], v[130:133], off offset:256 nt
	v_mov_b32_e32 v142, v125
	v_mov_b32_e32 v143, v121
	v_mov_b32_e32 v132, v123
	v_mov_b32_e32 v133, v119
	v_mov_b32_e32 v130, v122
	v_mov_b32_e32 v131, v118
	v_pk_mul_f32 v[132:133], v[132:133], v[132:133]
	v_pk_mul_f32 v[142:143], v[142:143], v[142:143]
	v_pk_fma_f32 v[130:131], v[130:131], v[130:131], v[132:133]
	v_mov_b32_e32 v132, v124
	v_mov_b32_e32 v133, v120
	v_pk_fma_f32 v[132:133], v[132:133], v[132:133], v[142:143]
	s_nop 0
	v_pk_add_f32 v[130:131], v[130:131], v[132:133]
	s_nop 0
	v_add_f32_e32 v129, v130, v131
	v_add_f32_e32 v129, v129, v153

; __device__ __forceinline__ u32x4 pack8(f32x4 a, f32x4 b) { u32x4 w; w.x = pk2(a[0], a[1]); w.y = pk2(a[2], a[3]); w.z = pk2(b[0], b[1]); w.w = pk2(b[2], b[3]); return w; }
; __device__ __forceinline__ float sq8(const f32x4& a, const f32x4& b) { return ((a[0] * a[0] + a[1] * a[1]) + (a[2] * a[2] + a[3] * a[3])) + ((b[0] * b[0] + b[1] * b[1]) + (b[2] * b[2] + b[3] * b[3])); }
;     __device__ __forceinline__ void operator()(const f32x4 (&acc)[2][2][4][2], const Unit& u, int ui, int wr, int wc, int fr, int fq, LAS unsigned char* lds) const {
;     ...
;                 for (int bj = 0; bj < 2; ++bj) {
;                     const int c = bj * 128 + wc * 32 + fq * 8;
;                     f32x4 v0 = acc[ai][bj][m][0] * rs, v1 = acc[ai][bj][m][1] * rs;
;                     if (pn < 6) { if (pn < 2) { v0 = v0 * QS_SB; v1 = v1 * QS_SB; } *(u32x4*)(QKV + (size_t)row * 1536 + pn * 256 + c) = pack8(v0, v1); }
;                     else if (pn == 6) { *(u32x4*)(CKV + (size_t)row * 256 + c) = pack8(v0, v1); sq += sq8(v0, v1); }
.LBB0_373:
	s_andn2_b64 vcc, exec, s[14:15]
	s_cbranch_vccnz .LBB0_375
	v_lshl_add_u64 v[140:141], s[38:39], 0, v[140:141]
	v_cvt_pk_bf16_f32 v130, v122, v123
	v_cvt_pk_bf16_f32 v131, v124, v125
	v_cvt_pk_bf16_f32 v132, v118, v119
	v_cvt_pk_bf16_f32 v133, v120, v121
	v_lshl_add_u64 v[140:141], v[140:141], 0, v[0:1]
	global_store_dwordx4 v[140:141], v[130:133], off offset:256 nt
	v_mov_b32_e32 v140, v125
	v_mov_b32_e32 v141, v121
	v_mov_b32_e32 v132, v123
	v_mov_b32_e32 v133, v119
	v_mov_b32_e32 v130, v122
	v_mov_b32_e32 v131, v118
	v_pk_mul_f32 v[132:133], v[132:133], v[132:133]
	v_pk_mul_f32 v[140:141], v[140:141], v[140:141]
	v_pk_fma_f32 v[130:131], v[130:131], v[130:131], v[132:133]
	v_mov_b32_e32 v132, v124
	v_mov_b32_e32 v133, v120
	v_pk_fma_f32 v[132:133], v[132:133], v[132:133], v[140:141]
	s_nop 0
	v_pk_add_f32 v[130:131], v[130:131], v[132:133]
	s_nop 0
	v_add_f32_e32 v129, v130, v131
	v_add_f32_e32 v129, v129, v153

; __device__ __forceinline__ u32x4 pack8(f32x4 a, f32x4 b) { u32x4 w; w.x = pk2(a[0], a[1]); w.y = pk2(a[2], a[3]); w.z = pk2(b[0], b[1]); w.w = pk2(b[2], b[3]); return w; }
;     __device__ __forceinline__ void operator()(const f32x4 (&acc)[2][2][4][2], const Unit& u, int ui, int wr, int wc, int fr, int fq, LAS unsigned char* lds) const {
;     ...
;                 for (int bj = 0; bj < 2; ++bj) {
;                     const int c = bj * 128 + wc * 32 + fq * 8;
;                     f32x4 v0 = acc[ai][bj][m][0] * rs, v1 = acc[ai][bj][m][1] * rs;
;                     if (pn < 6) { if (pn < 2) { v0 = v0 * QS_SB; v1 = v1 * QS_SB; } *(u32x4*)(QKV + (size_t)row * 1536 + pn * 256 + c) = pack8(v0, v1); }
.LBB0_376:
	s_and_b64 vcc, exec, s[14:15]
	s_cbranch_vccz .LBB0_378
	v_pk_mul_f32 v[130:131], v[124:125], s[96:97] op_sel_hi:[1,0]
	v_pk_mul_f32 v[132:133], v[122:123], s[96:97] op_sel_hi:[1,0]
	v_pk_mul_f32 v[140:141], v[120:121], s[96:97] op_sel_hi:[1,0]
	v_pk_mul_f32 v[142:143], v[118:119], s[96:97] op_sel_hi:[1,0]
	v_cndmask_b32_e64 v121, v121, v141, s[12:13]
	v_cndmask_b32_e64 v129, v120, v140, s[12:13]
	v_cndmask_b32_e64 v120, v119, v143, s[12:13]
	v_cndmask_b32_e64 v140, v118, v142, s[12:13]
	v_cndmask_b32_e64 v119, v125, v131, s[12:13]
	v_cndmask_b32_e64 v124, v124, v130, s[12:13]
	v_cndmask_b32_e64 v118, v123, v133, s[12:13]
	v_cndmask_b32_e64 v122, v122, v132, s[12:13]
	v_cvt_pk_bf16_f32 v118, v122, v118
	v_cvt_pk_bf16_f32 v119, v124, v119
	v_cvt_pk_bf16_f32 v120, v140, v120
	v_cvt_pk_bf16_f32 v121, v129, v121
	v_lshl_add_u64 v[116:117], v[116:117], 0, v[0:1]
	v_mov_b32_e32 v129, v153
	global_store_dwordx4 v[116:117], v[118:121], off offset:256 nt

; __device__ __forceinline__ u32x4 pack8(f32x4 a, f32x4 b) { u32x4 w; w.x = pk2(a[0], a[1]); w.y = pk2(a[2], a[3]); w.z = pk2(b[0], b[1]); w.w = pk2(b[2], b[3]); return w; }
; __device__ __forceinline__ float sq8(const f32x4& a, const f32x4& b) { return ((a[0] * a[0] + a[1] * a[1]) + (a[2] * a[2] + a[3] * a[3])) + ((b[0] * b[0] + b[1] * b[1]) + (b[2] * b[2] + b[3] * b[3])); }
; __device__ __forceinline__ f32x2 rtab_get(LAS unsigned char* lds, int ui, int r) { return ((const LAS f32x2*)(lds + RTAB_OFF))[(ui & 1) * 256 + r]; }
;     __device__ __forceinline__ void operator()(const f32x4 (&acc)[2][2][4][2], const Unit& u, int ui, int wr, int wc, int fr, int fq, LAS unsigned char* lds) const {
;     ...
;                 const int rr = ai * 128 + wr * 64 + m * 16 + fr, row = u.pm * 256 + rr; const float rs = rtab_get(lds, ui, rr)[0];
;                 float sq = 0.f;
; #pragma unroll
;                 for (int bj = 0; bj < 2; ++bj) {
;                     const int c = bj * 128 + wc * 32 + fq * 8;
;                     f32x4 v0 = acc[ai][bj][m][0] * rs, v1 = acc[ai][bj][m][1] * rs;
;                     if (pn < 6) { if (pn < 2) { v0 = v0 * QS_SB; v1 = v1 * QS_SB; } *(u32x4*)(QKV + (size_t)row * 1536 + pn * 256 + c) = pack8(v0, v1); }
;                     else if (pn == 6) { *(u32x4*)(CKV + (size_t)row * 256 + c) = pack8(v0, v1); sq += sq8(v0, v1); }
;                     else if (pn == 7) { *(u32x4*)(CQ + (size_t)row * 384 + c) = pack8(v0, v1); sq += sq8(v0, v1); }
;                     else if (bj == 0) { *(u32x4*)(CQ + (size_t)row * 384 + 256 + c) = pack8(v0, v1); sq += sq8(v0, v1); }
.LBB0_382:
	ds_read_b32 v122, v150 offset:128
	v_add3_u32 v116, s3, v151, 16
	v_ashrrev_i32_e32 v117, 31, v116
	v_mad_i64_i32 v[120:121], s[6:7], v116, s59, 0
	v_lshlrev_b64 v[118:119], 9, v[116:117]
	s_waitcnt lgkmcnt(0)
	v_pk_mul_f32 v[112:113], v[112:113], v[122:123] op_sel_hi:[1,0]
	v_pk_mul_f32 v[110:111], v[110:111], v[122:123] op_sel_hi:[1,0]
	v_pk_mul_f32 v[126:127], v[108:109], v[122:123] op_sel_hi:[1,0]
	v_pk_mul_f32 v[124:125], v[106:107], v[122:123] op_sel_hi:[1,0]
	s_and_b64 vcc, exec, s[18:19]
	s_mov_b64 s[20:21], -1
	s_cbranch_vccnz .LBB0_392
	v_cvt_pk_bf16_f32 v106, v110, v111
	v_cvt_pk_bf16_f32 v107, v112, v113
	v_cvt_pk_bf16_f32 v108, v124, v125
	v_cvt_pk_bf16_f32 v109, v126, v127
	s_cmp_lt_i32 s26, 7
	s_cbranch_scc1 .LBB0_389
	s_cmp_lg_u32 s26, 7
	s_cbranch_scc0 .LBB0_386
	v_lshl_add_u64 v[130:131], s[40:41], 0, v[120:121]
	v_lshl_add_u64 v[130:131], v[130:131], 0, v[0:1]
	v_mov_b32_e32 v132, v111
	v_mov_b32_e32 v133, v125
	global_store_dwordx4 v[130:131], v[106:109], off offset:512 nt
	v_mov_b32_e32 v130, v110
	v_mov_b32_e32 v131, v124
	v_pk_mul_f32 v[132:133], v[132:133], v[132:133]
	v_mov_b32_e32 v140, v113
	v_mov_b32_e32 v141, v127
	v_pk_fma_f32 v[130:131], v[130:131], v[130:131], v[132:133]
	v_mov_b32_e32 v132, v112
	v_mov_b32_e32 v133, v126
	v_pk_mul_f32 v[140:141], v[140:141], v[140:141]
	s_mov_b64 s[20:21], 0
	v_pk_fma_f32 v[132:133], v[132:133], v[132:133], v[140:141]
	s_nop 0
	v_pk_add_f32 v[130:131], v[130:131], v[132:133]
	s_nop 0
	v_add_f32_e32 v129, v130, v131
.LBB0_386:
	s_andn2_b64 vcc, exec, s[20:21]
	s_cbranch_vccnz .LBB0_388
	v_lshl_add_u64 v[130:131], s[40:41], 0, v[120:121]
	v_lshl_add_u64 v[130:131], v[130:131], 0, v[0:1]
	v_mov_b32_e32 v132, v111
	v_mov_b32_e32 v133, v125
	global_store_dwordx4 v[130:131], v[106:109], off nt
	v_mov_b32_e32 v130, v110
	v_mov_b32_e32 v131, v124
	v_pk_mul_f32 v[132:133], v[132:133], v[132:133]
	v_mov_b32_e32 v140, v113
	v_mov_b32_e32 v141, v127
	v_pk_fma_f32 v[130:131], v[130:131], v[130:131], v[132:133]
	v_mov_b32_e32 v132, v112
	v_mov_b32_e32 v133, v126
	v_pk_mul_f32 v[140:141], v[140:141], v[140:141]
	s_nop 0
	v_pk_fma_f32 v[132:133], v[132:133], v[132:133], v[140:141]
	s_nop 0
	v_pk_add_f32 v[130:131], v[130:131], v[132:133]
	s_nop 0
	v_add_f32_e32 v129, v130, v131

; __device__ __forceinline__ u32x4 pack8(f32x4 a, f32x4 b) { u32x4 w; w.x = pk2(a[0], a[1]); w.y = pk2(a[2], a[3]); w.z = pk2(b[0], b[1]); w.w = pk2(b[2], b[3]); return w; }
; __device__ __forceinline__ float sq8(const f32x4& a, const f32x4& b) { return ((a[0] * a[0] + a[1] * a[1]) + (a[2] * a[2] + a[3] * a[3])) + ((b[0] * b[0] + b[1] * b[1]) + (b[2] * b[2] + b[3] * b[3])); }
;     __device__ __forceinline__ void operator()(const f32x4 (&acc)[2][2][4][2], const Unit& u, int ui, int wr, int wc, int fr, int fq, LAS unsigned char* lds) const {
;     ...
;                 for (int bj = 0; bj < 2; ++bj) {
;                     const int c = bj * 128 + wc * 32 + fq * 8;
;                     f32x4 v0 = acc[ai][bj][m][0] * rs, v1 = acc[ai][bj][m][1] * rs;
;                     if (pn < 6) { if (pn < 2) { v0 = v0 * QS_SB; v1 = v1 * QS_SB; } *(u32x4*)(QKV + (size_t)row * 1536 + pn * 256 + c) = pack8(v0, v1); }
;                     else if (pn == 6) { *(u32x4*)(CKV + (size_t)row * 256 + c) = pack8(v0, v1); sq += sq8(v0, v1); }
.LBB0_389:
	s_andn2_b64 vcc, exec, s[20:21]
	s_cbranch_vccnz .LBB0_391
	v_lshl_add_u64 v[130:131], s[38:39], 0, v[118:119]
	v_lshl_add_u64 v[130:131], v[130:131], 0, v[0:1]
	global_store_dwordx4 v[130:131], v[106:109], off nt
	v_mov_b32_e32 v130, v113
	v_mov_b32_e32 v131, v127
	v_mov_b32_e32 v108, v111
	v_mov_b32_e32 v109, v125
	v_mov_b32_e32 v106, v110
	v_mov_b32_e32 v107, v124
	v_pk_mul_f32 v[108:109], v[108:109], v[108:109]
	v_pk_mul_f32 v[130:131], v[130:131], v[130:131]
	v_pk_fma_f32 v[106:107], v[106:107], v[106:107], v[108:109]
	v_mov_b32_e32 v108, v112
	v_mov_b32_e32 v109, v126
	v_pk_fma_f32 v[108:109], v[108:109], v[108:109], v[130:131]
	s_nop 0
	v_pk_add_f32 v[106:107], v[106:107], v[108:109]
	s_nop 0
	v_add_f32_e32 v129, v106, v107

; __device__ __forceinline__ u32x4 pack8(f32x4 a, f32x4 b) { u32x4 w; w.x = pk2(a[0], a[1]); w.y = pk2(a[2], a[3]); w.z = pk2(b[0], b[1]); w.w = pk2(b[2], b[3]); return w; }
;     __device__ __forceinline__ void operator()(const f32x4 (&acc)[2][2][4][2], const Unit& u, int ui, int wr, int wc, int fr, int fq, LAS unsigned char* lds) const {
;     ...
;                 for (int bj = 0; bj < 2; ++bj) {
;                     const int c = bj * 128 + wc * 32 + fq * 8;
;                     f32x4 v0 = acc[ai][bj][m][0] * rs, v1 = acc[ai][bj][m][1] * rs;
;                     if (pn < 6) { if (pn < 2) { v0 = v0 * QS_SB; v1 = v1 * QS_SB; } *(u32x4*)(QKV + (size_t)row * 1536 + pn * 256 + c) = pack8(v0, v1); }
.LBB0_392:
	s_movk_i32 s6, 0xc00
	v_mad_i64_i32 v[106:107], s[6:7], v116, s6, 0
	v_lshl_add_u64 v[106:107], s[36:37], 0, v[106:107]
	s_and_b64 vcc, exec, s[20:21]
	v_lshl_add_u64 v[106:107], s[62:63], 1, v[106:107]
	s_cbranch_vccz .LBB0_394
	v_pk_mul_f32 v[108:109], v[112:113], s[96:97] op_sel_hi:[1,0]
	v_pk_mul_f32 v[130:131], v[110:111], s[96:97] op_sel_hi:[1,0]
	v_pk_mul_f32 v[132:133], v[126:127], s[96:97] op_sel_hi:[1,0]
	v_pk_mul_f32 v[140:141], v[124:125], s[96:97] op_sel_hi:[1,0]
	v_cndmask_b32_e64 v123, v127, v133, s[12:13]
	v_cndmask_b32_e64 v126, v126, v132, s[12:13]
	v_cndmask_b32_e64 v125, v125, v141, s[12:13]
	v_cndmask_b32_e64 v124, v124, v140, s[12:13]
	v_cndmask_b32_e64 v109, v113, v109, s[12:13]
	v_cndmask_b32_e64 v112, v112, v108, s[12:13]
	v_cndmask_b32_e64 v108, v111, v131, s[12:13]
	v_cndmask_b32_e64 v110, v110, v130, s[12:13]
	v_cvt_pk_bf16_f32 v108, v110, v108
	v_cvt_pk_bf16_f32 v109, v112, v109
	v_cvt_pk_bf16_f32 v110, v124, v125
	v_cvt_pk_bf16_f32 v111, v126, v123
	v_lshl_add_u64 v[112:113], v[106:107], 0, v[0:1]
	v_mov_b32_e32 v129, 0
	global_store_dwordx4 v[112:113], v[108:111], off nt

; __device__ __forceinline__ float xor32(float x) { auto rr = __builtin_amdgcn_permlane32_swap(__float_as_uint(x), __float_as_uint(x), false, false); return __uint_as_float(((unsigned)(threadIdx.x & 32)) ? rr[0] : rr[1]); }
; __device__ __forceinline__ u32x4 pack8(f32x4 a, f32x4 b) { u32x4 w; w.x = pk2(a[0], a[1]); w.y = pk2(a[2], a[3]); w.z = pk2(b[0], b[1]); w.w = pk2(b[2], b[3]); return w; }
;     __device__ __forceinline__ void operator()(const f32x4 (&acc)[2][2][4][2], const Unit& u, int ui, int wr, int wc, int fr, int fq, LAS unsigned char* lds) const {
;     ...
;                     else if (wc == 0) {
;                         const int ib = 8 * (fq & 1);
;                         const f32x4 c0 = *(const f32x4*)(COS + (size_t)row * 16 + ib), c1 = *(const f32x4*)(COS + (size_t)row * 16 + ib + 4);
;                         const f32x4 s0 = *(const f32x4*)(SIN + (size_t)row * 16 + ib), s1 = *(const f32x4*)(SIN + (size_t)row * 16 + ib + 4);
;                         f32x4 p0, p1;
; #pragma unroll
;                         for (int i = 0; i < 4; ++i) { p0[i] = xor32(v0[i]); p1[i] = xor32(v1[i]); }
;                         const float sg = (fq < 2) ? -1.f : 1.f;
;                         const f32x4 o0 = v0 * c0 + p0 * s0 * sg, o1 = v1 * c1 + p1 * s1 * sg;
;                         *(u32x4*)(KR + (size_t)row * 32 + fq * 8) = pack8(o0, o1);
.LBB0_397:
	s_cmp_lt_i32 s26, 7
	s_cbranch_scc1 .LBB0_405
	s_cmp_lg_u32 s26, 7
	s_cbranch_scc0 .LBB0_402
	s_andn2_b64 vcc, exec, s[56:57]
	s_cbranch_vccnz .LBB0_401
	v_lshlrev_b64 v[130:131], 2, v[108:109]
	v_lshl_add_u64 v[110:111], s[44:45], 0, v[130:131]
	v_lshlrev_b32_e32 v132, 2, v128
	v_mov_b32_e32 v133, v1
	v_lshl_add_u64 v[130:131], s[46:47], 0, v[130:131]
	v_lshl_add_u64 v[122:123], v[110:111], 0, v[132:133]
	v_lshl_add_u64 v[140:141], v[130:131], 0, v[132:133]
	s_waitcnt vmcnt(8)
	v_mov_b32_e32 v110, v174
	v_mov_b32_e32 v111, v175
	v_mov_b32_e32 v112, v176
	v_mov_b32_e32 v113, v177
	v_mov_b32_e32 v122, v178
	v_mov_b32_e32 v123, v179
	v_mov_b32_e32 v124, v180
	v_mov_b32_e32 v125, v181
	v_mov_b32_e32 v130, v182
	v_mov_b32_e32 v131, v183
	v_mov_b32_e32 v132, v184
	v_mov_b32_e32 v133, v185
	v_mov_b32_e32 v140, v230
	v_mov_b32_e32 v141, v231
	v_mov_b32_e32 v142, v232
	v_mov_b32_e32 v143, v233
	global_load_dwordx4 v[174:177], v[202:203], off offset:3072
	global_load_dwordx4 v[178:181], v[202:203], off offset:3088
	global_load_dwordx4 v[182:185], v[204:205], off offset:3072
	global_load_dwordx4 v[230:233], v[204:205], off offset:3088
	v_mov_b32_e32 v139, v102
	v_mov_b32_e32 v144, v102
	s_nop 1
	v_permlane32_swap_b32_e32 v139, v144
	v_cndmask_b32_e64 v144, v139, v144, s[4:5]
	v_mov_b32_e32 v139, v98
	v_mov_b32_e32 v145, v98
	s_nop 1
	v_permlane32_swap_b32_e32 v139, v145
	v_cndmask_b32_e64 v152, v139, v145, s[4:5]
	v_mov_b32_e32 v139, v103
	v_mov_b32_e32 v145, v103
	s_nop 1
	v_permlane32_swap_b32_e32 v139, v145
	v_cndmask_b32_e64 v145, v139, v145, s[4:5]
	v_mov_b32_e32 v139, v99
	v_mov_b32_e32 v153, v99
	s_nop 1
	v_permlane32_swap_b32_e32 v139, v153
	v_cndmask_b32_e64 v153, v139, v153, s[4:5]
	v_mov_b32_e32 v139, v104
	v_mov_b32_e32 v154, v104
	s_nop 1
	v_permlane32_swap_b32_e32 v139, v154
	v_cndmask_b32_e64 v154, v139, v154, s[4:5]
	v_mov_b32_e32 v139, v100
	v_mov_b32_e32 v155, v100
	s_nop 1
	v_permlane32_swap_b32_e32 v139, v155
	v_cndmask_b32_e64 v156, v139, v155, s[4:5]
	v_mov_b32_e32 v139, v105
	v_mov_b32_e32 v155, v105
	s_nop 1
	v_permlane32_swap_b32_e32 v139, v155
	v_cndmask_b32_e64 v155, v139, v155, s[4:5]
	v_mov_b32_e32 v139, v101
	v_mov_b32_e32 v157, v101
	s_nop 1
	v_permlane32_swap_b32_e32 v139, v157
	v_cndmask_b32_e64 v157, v139, v157, s[4:5]
	v_lshlrev_b64 v[126:127], 6, v[116:117]
	s_waitcnt lgkmcnt(0)
	v_pk_mul_f32 v[132:133], v[132:133], v[154:155]
	v_pk_mul_f32 v[130:131], v[130:131], v[144:145]
	v_mov_b32_e32 v144, v114
	v_mov_b32_e32 v145, v114
	v_pk_mul_f32 v[130:131], v[114:115], v[130:131]
	v_pk_mul_f32 v[132:133], v[144:145], v[132:133]
	v_pk_fma_f32 v[110:111], v[102:103], v[110:111], v[130:131]
	v_pk_fma_f32 v[112:113], v[104:105], v[112:113], v[132:133]
	v_pk_mul_f32 v[130:131], v[142:143], v[156:157]
	v_pk_mul_f32 v[132:133], v[140:141], v[152:153]
	v_pk_mul_f32 v[130:131], v[144:145], v[130:131]
	v_pk_mul_f32 v[132:133], v[114:115], v[132:133]
	v_pk_fma_f32 v[124:125], v[100:101], v[124:125], v[130:131]
	v_pk_fma_f32 v[122:123], v[98:99], v[122:123], v[132:133]
	v_cvt_pk_bf16_f32 v110, v110, v111
	v_cvt_pk_bf16_f32 v111, v112, v113
	v_cvt_pk_bf16_f32 v112, v122, v123
	v_cvt_pk_bf16_f32 v113, v124, v125
	v_lshl_add_u64 v[122:123], s[42:43], 0, v[126:127]
	v_lshlrev_b32_e32 v124, 1, v149
	v_mov_b32_e32 v125, v1
	v_lshl_add_u64 v[122:123], v[122:123], 0, v[124:125]
	global_store_dwordx4 v[122:123], v[110:113], off nt

; __device__ __forceinline__ u32x4 pack8(f32x4 a, f32x4 b) { u32x4 w; w.x = pk2(a[0], a[1]); w.y = pk2(a[2], a[3]); w.z = pk2(b[0], b[1]); w.w = pk2(b[2], b[3]); return w; }
; __device__ __forceinline__ float sq8(const f32x4& a, const f32x4& b) { return ((a[0] * a[0] + a[1] * a[1]) + (a[2] * a[2] + a[3] * a[3])) + ((b[0] * b[0] + b[1] * b[1]) + (b[2] * b[2] + b[3] * b[3])); }
;     __device__ __forceinline__ void operator()(const f32x4 (&acc)[2][2][4][2], const Unit& u, int ui, int wr, int wc, int fr, int fq, LAS unsigned char* lds) const {
;     ...
;                 for (int bj = 0; bj < 2; ++bj) {
;                     const int c = bj * 128 + wc * 32 + fq * 8;
;                     f32x4 v0 = acc[ai][bj][m][0] * rs, v1 = acc[ai][bj][m][1] * rs;
;                     if (pn < 6) { if (pn < 2) { v0 = v0 * QS_SB; v1 = v1 * QS_SB; } *(u32x4*)(QKV + (size_t)row * 1536 + pn * 256 + c) = pack8(v0, v1); }
;                     else if (pn == 6) { *(u32x4*)(CKV + (size_t)row * 256 + c) = pack8(v0, v1); sq += sq8(v0, v1); }
;                     else if (pn == 7) { *(u32x4*)(CQ + (size_t)row * 384 + c) = pack8(v0, v1); sq += sq8(v0, v1); }
.LBB0_402:
	s_andn2_b64 vcc, exec, s[20:21]
	v_mov_b32_e32 v110, v129
	s_cbranch_vccnz .LBB0_404
	v_lshl_add_u64 v[120:121], s[40:41], 0, v[120:121]
	v_cvt_pk_bf16_f32 v110, v102, v103
	v_cvt_pk_bf16_f32 v111, v104, v105
	v_cvt_pk_bf16_f32 v112, v98, v99
	v_cvt_pk_bf16_f32 v113, v100, v101
	v_lshl_add_u64 v[120:121], v[120:121], 0, v[0:1]
	global_store_dwordx4 v[120:121], v[110:113], off offset:256 nt
	v_mov_b32_e32 v120, v105
	v_mov_b32_e32 v121, v101
	v_mov_b32_e32 v112, v103
	v_mov_b32_e32 v113, v99
	v_mov_b32_e32 v110, v102
	v_mov_b32_e32 v111, v98
	v_pk_mul_f32 v[112:113], v[112:113], v[112:113]
	v_pk_mul_f32 v[120:121], v[120:121], v[120:121]
	v_pk_fma_f32 v[110:111], v[110:111], v[110:111], v[112:113]
	v_mov_b32_e32 v112, v104
	v_mov_b32_e32 v113, v100
	v_pk_fma_f32 v[112:113], v[112:113], v[112:113], v[120:121]
	s_nop 0
	v_pk_add_f32 v[110:111], v[110:111], v[112:113]
	s_nop 0
	v_add_f32_e32 v110, v110, v111
	v_add_f32_e32 v110, v110, v129

; __device__ __forceinline__ u32x4 pack8(f32x4 a, f32x4 b) { u32x4 w; w.x = pk2(a[0], a[1]); w.y = pk2(a[2], a[3]); w.z = pk2(b[0], b[1]); w.w = pk2(b[2], b[3]); return w; }
; __device__ __forceinline__ float sq8(const f32x4& a, const f32x4& b) { return ((a[0] * a[0] + a[1] * a[1]) + (a[2] * a[2] + a[3] * a[3])) + ((b[0] * b[0] + b[1] * b[1]) + (b[2] * b[2] + b[3] * b[3])); }
;     __device__ __forceinline__ void operator()(const f32x4 (&acc)[2][2][4][2], const Unit& u, int ui, int wr, int wc, int fr, int fq, LAS unsigned char* lds) const {
;     ...
;                 for (int bj = 0; bj < 2; ++bj) {
;                     const int c = bj * 128 + wc * 32 + fq * 8;
;                     f32x4 v0 = acc[ai][bj][m][0] * rs, v1 = acc[ai][bj][m][1] * rs;
;                     if (pn < 6) { if (pn < 2) { v0 = v0 * QS_SB; v1 = v1 * QS_SB; } *(u32x4*)(QKV + (size_t)row * 1536 + pn * 256 + c) = pack8(v0, v1); }
;                     else if (pn == 6) { *(u32x4*)(CKV + (size_t)row * 256 + c) = pack8(v0, v1); sq += sq8(v0, v1); }
.LBB0_405:
	s_andn2_b64 vcc, exec, s[20:21]
	s_cbranch_vccnz .LBB0_407
	v_lshl_add_u64 v[118:119], s[38:39], 0, v[118:119]
	v_cvt_pk_bf16_f32 v110, v102, v103
	v_cvt_pk_bf16_f32 v111, v104, v105
	v_cvt_pk_bf16_f32 v112, v98, v99
	v_cvt_pk_bf16_f32 v113, v100, v101
	v_lshl_add_u64 v[118:119], v[118:119], 0, v[0:1]
	global_store_dwordx4 v[118:119], v[110:113], off offset:256 nt
	v_mov_b32_e32 v118, v105
	v_mov_b32_e32 v119, v101
	v_mov_b32_e32 v112, v103
	v_mov_b32_e32 v113, v99
	v_mov_b32_e32 v110, v102
	v_mov_b32_e32 v111, v98
	v_pk_mul_f32 v[112:113], v[112:113], v[112:113]
	v_pk_mul_f32 v[118:119], v[118:119], v[118:119]
	v_pk_fma_f32 v[110:111], v[110:111], v[110:111], v[112:113]
	v_mov_b32_e32 v112, v104
	v_mov_b32_e32 v113, v100
	v_pk_fma_f32 v[112:113], v[112:113], v[112:113], v[118:119]
	s_nop 0
	v_pk_add_f32 v[110:111], v[110:111], v[112:113]
	s_nop 0
	v_add_f32_e32 v110, v110, v111
	v_add_f32_e32 v110, v110, v129

; __device__ __forceinline__ u32x4 pack8(f32x4 a, f32x4 b) { u32x4 w; w.x = pk2(a[0], a[1]); w.y = pk2(a[2], a[3]); w.z = pk2(b[0], b[1]); w.w = pk2(b[2], b[3]); return w; }
;     __device__ __forceinline__ void operator()(const f32x4 (&acc)[2][2][4][2], const Unit& u, int ui, int wr, int wc, int fr, int fq, LAS unsigned char* lds) const {
;     ...
;                 for (int bj = 0; bj < 2; ++bj) {
;                     const int c = bj * 128 + wc * 32 + fq * 8;
;                     f32x4 v0 = acc[ai][bj][m][0] * rs, v1 = acc[ai][bj][m][1] * rs;
;                     if (pn < 6) { if (pn < 2) { v0 = v0 * QS_SB; v1 = v1 * QS_SB; } *(u32x4*)(QKV + (size_t)row * 1536 + pn * 256 + c) = pack8(v0, v1); }
.LBB0_408:
	v_pk_mul_f32 v[110:111], v[104:105], s[96:97] op_sel_hi:[1,0]
	v_pk_mul_f32 v[112:113], v[102:103], s[96:97] op_sel_hi:[1,0]
	v_pk_mul_f32 v[118:119], v[100:101], s[96:97] op_sel_hi:[1,0]
	v_pk_mul_f32 v[120:121], v[98:99], s[96:97] op_sel_hi:[1,0]
	v_cndmask_b32_e64 v101, v101, v119, s[12:13]
	v_cndmask_b32_e64 v118, v100, v118, s[12:13]
	v_cndmask_b32_e64 v100, v99, v121, s[12:13]
	v_cndmask_b32_e64 v119, v98, v120, s[12:13]
	v_cndmask_b32_e64 v99, v105, v111, s[12:13]
	v_cndmask_b32_e64 v104, v104, v110, s[12:13]
	v_cndmask_b32_e64 v98, v103, v113, s[12:13]
	v_cndmask_b32_e64 v102, v102, v112, s[12:13]
	v_cvt_pk_bf16_f32 v98, v102, v98
	v_cvt_pk_bf16_f32 v99, v104, v99
	v_cvt_pk_bf16_f32 v100, v119, v100
	v_cvt_pk_bf16_f32 v101, v118, v101
	v_lshl_add_u64 v[102:103], v[106:107], 0, v[0:1]
	v_mov_b32_e32 v110, v129
	global_store_dwordx4 v[102:103], v[98:101], off offset:256 nt
	s_nop 1
	v_cndmask_b32_e64 v98, 0, 1, s[64:65]
	v_cmp_ne_u32_e64 s[20:21], 1, v98
	s_andn2_b64 vcc, exec, s[64:65]
	s_cbranch_vccnz .LBB0_412

; __device__ __forceinline__ u32x4 pack8(f32x4 a, f32x4 b) { u32x4 w; w.x = pk2(a[0], a[1]); w.y = pk2(a[2], a[3]); w.z = pk2(b[0], b[1]); w.w = pk2(b[2], b[3]); return w; }
; __device__ __forceinline__ float sq8(const f32x4& a, const f32x4& b) { return ((a[0] * a[0] + a[1] * a[1]) + (a[2] * a[2] + a[3] * a[3])) + ((b[0] * b[0] + b[1] * b[1]) + (b[2] * b[2] + b[3] * b[3])); }
; __device__ __forceinline__ f32x2 rtab_get(LAS unsigned char* lds, int ui, int r) { return ((const LAS f32x2*)(lds + RTAB_OFF))[(ui & 1) * 256 + r]; }
;     __device__ __forceinline__ void operator()(const f32x4 (&acc)[2][2][4][2], const Unit& u, int ui, int wr, int wc, int fr, int fq, LAS unsigned char* lds) const {
;     ...
;                 const int rr = ai * 128 + wr * 64 + m * 16 + fr, row = u.pm * 256 + rr; const float rs = rtab_get(lds, ui, rr)[0];
;                 float sq = 0.f;
; #pragma unroll
;                 for (int bj = 0; bj < 2; ++bj) {
;                     const int c = bj * 128 + wc * 32 + fq * 8;
;                     f32x4 v0 = acc[ai][bj][m][0] * rs, v1 = acc[ai][bj][m][1] * rs;
;                     if (pn < 6) { if (pn < 2) { v0 = v0 * QS_SB; v1 = v1 * QS_SB; } *(u32x4*)(QKV + (size_t)row * 1536 + pn * 256 + c) = pack8(v0, v1); }
;                     else if (pn == 6) { *(u32x4*)(CKV + (size_t)row * 256 + c) = pack8(v0, v1); sq += sq8(v0, v1); }
;                     else if (pn == 7) { *(u32x4*)(CQ + (size_t)row * 384 + c) = pack8(v0, v1); sq += sq8(v0, v1); }
;                     else if (bj == 0) { *(u32x4*)(CQ + (size_t)row * 384 + 256 + c) = pack8(v0, v1); sq += sq8(v0, v1); }
.LBB0_412:
	ds_read_b32 v104, v150 offset:256
	v_add3_u32 v98, s3, v151, 32
	v_ashrrev_i32_e32 v99, 31, v98
	v_mad_i64_i32 v[102:103], s[6:7], v98, s59, 0
	v_lshlrev_b64 v[100:101], 9, v[98:99]
	s_waitcnt lgkmcnt(0)
	v_pk_mul_f32 v[96:97], v[96:97], v[104:105] op_sel_hi:[1,0]
	v_pk_mul_f32 v[94:95], v[94:95], v[104:105] op_sel_hi:[1,0]
	v_pk_mul_f32 v[108:109], v[92:93], v[104:105] op_sel_hi:[1,0]
	v_pk_mul_f32 v[106:107], v[90:91], v[104:105] op_sel_hi:[1,0]
	s_and_b64 vcc, exec, s[18:19]
	s_mov_b64 s[64:65], -1
	s_cbranch_vccnz .LBB0_422
	v_cvt_pk_bf16_f32 v90, v94, v95
	v_cvt_pk_bf16_f32 v91, v96, v97
	v_cvt_pk_bf16_f32 v92, v106, v107
	v_cvt_pk_bf16_f32 v93, v108, v109
	s_cmp_lt_i32 s26, 7
	s_cbranch_scc1 .LBB0_419
	s_cmp_lg_u32 s26, 7
	s_cbranch_scc0 .LBB0_416
	v_lshl_add_u64 v[110:111], s[40:41], 0, v[102:103]
	v_lshl_add_u64 v[110:111], v[110:111], 0, v[0:1]
	v_mov_b32_e32 v112, v95
	v_mov_b32_e32 v113, v107
	global_store_dwordx4 v[110:111], v[90:93], off offset:512 nt
	v_mov_b32_e32 v110, v94
	v_mov_b32_e32 v111, v106
	v_pk_mul_f32 v[112:113], v[112:113], v[112:113]
	v_mov_b32_e32 v116, v97
	v_mov_b32_e32 v117, v109
	v_pk_fma_f32 v[110:111], v[110:111], v[110:111], v[112:113]
	v_mov_b32_e32 v112, v96
	v_mov_b32_e32 v113, v108
	v_pk_mul_f32 v[116:117], v[116:117], v[116:117]
	s_mov_b64 s[64:65], 0
	v_pk_fma_f32 v[112:113], v[112:113], v[112:113], v[116:117]
	s_nop 0
	v_pk_add_f32 v[110:111], v[110:111], v[112:113]
	s_nop 0
	v_add_f32_e32 v110, v110, v111
.LBB0_416:
	s_andn2_b64 vcc, exec, s[64:65]
	s_cbranch_vccnz .LBB0_418
	v_lshl_add_u64 v[110:111], s[40:41], 0, v[102:103]
	v_lshl_add_u64 v[110:111], v[110:111], 0, v[0:1]
	v_mov_b32_e32 v112, v95
	v_mov_b32_e32 v113, v107
	global_store_dwordx4 v[110:111], v[90:93], off nt
	v_mov_b32_e32 v110, v94
	v_mov_b32_e32 v111, v106
	v_pk_mul_f32 v[112:113], v[112:113], v[112:113]
	v_mov_b32_e32 v116, v97
	v_mov_b32_e32 v117, v109
	v_pk_fma_f32 v[110:111], v[110:111], v[110:111], v[112:113]
	v_mov_b32_e32 v112, v96
	v_mov_b32_e32 v113, v108
	v_pk_mul_f32 v[116:117], v[116:117], v[116:117]
	s_nop 0
	v_pk_fma_f32 v[112:113], v[112:113], v[112:113], v[116:117]
	s_nop 0
	v_pk_add_f32 v[110:111], v[110:111], v[112:113]
	s_nop 0
	v_add_f32_e32 v110, v110, v111

; __device__ __forceinline__ u32x4 pack8(f32x4 a, f32x4 b) { u32x4 w; w.x = pk2(a[0], a[1]); w.y = pk2(a[2], a[3]); w.z = pk2(b[0], b[1]); w.w = pk2(b[2], b[3]); return w; }
; __device__ __forceinline__ float sq8(const f32x4& a, const f32x4& b) { return ((a[0] * a[0] + a[1] * a[1]) + (a[2] * a[2] + a[3] * a[3])) + ((b[0] * b[0] + b[1] * b[1]) + (b[2] * b[2] + b[3] * b[3])); }
;     __device__ __forceinline__ void operator()(const f32x4 (&acc)[2][2][4][2], const Unit& u, int ui, int wr, int wc, int fr, int fq, LAS unsigned char* lds) const {
;     ...
;                 for (int bj = 0; bj < 2; ++bj) {
;                     const int c = bj * 128 + wc * 32 + fq * 8;
;                     f32x4 v0 = acc[ai][bj][m][0] * rs, v1 = acc[ai][bj][m][1] * rs;
;                     if (pn < 6) { if (pn < 2) { v0 = v0 * QS_SB; v1 = v1 * QS_SB; } *(u32x4*)(QKV + (size_t)row * 1536 + pn * 256 + c) = pack8(v0, v1); }
;                     else if (pn == 6) { *(u32x4*)(CKV + (size_t)row * 256 + c) = pack8(v0, v1); sq += sq8(v0, v1); }
.LBB0_419:
	s_andn2_b64 vcc, exec, s[64:65]
	s_cbranch_vccnz .LBB0_421
	v_lshl_add_u64 v[110:111], s[38:39], 0, v[100:101]
	v_lshl_add_u64 v[110:111], v[110:111], 0, v[0:1]
	global_store_dwordx4 v[110:111], v[90:93], off nt
	v_mov_b32_e32 v110, v97
	v_mov_b32_e32 v111, v109
	v_mov_b32_e32 v92, v95
	v_mov_b32_e32 v93, v107
	v_mov_b32_e32 v90, v94
	v_mov_b32_e32 v91, v106
	v_pk_mul_f32 v[92:93], v[92:93], v[92:93]
	v_pk_mul_f32 v[110:111], v[110:111], v[110:111]
	v_pk_fma_f32 v[90:91], v[90:91], v[90:91], v[92:93]
	v_mov_b32_e32 v92, v96
	v_mov_b32_e32 v93, v108
	v_pk_fma_f32 v[92:93], v[92:93], v[92:93], v[110:111]
	s_nop 0
	v_pk_add_f32 v[90:91], v[90:91], v[92:93]
	s_nop 0
	v_add_f32_e32 v110, v90, v91

; __device__ __forceinline__ u32x4 pack8(f32x4 a, f32x4 b) { u32x4 w; w.x = pk2(a[0], a[1]); w.y = pk2(a[2], a[3]); w.z = pk2(b[0], b[1]); w.w = pk2(b[2], b[3]); return w; }
;     __device__ __forceinline__ void operator()(const f32x4 (&acc)[2][2][4][2], const Unit& u, int ui, int wr, int wc, int fr, int fq, LAS unsigned char* lds) const {
;     ...
;                 for (int bj = 0; bj < 2; ++bj) {
;                     const int c = bj * 128 + wc * 32 + fq * 8;
;                     f32x4 v0 = acc[ai][bj][m][0] * rs, v1 = acc[ai][bj][m][1] * rs;
;                     if (pn < 6) { if (pn < 2) { v0 = v0 * QS_SB; v1 = v1 * QS_SB; } *(u32x4*)(QKV + (size_t)row * 1536 + pn * 256 + c) = pack8(v0, v1); }
.LBB0_422:
	s_movk_i32 s6, 0xc00
	v_mad_i64_i32 v[90:91], s[6:7], v98, s6, 0
	v_lshl_add_u64 v[90:91], s[36:37], 0, v[90:91]
	s_and_b64 vcc, exec, s[64:65]
	v_lshl_add_u64 v[90:91], s[62:63], 1, v[90:91]
	s_cbranch_vccz .LBB0_424
	v_pk_mul_f32 v[92:93], v[96:97], s[96:97] op_sel_hi:[1,0]
	v_pk_mul_f32 v[110:111], v[94:95], s[96:97] op_sel_hi:[1,0]
	v_pk_mul_f32 v[112:113], v[108:109], s[96:97] op_sel_hi:[1,0]
	v_pk_mul_f32 v[116:117], v[106:107], s[96:97] op_sel_hi:[1,0]
	v_cndmask_b32_e64 v105, v109, v113, s[12:13]
	v_cndmask_b32_e64 v108, v108, v112, s[12:13]
	v_cndmask_b32_e64 v107, v107, v117, s[12:13]
	v_cndmask_b32_e64 v106, v106, v116, s[12:13]
	v_cndmask_b32_e64 v93, v97, v93, s[12:13]
	v_cndmask_b32_e64 v96, v96, v92, s[12:13]
	v_cndmask_b32_e64 v92, v95, v111, s[12:13]
	v_cndmask_b32_e64 v94, v94, v110, s[12:13]
	v_cvt_pk_bf16_f32 v92, v94, v92
	v_cvt_pk_bf16_f32 v93, v96, v93
	v_cvt_pk_bf16_f32 v94, v106, v107
	v_cvt_pk_bf16_f32 v95, v108, v105
	v_lshl_add_u64 v[96:97], v[90:91], 0, v[0:1]
	v_mov_b32_e32 v110, 0
	global_store_dwordx4 v[96:97], v[92:95], off nt

; __device__ __forceinline__ float xor32(float x) { auto rr = __builtin_amdgcn_permlane32_swap(__float_as_uint(x), __float_as_uint(x), false, false); return __uint_as_float(((unsigned)(threadIdx.x & 32)) ? rr[0] : rr[1]); }
; __device__ __forceinline__ u32x4 pack8(f32x4 a, f32x4 b) { u32x4 w; w.x = pk2(a[0], a[1]); w.y = pk2(a[2], a[3]); w.z = pk2(b[0], b[1]); w.w = pk2(b[2], b[3]); return w; }
;     __device__ __forceinline__ void operator()(const f32x4 (&acc)[2][2][4][2], const Unit& u, int ui, int wr, int wc, int fr, int fq, LAS unsigned char* lds) const {
;     ...
;                     else if (wc == 0) {
;                         const int ib = 8 * (fq & 1);
;                         const f32x4 c0 = *(const f32x4*)(COS + (size_t)row * 16 + ib), c1 = *(const f32x4*)(COS + (size_t)row * 16 + ib + 4);
;                         const f32x4 s0 = *(const f32x4*)(SIN + (size_t)row * 16 + ib), s1 = *(const f32x4*)(SIN + (size_t)row * 16 + ib + 4);
;                         f32x4 p0, p1;
; #pragma unroll
;                         for (int i = 0; i < 4; ++i) { p0[i] = xor32(v0[i]); p1[i] = xor32(v1[i]); }
;                         const float sg = (fq < 2) ? -1.f : 1.f;
;                         const f32x4 o0 = v0 * c0 + p0 * s0 * sg, o1 = v1 * c1 + p1 * s1 * sg;
;                         *(u32x4*)(KR + (size_t)row * 32 + fq * 8) = pack8(o0, o1);
.LBB0_427:
	s_cmp_lt_i32 s26, 7
	s_cbranch_scc1 .LBB0_435
	s_cmp_lg_u32 s26, 7
	s_cbranch_scc0 .LBB0_432
	s_andn2_b64 vcc, exec, s[56:57]
	s_cbranch_vccnz .LBB0_431
	v_lshlrev_b64 v[112:113], 2, v[92:93]
	v_lshl_add_u64 v[94:95], s[44:45], 0, v[112:113]
	v_lshlrev_b32_e32 v116, 2, v128
	v_mov_b32_e32 v117, v1
	v_lshl_add_u64 v[112:113], s[46:47], 0, v[112:113]
	v_lshl_add_u64 v[104:105], v[94:95], 0, v[116:117]
	v_lshl_add_u64 v[112:113], v[112:113], 0, v[116:117]
	s_waitcnt vmcnt(10)
	v_mov_b32_e32 v94, v214
	v_mov_b32_e32 v95, v215
	v_mov_b32_e32 v96, v216
	v_mov_b32_e32 v97, v217
	v_mov_b32_e32 v104, v218
	v_mov_b32_e32 v105, v219
	v_mov_b32_e32 v106, v220
	v_mov_b32_e32 v107, v221
	v_mov_b32_e32 v116, v222
	v_mov_b32_e32 v117, v223
	v_mov_b32_e32 v118, v224
	v_mov_b32_e32 v119, v225
	v_mov_b32_e32 v120, v226
	v_mov_b32_e32 v121, v227
	v_mov_b32_e32 v122, v228
	v_mov_b32_e32 v123, v229
	global_load_dwordx4 v[214:217], v[206:207], off
	global_load_dwordx4 v[218:221], v[206:207], off offset:16
	global_load_dwordx4 v[222:225], v[208:209], off
	global_load_dwordx4 v[226:229], v[208:209], off offset:16
	v_mov_b32_e32 v111, v86
	v_mov_b32_e32 v112, v86
	s_nop 1
	v_permlane32_swap_b32_e32 v111, v112
	v_cndmask_b32_e64 v112, v111, v112, s[4:5]
	v_mov_b32_e32 v111, v82
	v_mov_b32_e32 v113, v82
	s_nop 1
	v_permlane32_swap_b32_e32 v111, v113
	v_cndmask_b32_e64 v124, v111, v113, s[4:5]
	v_mov_b32_e32 v111, v87
	v_mov_b32_e32 v113, v87
	s_nop 1
	v_permlane32_swap_b32_e32 v111, v113
	v_cndmask_b32_e64 v113, v111, v113, s[4:5]
	v_mov_b32_e32 v111, v83
	v_mov_b32_e32 v125, v83
	s_nop 1
	v_permlane32_swap_b32_e32 v111, v125
	v_cndmask_b32_e64 v125, v111, v125, s[4:5]
	v_mov_b32_e32 v111, v88
	v_mov_b32_e32 v126, v88
	s_nop 1
	v_permlane32_swap_b32_e32 v111, v126
	v_cndmask_b32_e64 v126, v111, v126, s[4:5]
	v_mov_b32_e32 v111, v84
	v_mov_b32_e32 v127, v84
	s_nop 1
	v_permlane32_swap_b32_e32 v111, v127
	v_cndmask_b32_e64 v130, v111, v127, s[4:5]
	v_mov_b32_e32 v111, v89
	v_mov_b32_e32 v127, v89
	s_nop 1
	v_permlane32_swap_b32_e32 v111, v127
	v_cndmask_b32_e64 v127, v111, v127, s[4:5]
	v_mov_b32_e32 v111, v85
	v_mov_b32_e32 v129, v85
	s_nop 1
	v_permlane32_swap_b32_e32 v111, v129
	v_cndmask_b32_e64 v131, v111, v129, s[4:5]
	v_lshlrev_b64 v[108:109], 6, v[98:99]
	s_waitcnt lgkmcnt(0)
	v_pk_mul_f32 v[118:119], v[118:119], v[126:127]
	v_pk_mul_f32 v[112:113], v[116:117], v[112:113]
	v_mov_b32_e32 v116, v114
	v_mov_b32_e32 v117, v114
	v_pk_mul_f32 v[112:113], v[114:115], v[112:113]
	v_pk_mul_f32 v[118:119], v[116:117], v[118:119]
	v_pk_fma_f32 v[94:95], v[86:87], v[94:95], v[112:113]
	v_pk_fma_f32 v[96:97], v[88:89], v[96:97], v[118:119]
	v_pk_mul_f32 v[112:113], v[122:123], v[130:131]
	v_pk_mul_f32 v[118:119], v[120:121], v[124:125]
	v_pk_mul_f32 v[112:113], v[116:117], v[112:113]
	v_pk_mul_f32 v[118:119], v[114:115], v[118:119]
	v_pk_fma_f32 v[106:107], v[84:85], v[106:107], v[112:113]
	v_pk_fma_f32 v[104:105], v[82:83], v[104:105], v[118:119]
	v_cvt_pk_bf16_f32 v94, v94, v95
	v_cvt_pk_bf16_f32 v95, v96, v97
	v_cvt_pk_bf16_f32 v96, v104, v105
	v_cvt_pk_bf16_f32 v97, v106, v107
	v_lshl_add_u64 v[104:105], s[42:43], 0, v[108:109]
	v_lshlrev_b32_e32 v106, 1, v149
	v_mov_b32_e32 v107, v1
	v_lshl_add_u64 v[104:105], v[104:105], 0, v[106:107]
	global_store_dwordx4 v[104:105], v[94:97], off nt

; __device__ __forceinline__ u32x4 pack8(f32x4 a, f32x4 b) { u32x4 w; w.x = pk2(a[0], a[1]); w.y = pk2(a[2], a[3]); w.z = pk2(b[0], b[1]); w.w = pk2(b[2], b[3]); return w; }
; __device__ __forceinline__ float sq8(const f32x4& a, const f32x4& b) { return ((a[0] * a[0] + a[1] * a[1]) + (a[2] * a[2] + a[3] * a[3])) + ((b[0] * b[0] + b[1] * b[1]) + (b[2] * b[2] + b[3] * b[3])); }
;     __device__ __forceinline__ void operator()(const f32x4 (&acc)[2][2][4][2], const Unit& u, int ui, int wr, int wc, int fr, int fq, LAS unsigned char* lds) const {
;     ...
;                 for (int bj = 0; bj < 2; ++bj) {
;                     const int c = bj * 128 + wc * 32 + fq * 8;
;                     f32x4 v0 = acc[ai][bj][m][0] * rs, v1 = acc[ai][bj][m][1] * rs;
;                     if (pn < 6) { if (pn < 2) { v0 = v0 * QS_SB; v1 = v1 * QS_SB; } *(u32x4*)(QKV + (size_t)row * 1536 + pn * 256 + c) = pack8(v0, v1); }
;                     else if (pn == 6) { *(u32x4*)(CKV + (size_t)row * 256 + c) = pack8(v0, v1); sq += sq8(v0, v1); }
;                     else if (pn == 7) { *(u32x4*)(CQ + (size_t)row * 384 + c) = pack8(v0, v1); sq += sq8(v0, v1); }
.LBB0_432:
	s_andn2_b64 vcc, exec, s[64:65]
	v_mov_b32_e32 v94, v110
	s_cbranch_vccnz .LBB0_434
	v_lshl_add_u64 v[102:103], s[40:41], 0, v[102:103]
	v_cvt_pk_bf16_f32 v94, v86, v87
	v_cvt_pk_bf16_f32 v95, v88, v89
	v_cvt_pk_bf16_f32 v96, v82, v83
	v_cvt_pk_bf16_f32 v97, v84, v85
	v_lshl_add_u64 v[102:103], v[102:103], 0, v[0:1]
	global_store_dwordx4 v[102:103], v[94:97], off offset:256 nt
	v_mov_b32_e32 v102, v89
	v_mov_b32_e32 v103, v85
	v_mov_b32_e32 v96, v87
	v_mov_b32_e32 v97, v83
	v_mov_b32_e32 v94, v86
	v_mov_b32_e32 v95, v82
	v_pk_mul_f32 v[96:97], v[96:97], v[96:97]
	v_pk_mul_f32 v[102:103], v[102:103], v[102:103]
	v_pk_fma_f32 v[94:95], v[94:95], v[94:95], v[96:97]
	v_mov_b32_e32 v96, v88
	v_mov_b32_e32 v97, v84
	v_pk_fma_f32 v[96:97], v[96:97], v[96:97], v[102:103]
	s_nop 0
	v_pk_add_f32 v[94:95], v[94:95], v[96:97]
	s_nop 0
	v_add_f32_e32 v94, v94, v95
	v_add_f32_e32 v94, v94, v110

; __device__ __forceinline__ u32x4 pack8(f32x4 a, f32x4 b) { u32x4 w; w.x = pk2(a[0], a[1]); w.y = pk2(a[2], a[3]); w.z = pk2(b[0], b[1]); w.w = pk2(b[2], b[3]); return w; }
; __device__ __forceinline__ float sq8(const f32x4& a, const f32x4& b) { return ((a[0] * a[0] + a[1] * a[1]) + (a[2] * a[2] + a[3] * a[3])) + ((b[0] * b[0] + b[1] * b[1]) + (b[2] * b[2] + b[3] * b[3])); }
;     __device__ __forceinline__ void operator()(const f32x4 (&acc)[2][2][4][2], const Unit& u, int ui, int wr, int wc, int fr, int fq, LAS unsigned char* lds) const {
;     ...
;                 for (int bj = 0; bj < 2; ++bj) {
;                     const int c = bj * 128 + wc * 32 + fq * 8;
;                     f32x4 v0 = acc[ai][bj][m][0] * rs, v1 = acc[ai][bj][m][1] * rs;
;                     if (pn < 6) { if (pn < 2) { v0 = v0 * QS_SB; v1 = v1 * QS_SB; } *(u32x4*)(QKV + (size_t)row * 1536 + pn * 256 + c) = pack8(v0, v1); }
;                     else if (pn == 6) { *(u32x4*)(CKV + (size_t)row * 256 + c) = pack8(v0, v1); sq += sq8(v0, v1); }
.LBB0_435:
	s_andn2_b64 vcc, exec, s[64:65]
	s_cbranch_vccnz .LBB0_437
	v_lshl_add_u64 v[100:101], s[38:39], 0, v[100:101]
	v_cvt_pk_bf16_f32 v94, v86, v87
	v_cvt_pk_bf16_f32 v95, v88, v89
	v_cvt_pk_bf16_f32 v96, v82, v83
	v_cvt_pk_bf16_f32 v97, v84, v85
	v_lshl_add_u64 v[100:101], v[100:101], 0, v[0:1]
	global_store_dwordx4 v[100:101], v[94:97], off offset:256 nt
	v_mov_b32_e32 v100, v89
	v_mov_b32_e32 v101, v85
	v_mov_b32_e32 v96, v87
	v_mov_b32_e32 v97, v83
	v_mov_b32_e32 v94, v86
	v_mov_b32_e32 v95, v82
	v_pk_mul_f32 v[96:97], v[96:97], v[96:97]
	v_pk_mul_f32 v[100:101], v[100:101], v[100:101]
	v_pk_fma_f32 v[94:95], v[94:95], v[94:95], v[96:97]
	v_mov_b32_e32 v96, v88
	v_mov_b32_e32 v97, v84
	v_pk_fma_f32 v[96:97], v[96:97], v[96:97], v[100:101]
	s_nop 0
	v_pk_add_f32 v[94:95], v[94:95], v[96:97]
	s_nop 0
	v_add_f32_e32 v94, v94, v95
	v_add_f32_e32 v94, v94, v110

; __device__ __forceinline__ u32x4 pack8(f32x4 a, f32x4 b) { u32x4 w; w.x = pk2(a[0], a[1]); w.y = pk2(a[2], a[3]); w.z = pk2(b[0], b[1]); w.w = pk2(b[2], b[3]); return w; }
;     __device__ __forceinline__ void operator()(const f32x4 (&acc)[2][2][4][2], const Unit& u, int ui, int wr, int wc, int fr, int fq, LAS unsigned char* lds) const {
;     ...
;                 for (int bj = 0; bj < 2; ++bj) {
;                     const int c = bj * 128 + wc * 32 + fq * 8;
;                     f32x4 v0 = acc[ai][bj][m][0] * rs, v1 = acc[ai][bj][m][1] * rs;
;                     if (pn < 6) { if (pn < 2) { v0 = v0 * QS_SB; v1 = v1 * QS_SB; } *(u32x4*)(QKV + (size_t)row * 1536 + pn * 256 + c) = pack8(v0, v1); }
.LBB0_438:
	v_pk_mul_f32 v[94:95], v[88:89], s[96:97] op_sel_hi:[1,0]
	v_pk_mul_f32 v[96:97], v[86:87], s[96:97] op_sel_hi:[1,0]
	v_pk_mul_f32 v[100:101], v[84:85], s[96:97] op_sel_hi:[1,0]
	v_pk_mul_f32 v[102:103], v[82:83], s[96:97] op_sel_hi:[1,0]
	v_cndmask_b32_e64 v85, v85, v101, s[12:13]
	v_cndmask_b32_e64 v100, v84, v100, s[12:13]
	v_cndmask_b32_e64 v84, v83, v103, s[12:13]
	v_cndmask_b32_e64 v101, v82, v102, s[12:13]
	v_cndmask_b32_e64 v83, v89, v95, s[12:13]
	v_cndmask_b32_e64 v88, v88, v94, s[12:13]
	v_cndmask_b32_e64 v82, v87, v97, s[12:13]
	v_cndmask_b32_e64 v86, v86, v96, s[12:13]
	v_cvt_pk_bf16_f32 v82, v86, v82
	v_cvt_pk_bf16_f32 v83, v88, v83
	v_cvt_pk_bf16_f32 v84, v101, v84
	v_cvt_pk_bf16_f32 v85, v100, v85
	v_lshl_add_u64 v[86:87], v[90:91], 0, v[0:1]
	v_mov_b32_e32 v94, v110
	global_store_dwordx4 v[86:87], v[82:85], off offset:256 nt
	s_and_b64 vcc, exec, s[20:21]
	s_cbranch_vccnz .LBB0_442

; __device__ __forceinline__ u32x4 pack8(f32x4 a, f32x4 b) { u32x4 w; w.x = pk2(a[0], a[1]); w.y = pk2(a[2], a[3]); w.z = pk2(b[0], b[1]); w.w = pk2(b[2], b[3]); return w; }
; __device__ __forceinline__ float sq8(const f32x4& a, const f32x4& b) { return ((a[0] * a[0] + a[1] * a[1]) + (a[2] * a[2] + a[3] * a[3])) + ((b[0] * b[0] + b[1] * b[1]) + (b[2] * b[2] + b[3] * b[3])); }
; __device__ __forceinline__ f32x2 rtab_get(LAS unsigned char* lds, int ui, int r) { return ((const LAS f32x2*)(lds + RTAB_OFF))[(ui & 1) * 256 + r]; }
;     __device__ __forceinline__ void operator()(const f32x4 (&acc)[2][2][4][2], const Unit& u, int ui, int wr, int wc, int fr, int fq, LAS unsigned char* lds) const {
;     ...
;                 const int rr = ai * 128 + wr * 64 + m * 16 + fr, row = u.pm * 256 + rr; const float rs = rtab_get(lds, ui, rr)[0];
;                 float sq = 0.f;
; #pragma unroll
;                 for (int bj = 0; bj < 2; ++bj) {
;                     const int c = bj * 128 + wc * 32 + fq * 8;
;                     f32x4 v0 = acc[ai][bj][m][0] * rs, v1 = acc[ai][bj][m][1] * rs;
;                     if (pn < 6) { if (pn < 2) { v0 = v0 * QS_SB; v1 = v1 * QS_SB; } *(u32x4*)(QKV + (size_t)row * 1536 + pn * 256 + c) = pack8(v0, v1); }
;                     else if (pn == 6) { *(u32x4*)(CKV + (size_t)row * 256 + c) = pack8(v0, v1); sq += sq8(v0, v1); }
;                     else if (pn == 7) { *(u32x4*)(CQ + (size_t)row * 384 + c) = pack8(v0, v1); sq += sq8(v0, v1); }
;                     else if (bj == 0) { *(u32x4*)(CQ + (size_t)row * 384 + 256 + c) = pack8(v0, v1); sq += sq8(v0, v1); }
.LBB0_442:
	ds_read_b32 v88, v150 offset:384
	v_add3_u32 v82, s3, v151, 48
	v_ashrrev_i32_e32 v83, 31, v82
	v_mad_i64_i32 v[86:87], s[6:7], v82, s59, 0
	v_lshlrev_b64 v[84:85], 9, v[82:83]
	s_waitcnt lgkmcnt(0)
	v_pk_mul_f32 v[80:81], v[80:81], v[88:89] op_sel_hi:[1,0]
	v_pk_mul_f32 v[78:79], v[78:79], v[88:89] op_sel_hi:[1,0]
	v_pk_mul_f32 v[92:93], v[76:77], v[88:89] op_sel_hi:[1,0]
	v_pk_mul_f32 v[90:91], v[74:75], v[88:89] op_sel_hi:[1,0]
	s_and_b64 vcc, exec, s[18:19]
	s_mov_b64 s[64:65], -1
	s_cbranch_vccnz .LBB0_452
	v_cvt_pk_bf16_f32 v74, v78, v79
	v_cvt_pk_bf16_f32 v75, v80, v81
	v_cvt_pk_bf16_f32 v76, v90, v91
	v_cvt_pk_bf16_f32 v77, v92, v93
	s_cmp_lt_i32 s26, 7
	s_cbranch_scc1 .LBB0_449
	s_cmp_lg_u32 s26, 7
	s_cbranch_scc0 .LBB0_446
	v_lshl_add_u64 v[94:95], s[40:41], 0, v[86:87]
	v_lshl_add_u64 v[94:95], v[94:95], 0, v[0:1]
	v_mov_b32_e32 v96, v79
	v_mov_b32_e32 v97, v91
	global_store_dwordx4 v[94:95], v[74:77], off offset:512 nt
	v_mov_b32_e32 v94, v78
	v_mov_b32_e32 v95, v90
	v_pk_mul_f32 v[96:97], v[96:97], v[96:97]
	v_mov_b32_e32 v98, v81
	v_mov_b32_e32 v99, v93
	v_pk_fma_f32 v[94:95], v[94:95], v[94:95], v[96:97]
	v_mov_b32_e32 v96, v80
	v_mov_b32_e32 v97, v92
	v_pk_mul_f32 v[98:99], v[98:99], v[98:99]
	s_mov_b64 s[64:65], 0
	v_pk_fma_f32 v[96:97], v[96:97], v[96:97], v[98:99]
	s_nop 0
	v_pk_add_f32 v[94:95], v[94:95], v[96:97]
	s_nop 0
	v_add_f32_e32 v94, v94, v95
.LBB0_446:
	s_andn2_b64 vcc, exec, s[64:65]
	s_cbranch_vccnz .LBB0_448
	v_lshl_add_u64 v[94:95], s[40:41], 0, v[86:87]
	v_lshl_add_u64 v[94:95], v[94:95], 0, v[0:1]
	v_mov_b32_e32 v96, v79
	v_mov_b32_e32 v97, v91
	global_store_dwordx4 v[94:95], v[74:77], off nt
	v_mov_b32_e32 v94, v78
	v_mov_b32_e32 v95, v90
	v_pk_mul_f32 v[96:97], v[96:97], v[96:97]
	v_mov_b32_e32 v98, v81
	v_mov_b32_e32 v99, v93
	v_pk_fma_f32 v[94:95], v[94:95], v[94:95], v[96:97]
	v_mov_b32_e32 v96, v80
	v_mov_b32_e32 v97, v92
	v_pk_mul_f32 v[98:99], v[98:99], v[98:99]
	s_nop 0
	v_pk_fma_f32 v[96:97], v[96:97], v[96:97], v[98:99]
	s_nop 0
	v_pk_add_f32 v[94:95], v[94:95], v[96:97]
	s_nop 0
	v_add_f32_e32 v94, v94, v95

; __device__ __forceinline__ u32x4 pack8(f32x4 a, f32x4 b) { u32x4 w; w.x = pk2(a[0], a[1]); w.y = pk2(a[2], a[3]); w.z = pk2(b[0], b[1]); w.w = pk2(b[2], b[3]); return w; }
; __device__ __forceinline__ float sq8(const f32x4& a, const f32x4& b) { return ((a[0] * a[0] + a[1] * a[1]) + (a[2] * a[2] + a[3] * a[3])) + ((b[0] * b[0] + b[1] * b[1]) + (b[2] * b[2] + b[3] * b[3])); }
;     __device__ __forceinline__ void operator()(const f32x4 (&acc)[2][2][4][2], const Unit& u, int ui, int wr, int wc, int fr, int fq, LAS unsigned char* lds) const {
;     ...
;                 for (int bj = 0; bj < 2; ++bj) {
;                     const int c = bj * 128 + wc * 32 + fq * 8;
;                     f32x4 v0 = acc[ai][bj][m][0] * rs, v1 = acc[ai][bj][m][1] * rs;
;                     if (pn < 6) { if (pn < 2) { v0 = v0 * QS_SB; v1 = v1 * QS_SB; } *(u32x4*)(QKV + (size_t)row * 1536 + pn * 256 + c) = pack8(v0, v1); }
;                     else if (pn == 6) { *(u32x4*)(CKV + (size_t)row * 256 + c) = pack8(v0, v1); sq += sq8(v0, v1); }
.LBB0_449:
	s_andn2_b64 vcc, exec, s[64:65]
	s_cbranch_vccnz .LBB0_451
	v_lshl_add_u64 v[94:95], s[38:39], 0, v[84:85]
	v_lshl_add_u64 v[94:95], v[94:95], 0, v[0:1]
	global_store_dwordx4 v[94:95], v[74:77], off nt
	v_mov_b32_e32 v94, v81
	v_mov_b32_e32 v95, v93
	v_mov_b32_e32 v76, v79
	v_mov_b32_e32 v77, v91
	v_mov_b32_e32 v74, v78
	v_mov_b32_e32 v75, v90
	v_pk_mul_f32 v[76:77], v[76:77], v[76:77]
	v_pk_mul_f32 v[94:95], v[94:95], v[94:95]
	v_pk_fma_f32 v[74:75], v[74:75], v[74:75], v[76:77]
	v_mov_b32_e32 v76, v80
	v_mov_b32_e32 v77, v92
	v_pk_fma_f32 v[76:77], v[76:77], v[76:77], v[94:95]
	s_nop 0
	v_pk_add_f32 v[74:75], v[74:75], v[76:77]
	s_nop 0
	v_add_f32_e32 v94, v74, v75

; __device__ __forceinline__ u32x4 pack8(f32x4 a, f32x4 b) { u32x4 w; w.x = pk2(a[0], a[1]); w.y = pk2(a[2], a[3]); w.z = pk2(b[0], b[1]); w.w = pk2(b[2], b[3]); return w; }
;     __device__ __forceinline__ void operator()(const f32x4 (&acc)[2][2][4][2], const Unit& u, int ui, int wr, int wc, int fr, int fq, LAS unsigned char* lds) const {
;     ...
;                 for (int bj = 0; bj < 2; ++bj) {
;                     const int c = bj * 128 + wc * 32 + fq * 8;
;                     f32x4 v0 = acc[ai][bj][m][0] * rs, v1 = acc[ai][bj][m][1] * rs;
;                     if (pn < 6) { if (pn < 2) { v0 = v0 * QS_SB; v1 = v1 * QS_SB; } *(u32x4*)(QKV + (size_t)row * 1536 + pn * 256 + c) = pack8(v0, v1); }
.LBB0_452:
	s_movk_i32 s3, 0xc00
	v_mad_i64_i32 v[74:75], s[6:7], v82, s3, 0
	v_lshl_add_u64 v[74:75], s[36:37], 0, v[74:75]
	s_and_b64 vcc, exec, s[64:65]
	v_lshl_add_u64 v[74:75], s[62:63], 1, v[74:75]
	s_cbranch_vccz .LBB0_454
	v_pk_mul_f32 v[76:77], v[80:81], s[96:97] op_sel_hi:[1,0]
	v_pk_mul_f32 v[94:95], v[78:79], s[96:97] op_sel_hi:[1,0]
	v_pk_mul_f32 v[96:97], v[92:93], s[96:97] op_sel_hi:[1,0]
	v_pk_mul_f32 v[98:99], v[90:91], s[96:97] op_sel_hi:[1,0]
	v_cndmask_b32_e64 v89, v93, v97, s[12:13]
	v_cndmask_b32_e64 v92, v92, v96, s[12:13]
	v_cndmask_b32_e64 v91, v91, v99, s[12:13]
	v_cndmask_b32_e64 v90, v90, v98, s[12:13]
	v_cndmask_b32_e64 v77, v81, v77, s[12:13]
	v_cndmask_b32_e64 v80, v80, v76, s[12:13]
	v_cndmask_b32_e64 v76, v79, v95, s[12:13]
	v_cndmask_b32_e64 v78, v78, v94, s[12:13]
	v_cvt_pk_bf16_f32 v76, v78, v76
	v_cvt_pk_bf16_f32 v77, v80, v77
	v_cvt_pk_bf16_f32 v78, v90, v91
	v_cvt_pk_bf16_f32 v79, v92, v89
	v_lshl_add_u64 v[80:81], v[74:75], 0, v[0:1]
	v_mov_b32_e32 v94, 0
	global_store_dwordx4 v[80:81], v[76:79], off nt

; __device__ __forceinline__ float xor32(float x) { auto rr = __builtin_amdgcn_permlane32_swap(__float_as_uint(x), __float_as_uint(x), false, false); return __uint_as_float(((unsigned)(threadIdx.x & 32)) ? rr[0] : rr[1]); }
; __device__ __forceinline__ u32x4 pack8(f32x4 a, f32x4 b) { u32x4 w; w.x = pk2(a[0], a[1]); w.y = pk2(a[2], a[3]); w.z = pk2(b[0], b[1]); w.w = pk2(b[2], b[3]); return w; }
;     __device__ __forceinline__ void operator()(const f32x4 (&acc)[2][2][4][2], const Unit& u, int ui, int wr, int wc, int fr, int fq, LAS unsigned char* lds) const {
;     ...
;                     else if (wc == 0) {
;                         const int ib = 8 * (fq & 1);
;                         const f32x4 c0 = *(const f32x4*)(COS + (size_t)row * 16 + ib), c1 = *(const f32x4*)(COS + (size_t)row * 16 + ib + 4);
;                         const f32x4 s0 = *(const f32x4*)(SIN + (size_t)row * 16 + ib), s1 = *(const f32x4*)(SIN + (size_t)row * 16 + ib + 4);
;                         f32x4 p0, p1;
; #pragma unroll
;                         for (int i = 0; i < 4; ++i) { p0[i] = xor32(v0[i]); p1[i] = xor32(v1[i]); }
;                         const float sg = (fq < 2) ? -1.f : 1.f;
;                         const f32x4 o0 = v0 * c0 + p0 * s0 * sg, o1 = v1 * c1 + p1 * s1 * sg;
;                         *(u32x4*)(KR + (size_t)row * 32 + fq * 8) = pack8(o0, o1);
.LBB0_457:
	s_cmp_lt_i32 s26, 7
	s_cbranch_scc1 .LBB0_465
	s_cmp_lg_u32 s26, 7
	s_cbranch_scc0 .LBB0_462
	s_andn2_b64 vcc, exec, s[56:57]
	s_cbranch_vccnz .LBB0_461
	v_lshlrev_b64 v[96:97], 2, v[76:77]
	v_lshl_add_u64 v[78:79], s[44:45], 0, v[96:97]
	v_lshlrev_b32_e32 v98, 2, v128
	v_mov_b32_e32 v99, v1
	v_lshl_add_u64 v[96:97], s[46:47], 0, v[96:97]
	v_lshl_add_u64 v[88:89], v[78:79], 0, v[98:99]
	v_lshl_add_u64 v[100:101], v[96:97], 0, v[98:99]
	s_waitcnt vmcnt(10)
	v_mov_b32_e32 v78, v174
	v_mov_b32_e32 v79, v175
	v_mov_b32_e32 v80, v176
	v_mov_b32_e32 v81, v177
	v_mov_b32_e32 v88, v178
	v_mov_b32_e32 v89, v179
	v_mov_b32_e32 v90, v180
	v_mov_b32_e32 v91, v181
	v_mov_b32_e32 v96, v182
	v_mov_b32_e32 v97, v183
	v_mov_b32_e32 v98, v184
	v_mov_b32_e32 v99, v185
	v_mov_b32_e32 v100, v230
	v_mov_b32_e32 v101, v231
	v_mov_b32_e32 v102, v232
	v_mov_b32_e32 v103, v233
	global_load_dwordx4 v[174:177], v[206:207], off offset:1024
	global_load_dwordx4 v[178:181], v[206:207], off offset:1040
	global_load_dwordx4 v[182:185], v[208:209], off offset:1024
	global_load_dwordx4 v[230:233], v[208:209], off offset:1040
	v_mov_b32_e32 v95, v70
	v_mov_b32_e32 v104, v70
	s_nop 1
	v_permlane32_swap_b32_e32 v95, v104
	v_cndmask_b32_e64 v104, v95, v104, s[4:5]
	v_mov_b32_e32 v95, v66
	v_mov_b32_e32 v105, v66
	s_nop 1
	v_permlane32_swap_b32_e32 v95, v105
	v_cndmask_b32_e64 v106, v95, v105, s[4:5]
	v_mov_b32_e32 v95, v71
	v_mov_b32_e32 v105, v71
	s_nop 1
	v_permlane32_swap_b32_e32 v95, v105
	v_cndmask_b32_e64 v105, v95, v105, s[4:5]
	v_mov_b32_e32 v95, v67
	v_mov_b32_e32 v107, v67
	s_nop 1
	v_permlane32_swap_b32_e32 v95, v107
	v_cndmask_b32_e64 v107, v95, v107, s[4:5]
	v_mov_b32_e32 v95, v72
	v_mov_b32_e32 v108, v72
	s_nop 1
	v_permlane32_swap_b32_e32 v95, v108
	v_cndmask_b32_e64 v108, v95, v108, s[4:5]
	v_mov_b32_e32 v95, v68
	v_mov_b32_e32 v109, v68
	s_nop 1
	v_permlane32_swap_b32_e32 v95, v109
	v_cndmask_b32_e64 v110, v95, v109, s[4:5]
	v_mov_b32_e32 v95, v73
	v_mov_b32_e32 v109, v73
	s_nop 1
	v_permlane32_swap_b32_e32 v95, v109
	v_cndmask_b32_e64 v109, v95, v109, s[4:5]
	v_mov_b32_e32 v95, v69
	v_mov_b32_e32 v111, v69
	s_nop 1
	v_permlane32_swap_b32_e32 v95, v111
	v_cndmask_b32_e64 v111, v95, v111, s[4:5]
	v_lshlrev_b64 v[92:93], 6, v[82:83]
	s_waitcnt lgkmcnt(0)
	v_pk_mul_f32 v[98:99], v[98:99], v[108:109]
	v_pk_mul_f32 v[96:97], v[96:97], v[104:105]
	v_mov_b32_e32 v104, v114
	v_mov_b32_e32 v105, v114
	v_pk_mul_f32 v[96:97], v[114:115], v[96:97]
	v_pk_mul_f32 v[98:99], v[104:105], v[98:99]
	v_pk_fma_f32 v[78:79], v[70:71], v[78:79], v[96:97]
	v_pk_fma_f32 v[80:81], v[72:73], v[80:81], v[98:99]
	v_pk_mul_f32 v[96:97], v[102:103], v[110:111]
	v_pk_mul_f32 v[98:99], v[100:101], v[106:107]
	v_pk_mul_f32 v[96:97], v[104:105], v[96:97]
	v_pk_mul_f32 v[98:99], v[114:115], v[98:99]
	v_pk_fma_f32 v[90:91], v[68:69], v[90:91], v[96:97]
	v_pk_fma_f32 v[88:89], v[66:67], v[88:89], v[98:99]
	v_cvt_pk_bf16_f32 v78, v78, v79
	v_cvt_pk_bf16_f32 v79, v80, v81
	v_cvt_pk_bf16_f32 v80, v88, v89
	v_cvt_pk_bf16_f32 v81, v90, v91
	v_lshl_add_u64 v[88:89], s[42:43], 0, v[92:93]
	v_lshlrev_b32_e32 v90, 1, v149
	v_mov_b32_e32 v91, v1
	v_lshl_add_u64 v[88:89], v[88:89], 0, v[90:91]
	global_store_dwordx4 v[88:89], v[78:81], off nt

; __device__ __forceinline__ u32x4 pack8(f32x4 a, f32x4 b) { u32x4 w; w.x = pk2(a[0], a[1]); w.y = pk2(a[2], a[3]); w.z = pk2(b[0], b[1]); w.w = pk2(b[2], b[3]); return w; }
; __device__ __forceinline__ float sq8(const f32x4& a, const f32x4& b) { return ((a[0] * a[0] + a[1] * a[1]) + (a[2] * a[2] + a[3] * a[3])) + ((b[0] * b[0] + b[1] * b[1]) + (b[2] * b[2] + b[3] * b[3])); }
;     __device__ __forceinline__ void operator()(const f32x4 (&acc)[2][2][4][2], const Unit& u, int ui, int wr, int wc, int fr, int fq, LAS unsigned char* lds) const {
;     ...
;                 for (int bj = 0; bj < 2; ++bj) {
;                     const int c = bj * 128 + wc * 32 + fq * 8;
;                     f32x4 v0 = acc[ai][bj][m][0] * rs, v1 = acc[ai][bj][m][1] * rs;
;                     if (pn < 6) { if (pn < 2) { v0 = v0 * QS_SB; v1 = v1 * QS_SB; } *(u32x4*)(QKV + (size_t)row * 1536 + pn * 256 + c) = pack8(v0, v1); }
;                     else if (pn == 6) { *(u32x4*)(CKV + (size_t)row * 256 + c) = pack8(v0, v1); sq += sq8(v0, v1); }
;                     else if (pn == 7) { *(u32x4*)(CQ + (size_t)row * 384 + c) = pack8(v0, v1); sq += sq8(v0, v1); }
.LBB0_462:
	s_andn2_b64 vcc, exec, s[64:65]
	v_mov_b32_e32 v78, v94
	s_cbranch_vccnz .LBB0_464
	v_lshl_add_u64 v[86:87], s[40:41], 0, v[86:87]
	v_cvt_pk_bf16_f32 v78, v70, v71
	v_cvt_pk_bf16_f32 v79, v72, v73
	v_cvt_pk_bf16_f32 v80, v66, v67
	v_cvt_pk_bf16_f32 v81, v68, v69
	v_lshl_add_u64 v[86:87], v[86:87], 0, v[0:1]
	global_store_dwordx4 v[86:87], v[78:81], off offset:256 nt
	v_mov_b32_e32 v86, v73
	v_mov_b32_e32 v87, v69
	v_mov_b32_e32 v80, v71
	v_mov_b32_e32 v81, v67
	v_mov_b32_e32 v78, v70
	v_mov_b32_e32 v79, v66
	v_pk_mul_f32 v[80:81], v[80:81], v[80:81]
	v_pk_mul_f32 v[86:87], v[86:87], v[86:87]
	v_pk_fma_f32 v[78:79], v[78:79], v[78:79], v[80:81]
	v_mov_b32_e32 v80, v72
	v_mov_b32_e32 v81, v68
	v_pk_fma_f32 v[80:81], v[80:81], v[80:81], v[86:87]
	s_nop 0
	v_pk_add_f32 v[78:79], v[78:79], v[80:81]
	s_nop 0
	v_add_f32_e32 v78, v78, v79
	v_add_f32_e32 v78, v78, v94

; __device__ __forceinline__ u32x4 pack8(f32x4 a, f32x4 b) { u32x4 w; w.x = pk2(a[0], a[1]); w.y = pk2(a[2], a[3]); w.z = pk2(b[0], b[1]); w.w = pk2(b[2], b[3]); return w; }
; __device__ __forceinline__ float sq8(const f32x4& a, const f32x4& b) { return ((a[0] * a[0] + a[1] * a[1]) + (a[2] * a[2] + a[3] * a[3])) + ((b[0] * b[0] + b[1] * b[1]) + (b[2] * b[2] + b[3] * b[3])); }
;     __device__ __forceinline__ void operator()(const f32x4 (&acc)[2][2][4][2], const Unit& u, int ui, int wr, int wc, int fr, int fq, LAS unsigned char* lds) const {
;     ...
;                 for (int bj = 0; bj < 2; ++bj) {
;                     const int c = bj * 128 + wc * 32 + fq * 8;
;                     f32x4 v0 = acc[ai][bj][m][0] * rs, v1 = acc[ai][bj][m][1] * rs;
;                     if (pn < 6) { if (pn < 2) { v0 = v0 * QS_SB; v1 = v1 * QS_SB; } *(u32x4*)(QKV + (size_t)row * 1536 + pn * 256 + c) = pack8(v0, v1); }
;                     else if (pn == 6) { *(u32x4*)(CKV + (size_t)row * 256 + c) = pack8(v0, v1); sq += sq8(v0, v1); }
.LBB0_465:
	s_andn2_b64 vcc, exec, s[64:65]
	s_cbranch_vccnz .LBB0_467
	v_lshl_add_u64 v[84:85], s[38:39], 0, v[84:85]
	v_cvt_pk_bf16_f32 v78, v70, v71
	v_cvt_pk_bf16_f32 v79, v72, v73
	v_cvt_pk_bf16_f32 v80, v66, v67
	v_cvt_pk_bf16_f32 v81, v68, v69
	v_lshl_add_u64 v[84:85], v[84:85], 0, v[0:1]
	global_store_dwordx4 v[84:85], v[78:81], off offset:256 nt
	v_mov_b32_e32 v84, v73
	v_mov_b32_e32 v85, v69
	v_mov_b32_e32 v80, v71
	v_mov_b32_e32 v81, v67
	v_mov_b32_e32 v78, v70
	v_mov_b32_e32 v79, v66
	v_pk_mul_f32 v[80:81], v[80:81], v[80:81]
	v_pk_mul_f32 v[84:85], v[84:85], v[84:85]
	v_pk_fma_f32 v[78:79], v[78:79], v[78:79], v[80:81]
	v_mov_b32_e32 v80, v72
	v_mov_b32_e32 v81, v68
	v_pk_fma_f32 v[80:81], v[80:81], v[80:81], v[84:85]
	s_nop 0
	v_pk_add_f32 v[78:79], v[78:79], v[80:81]
	s_nop 0
	v_add_f32_e32 v78, v78, v79
	v_add_f32_e32 v78, v78, v94

; __device__ __forceinline__ u32x4 pack8(f32x4 a, f32x4 b) { u32x4 w; w.x = pk2(a[0], a[1]); w.y = pk2(a[2], a[3]); w.z = pk2(b[0], b[1]); w.w = pk2(b[2], b[3]); return w; }
;     __device__ __forceinline__ void operator()(const f32x4 (&acc)[2][2][4][2], const Unit& u, int ui, int wr, int wc, int fr, int fq, LAS unsigned char* lds) const {
;     ...
;                 for (int bj = 0; bj < 2; ++bj) {
;                     const int c = bj * 128 + wc * 32 + fq * 8;
;                     f32x4 v0 = acc[ai][bj][m][0] * rs, v1 = acc[ai][bj][m][1] * rs;
;                     if (pn < 6) { if (pn < 2) { v0 = v0 * QS_SB; v1 = v1 * QS_SB; } *(u32x4*)(QKV + (size_t)row * 1536 + pn * 256 + c) = pack8(v0, v1); }
.LBB0_468:
	v_pk_mul_f32 v[78:79], v[72:73], s[96:97] op_sel_hi:[1,0]
	v_pk_mul_f32 v[80:81], v[70:71], s[96:97] op_sel_hi:[1,0]
	v_pk_mul_f32 v[84:85], v[68:69], s[96:97] op_sel_hi:[1,0]
	v_pk_mul_f32 v[86:87], v[66:67], s[96:97] op_sel_hi:[1,0]
	v_cndmask_b32_e64 v69, v69, v85, s[12:13]
	v_cndmask_b32_e64 v84, v68, v84, s[12:13]
	v_cndmask_b32_e64 v68, v67, v87, s[12:13]
	v_cndmask_b32_e64 v85, v66, v86, s[12:13]
	v_cndmask_b32_e64 v67, v73, v79, s[12:13]
	v_cndmask_b32_e64 v72, v72, v78, s[12:13]
	v_cndmask_b32_e64 v66, v71, v81, s[12:13]
	v_cndmask_b32_e64 v70, v70, v80, s[12:13]
	v_cvt_pk_bf16_f32 v66, v70, v66
	v_cvt_pk_bf16_f32 v67, v72, v67
	v_cvt_pk_bf16_f32 v68, v85, v68
	v_cvt_pk_bf16_f32 v69, v84, v69
	v_lshl_add_u64 v[70:71], v[74:75], 0, v[0:1]
	v_mov_b32_e32 v78, v94
	global_store_dwordx4 v[70:71], v[66:69], off offset:256 nt
	s_and_b64 vcc, exec, s[20:21]
	s_cbranch_vccnz .LBB0_472

; __device__ __forceinline__ u32x4 pack8(f32x4 a, f32x4 b) { u32x4 w; w.x = pk2(a[0], a[1]); w.y = pk2(a[2], a[3]); w.z = pk2(b[0], b[1]); w.w = pk2(b[2], b[3]); return w; }
; __device__ __forceinline__ float sq8(const f32x4& a, const f32x4& b) { return ((a[0] * a[0] + a[1] * a[1]) + (a[2] * a[2] + a[3] * a[3])) + ((b[0] * b[0] + b[1] * b[1]) + (b[2] * b[2] + b[3] * b[3])); }
; __device__ __forceinline__ f32x2 rtab_get(LAS unsigned char* lds, int ui, int r) { return ((const LAS f32x2*)(lds + RTAB_OFF))[(ui & 1) * 256 + r]; }
;     __device__ __forceinline__ void operator()(const f32x4 (&acc)[2][2][4][2], const Unit& u, int ui, int wr, int wc, int fr, int fq, LAS unsigned char* lds) const {
;     ...
;                 const int rr = ai * 128 + wr * 64 + m * 16 + fr, row = u.pm * 256 + rr; const float rs = rtab_get(lds, ui, rr)[0];
;                 float sq = 0.f;
; #pragma unroll
;                 for (int bj = 0; bj < 2; ++bj) {
;                     const int c = bj * 128 + wc * 32 + fq * 8;
;                     f32x4 v0 = acc[ai][bj][m][0] * rs, v1 = acc[ai][bj][m][1] * rs;
;                     if (pn < 6) { if (pn < 2) { v0 = v0 * QS_SB; v1 = v1 * QS_SB; } *(u32x4*)(QKV + (size_t)row * 1536 + pn * 256 + c) = pack8(v0, v1); }
;                     else if (pn == 6) { *(u32x4*)(CKV + (size_t)row * 256 + c) = pack8(v0, v1); sq += sq8(v0, v1); }
;                     else if (pn == 7) { *(u32x4*)(CQ + (size_t)row * 384 + c) = pack8(v0, v1); sq += sq8(v0, v1); }
;                     else if (bj == 0) { *(u32x4*)(CQ + (size_t)row * 384 + 256 + c) = pack8(v0, v1); sq += sq8(v0, v1); }
.LBB0_472:
	ds_read_b32 v72, v150 offset:1024
	v_add_u32_e32 v66, 0x80, v138
	v_ashrrev_i32_e32 v67, 31, v66
	v_mad_i64_i32 v[70:71], s[6:7], v66, s59, 0
	v_lshlrev_b64 v[68:69], 9, v[66:67]
	s_waitcnt lgkmcnt(0)
	v_pk_mul_f32 v[64:65], v[64:65], v[72:73] op_sel_hi:[1,0]
	v_pk_mul_f32 v[62:63], v[62:63], v[72:73] op_sel_hi:[1,0]
	v_pk_mul_f32 v[76:77], v[60:61], v[72:73] op_sel_hi:[1,0]
	v_pk_mul_f32 v[74:75], v[58:59], v[72:73] op_sel_hi:[1,0]
	s_and_b64 vcc, exec, s[18:19]
	s_mov_b64 s[64:65], -1
	s_cbranch_vccnz .LBB0_482
	v_cvt_pk_bf16_f32 v58, v62, v63
	v_cvt_pk_bf16_f32 v59, v64, v65
	v_cvt_pk_bf16_f32 v60, v74, v75
	v_cvt_pk_bf16_f32 v61, v76, v77
	s_cmp_lt_i32 s26, 7
	s_cbranch_scc1 .LBB0_479
	s_cmp_lg_u32 s26, 7
	s_cbranch_scc0 .LBB0_476
	v_lshl_add_u64 v[78:79], s[40:41], 0, v[70:71]
	v_lshl_add_u64 v[78:79], v[78:79], 0, v[0:1]
	v_mov_b32_e32 v80, v63
	v_mov_b32_e32 v81, v75
	global_store_dwordx4 v[78:79], v[58:61], off offset:512 nt
	v_mov_b32_e32 v78, v62
	v_mov_b32_e32 v79, v74
	v_pk_mul_f32 v[80:81], v[80:81], v[80:81]
	v_mov_b32_e32 v82, v65
	v_mov_b32_e32 v83, v77
	v_pk_fma_f32 v[78:79], v[78:79], v[78:79], v[80:81]
	v_mov_b32_e32 v80, v64
	v_mov_b32_e32 v81, v76
	v_pk_mul_f32 v[82:83], v[82:83], v[82:83]
	s_mov_b64 s[64:65], 0
	v_pk_fma_f32 v[80:81], v[80:81], v[80:81], v[82:83]
	s_nop 0
	v_pk_add_f32 v[78:79], v[78:79], v[80:81]
	s_nop 0
	v_add_f32_e32 v78, v78, v79
.LBB0_476:
	s_andn2_b64 vcc, exec, s[64:65]
	s_cbranch_vccnz .LBB0_478
	v_lshl_add_u64 v[78:79], s[40:41], 0, v[70:71]
	v_lshl_add_u64 v[78:79], v[78:79], 0, v[0:1]
	v_mov_b32_e32 v80, v63
	v_mov_b32_e32 v81, v75
	global_store_dwordx4 v[78:79], v[58:61], off nt
	v_mov_b32_e32 v78, v62
	v_mov_b32_e32 v79, v74
	v_pk_mul_f32 v[80:81], v[80:81], v[80:81]
	v_mov_b32_e32 v82, v65
	v_mov_b32_e32 v83, v77
	v_pk_fma_f32 v[78:79], v[78:79], v[78:79], v[80:81]
	v_mov_b32_e32 v80, v64
	v_mov_b32_e32 v81, v76
	v_pk_mul_f32 v[82:83], v[82:83], v[82:83]
	s_nop 0
	v_pk_fma_f32 v[80:81], v[80:81], v[80:81], v[82:83]
	s_nop 0
	v_pk_add_f32 v[78:79], v[78:79], v[80:81]
	s_nop 0
	v_add_f32_e32 v78, v78, v79

; __device__ __forceinline__ u32x4 pack8(f32x4 a, f32x4 b) { u32x4 w; w.x = pk2(a[0], a[1]); w.y = pk2(a[2], a[3]); w.z = pk2(b[0], b[1]); w.w = pk2(b[2], b[3]); return w; }
; __device__ __forceinline__ float sq8(const f32x4& a, const f32x4& b) { return ((a[0] * a[0] + a[1] * a[1]) + (a[2] * a[2] + a[3] * a[3])) + ((b[0] * b[0] + b[1] * b[1]) + (b[2] * b[2] + b[3] * b[3])); }
;     __device__ __forceinline__ void operator()(const f32x4 (&acc)[2][2][4][2], const Unit& u, int ui, int wr, int wc, int fr, int fq, LAS unsigned char* lds) const {
;     ...
;                 for (int bj = 0; bj < 2; ++bj) {
;                     const int c = bj * 128 + wc * 32 + fq * 8;
;                     f32x4 v0 = acc[ai][bj][m][0] * rs, v1 = acc[ai][bj][m][1] * rs;
;                     if (pn < 6) { if (pn < 2) { v0 = v0 * QS_SB; v1 = v1 * QS_SB; } *(u32x4*)(QKV + (size_t)row * 1536 + pn * 256 + c) = pack8(v0, v1); }
;                     else if (pn == 6) { *(u32x4*)(CKV + (size_t)row * 256 + c) = pack8(v0, v1); sq += sq8(v0, v1); }
.LBB0_479:
	s_andn2_b64 vcc, exec, s[64:65]
	s_cbranch_vccnz .LBB0_481
	v_lshl_add_u64 v[78:79], s[38:39], 0, v[68:69]
	v_lshl_add_u64 v[78:79], v[78:79], 0, v[0:1]
	global_store_dwordx4 v[78:79], v[58:61], off nt
	v_mov_b32_e32 v78, v65
	v_mov_b32_e32 v79, v77
	v_mov_b32_e32 v60, v63
	v_mov_b32_e32 v61, v75
	v_mov_b32_e32 v58, v62
	v_mov_b32_e32 v59, v74
	v_pk_mul_f32 v[60:61], v[60:61], v[60:61]
	v_pk_mul_f32 v[78:79], v[78:79], v[78:79]
	v_pk_fma_f32 v[58:59], v[58:59], v[58:59], v[60:61]
	v_mov_b32_e32 v60, v64
	v_mov_b32_e32 v61, v76
	v_pk_fma_f32 v[60:61], v[60:61], v[60:61], v[78:79]
	s_nop 0
	v_pk_add_f32 v[58:59], v[58:59], v[60:61]
	s_nop 0
	v_add_f32_e32 v78, v58, v59

; __device__ __forceinline__ u32x4 pack8(f32x4 a, f32x4 b) { u32x4 w; w.x = pk2(a[0], a[1]); w.y = pk2(a[2], a[3]); w.z = pk2(b[0], b[1]); w.w = pk2(b[2], b[3]); return w; }
;     __device__ __forceinline__ void operator()(const f32x4 (&acc)[2][2][4][2], const Unit& u, int ui, int wr, int wc, int fr, int fq, LAS unsigned char* lds) const {
;     ...
;                 for (int bj = 0; bj < 2; ++bj) {
;                     const int c = bj * 128 + wc * 32 + fq * 8;
;                     f32x4 v0 = acc[ai][bj][m][0] * rs, v1 = acc[ai][bj][m][1] * rs;
;                     if (pn < 6) { if (pn < 2) { v0 = v0 * QS_SB; v1 = v1 * QS_SB; } *(u32x4*)(QKV + (size_t)row * 1536 + pn * 256 + c) = pack8(v0, v1); }
.LBB0_482:
	v_mad_i64_i32 v[58:59], s[6:7], v66, s3, 0
	v_lshl_add_u64 v[58:59], s[36:37], 0, v[58:59]
	s_and_b64 vcc, exec, s[64:65]
	v_lshl_add_u64 v[58:59], s[62:63], 1, v[58:59]
	s_cbranch_vccz .LBB0_484
	v_pk_mul_f32 v[60:61], v[64:65], s[96:97] op_sel_hi:[1,0]
	v_pk_mul_f32 v[78:79], v[62:63], s[96:97] op_sel_hi:[1,0]
	v_pk_mul_f32 v[80:81], v[76:77], s[96:97] op_sel_hi:[1,0]
	v_pk_mul_f32 v[82:83], v[74:75], s[96:97] op_sel_hi:[1,0]
	v_cndmask_b32_e64 v73, v77, v81, s[12:13]
	v_cndmask_b32_e64 v76, v76, v80, s[12:13]
	v_cndmask_b32_e64 v75, v75, v83, s[12:13]
	v_cndmask_b32_e64 v74, v74, v82, s[12:13]
	v_cndmask_b32_e64 v61, v65, v61, s[12:13]
	v_cndmask_b32_e64 v64, v64, v60, s[12:13]
	v_cndmask_b32_e64 v60, v63, v79, s[12:13]
	v_cndmask_b32_e64 v62, v62, v78, s[12:13]
	v_cvt_pk_bf16_f32 v60, v62, v60
	v_cvt_pk_bf16_f32 v61, v64, v61
	v_cvt_pk_bf16_f32 v62, v74, v75
	v_cvt_pk_bf16_f32 v63, v76, v73
	v_lshl_add_u64 v[64:65], v[58:59], 0, v[0:1]
	v_mov_b32_e32 v78, 0
	global_store_dwordx4 v[64:65], v[60:63], off nt

; __device__ __forceinline__ float xor32(float x) { auto rr = __builtin_amdgcn_permlane32_swap(__float_as_uint(x), __float_as_uint(x), false, false); return __uint_as_float(((unsigned)(threadIdx.x & 32)) ? rr[0] : rr[1]); }
; __device__ __forceinline__ u32x4 pack8(f32x4 a, f32x4 b) { u32x4 w; w.x = pk2(a[0], a[1]); w.y = pk2(a[2], a[3]); w.z = pk2(b[0], b[1]); w.w = pk2(b[2], b[3]); return w; }
;     __device__ __forceinline__ void operator()(const f32x4 (&acc)[2][2][4][2], const Unit& u, int ui, int wr, int wc, int fr, int fq, LAS unsigned char* lds) const {
;     ...
;                     else if (wc == 0) {
;                         const int ib = 8 * (fq & 1);
;                         const f32x4 c0 = *(const f32x4*)(COS + (size_t)row * 16 + ib), c1 = *(const f32x4*)(COS + (size_t)row * 16 + ib + 4);
;                         const f32x4 s0 = *(const f32x4*)(SIN + (size_t)row * 16 + ib), s1 = *(const f32x4*)(SIN + (size_t)row * 16 + ib + 4);
;                         f32x4 p0, p1;
; #pragma unroll
;                         for (int i = 0; i < 4; ++i) { p0[i] = xor32(v0[i]); p1[i] = xor32(v1[i]); }
;                         const float sg = (fq < 2) ? -1.f : 1.f;
;                         const f32x4 o0 = v0 * c0 + p0 * s0 * sg, o1 = v1 * c1 + p1 * s1 * sg;
;                         *(u32x4*)(KR + (size_t)row * 32 + fq * 8) = pack8(o0, o1);
.LBB0_487:
	s_cmp_lt_i32 s26, 7
	s_cbranch_scc1 .LBB0_495
	s_cmp_lg_u32 s26, 7
	s_cbranch_scc0 .LBB0_492
	s_andn2_b64 vcc, exec, s[56:57]
	s_cbranch_vccnz .LBB0_491
	v_lshlrev_b64 v[80:81], 2, v[60:61]
	v_lshl_add_u64 v[62:63], s[44:45], 0, v[80:81]
	v_lshlrev_b32_e32 v82, 2, v128
	v_mov_b32_e32 v83, v1
	v_lshl_add_u64 v[80:81], s[46:47], 0, v[80:81]
	v_lshl_add_u64 v[72:73], v[62:63], 0, v[82:83]
	v_lshl_add_u64 v[84:85], v[80:81], 0, v[82:83]
	s_waitcnt vmcnt(10)
	v_mov_b32_e32 v62, v214
	v_mov_b32_e32 v63, v215
	v_mov_b32_e32 v64, v216
	v_mov_b32_e32 v65, v217
	v_mov_b32_e32 v72, v218
	v_mov_b32_e32 v73, v219
	v_mov_b32_e32 v74, v220
	v_mov_b32_e32 v75, v221
	v_mov_b32_e32 v80, v222
	v_mov_b32_e32 v81, v223
	v_mov_b32_e32 v82, v224
	v_mov_b32_e32 v83, v225
	v_mov_b32_e32 v84, v226
	v_mov_b32_e32 v85, v227
	v_mov_b32_e32 v86, v228
	v_mov_b32_e32 v87, v229
	global_load_dwordx4 v[214:217], v[206:207], off offset:2048
	global_load_dwordx4 v[218:221], v[206:207], off offset:2064
	global_load_dwordx4 v[222:225], v[208:209], off offset:2048
	global_load_dwordx4 v[226:229], v[208:209], off offset:2064
	v_mov_b32_e32 v79, v54
	v_mov_b32_e32 v88, v54
	s_nop 1
	v_permlane32_swap_b32_e32 v79, v88
	v_cndmask_b32_e64 v88, v79, v88, s[4:5]
	v_mov_b32_e32 v79, v50
	v_mov_b32_e32 v89, v50
	s_nop 1
	v_permlane32_swap_b32_e32 v79, v89
	v_cndmask_b32_e64 v90, v79, v89, s[4:5]
	v_mov_b32_e32 v79, v55
	v_mov_b32_e32 v89, v55
	s_nop 1
	v_permlane32_swap_b32_e32 v79, v89
	v_cndmask_b32_e64 v89, v79, v89, s[4:5]
	v_mov_b32_e32 v79, v51
	v_mov_b32_e32 v91, v51
	s_nop 1
	v_permlane32_swap_b32_e32 v79, v91
	v_cndmask_b32_e64 v91, v79, v91, s[4:5]
	v_mov_b32_e32 v79, v56
	v_mov_b32_e32 v92, v56
	s_nop 1
	v_permlane32_swap_b32_e32 v79, v92
	v_cndmask_b32_e64 v92, v79, v92, s[4:5]
	v_mov_b32_e32 v79, v52
	v_mov_b32_e32 v93, v52
	s_nop 1
	v_permlane32_swap_b32_e32 v79, v93
	v_cndmask_b32_e64 v94, v79, v93, s[4:5]
	v_mov_b32_e32 v79, v57
	v_mov_b32_e32 v93, v57
	s_nop 1
	v_permlane32_swap_b32_e32 v79, v93
	v_cndmask_b32_e64 v93, v79, v93, s[4:5]
	v_mov_b32_e32 v79, v53
	v_mov_b32_e32 v95, v53
	s_nop 1
	v_permlane32_swap_b32_e32 v79, v95
	v_cndmask_b32_e64 v95, v79, v95, s[4:5]
	v_lshlrev_b64 v[76:77], 6, v[66:67]
	s_waitcnt lgkmcnt(0)
	v_pk_mul_f32 v[82:83], v[82:83], v[92:93]
	v_pk_mul_f32 v[80:81], v[80:81], v[88:89]
	v_mov_b32_e32 v88, v114
	v_mov_b32_e32 v89, v114
	v_pk_mul_f32 v[80:81], v[114:115], v[80:81]
	v_pk_mul_f32 v[82:83], v[88:89], v[82:83]
	v_pk_fma_f32 v[62:63], v[54:55], v[62:63], v[80:81]
	v_pk_fma_f32 v[64:65], v[56:57], v[64:65], v[82:83]
	v_pk_mul_f32 v[80:81], v[86:87], v[94:95]
	v_pk_mul_f32 v[82:83], v[84:85], v[90:91]
	v_pk_mul_f32 v[80:81], v[88:89], v[80:81]
	v_pk_mul_f32 v[82:83], v[114:115], v[82:83]
	v_pk_fma_f32 v[74:75], v[52:53], v[74:75], v[80:81]
	v_pk_fma_f32 v[72:73], v[50:51], v[72:73], v[82:83]
	v_cvt_pk_bf16_f32 v62, v62, v63
	v_cvt_pk_bf16_f32 v63, v64, v65
	v_cvt_pk_bf16_f32 v64, v72, v73
	v_cvt_pk_bf16_f32 v65, v74, v75
	v_lshl_add_u64 v[72:73], s[42:43], 0, v[76:77]
	v_lshlrev_b32_e32 v74, 1, v149
	v_mov_b32_e32 v75, v1
	v_lshl_add_u64 v[72:73], v[72:73], 0, v[74:75]
	global_store_dwordx4 v[72:73], v[62:65], off nt

; __device__ __forceinline__ u32x4 pack8(f32x4 a, f32x4 b) { u32x4 w; w.x = pk2(a[0], a[1]); w.y = pk2(a[2], a[3]); w.z = pk2(b[0], b[1]); w.w = pk2(b[2], b[3]); return w; }
; __device__ __forceinline__ float sq8(const f32x4& a, const f32x4& b) { return ((a[0] * a[0] + a[1] * a[1]) + (a[2] * a[2] + a[3] * a[3])) + ((b[0] * b[0] + b[1] * b[1]) + (b[2] * b[2] + b[3] * b[3])); }
;     __device__ __forceinline__ void operator()(const f32x4 (&acc)[2][2][4][2], const Unit& u, int ui, int wr, int wc, int fr, int fq, LAS unsigned char* lds) const {
;     ...
;                 for (int bj = 0; bj < 2; ++bj) {
;                     const int c = bj * 128 + wc * 32 + fq * 8;
;                     f32x4 v0 = acc[ai][bj][m][0] * rs, v1 = acc[ai][bj][m][1] * rs;
;                     if (pn < 6) { if (pn < 2) { v0 = v0 * QS_SB; v1 = v1 * QS_SB; } *(u32x4*)(QKV + (size_t)row * 1536 + pn * 256 + c) = pack8(v0, v1); }
;                     else if (pn == 6) { *(u32x4*)(CKV + (size_t)row * 256 + c) = pack8(v0, v1); sq += sq8(v0, v1); }
;                     else if (pn == 7) { *(u32x4*)(CQ + (size_t)row * 384 + c) = pack8(v0, v1); sq += sq8(v0, v1); }
.LBB0_492:
	s_andn2_b64 vcc, exec, s[64:65]
	v_mov_b32_e32 v62, v78
	s_cbranch_vccnz .LBB0_494
	v_lshl_add_u64 v[70:71], s[40:41], 0, v[70:71]
	v_cvt_pk_bf16_f32 v62, v54, v55
	v_cvt_pk_bf16_f32 v63, v56, v57
	v_cvt_pk_bf16_f32 v64, v50, v51
	v_cvt_pk_bf16_f32 v65, v52, v53
	v_lshl_add_u64 v[70:71], v[70:71], 0, v[0:1]
	global_store_dwordx4 v[70:71], v[62:65], off offset:256 nt
	v_mov_b32_e32 v70, v57
	v_mov_b32_e32 v71, v53
	v_mov_b32_e32 v64, v55
	v_mov_b32_e32 v65, v51
	v_mov_b32_e32 v62, v54
	v_mov_b32_e32 v63, v50
	v_pk_mul_f32 v[64:65], v[64:65], v[64:65]
	v_pk_mul_f32 v[70:71], v[70:71], v[70:71]
	v_pk_fma_f32 v[62:63], v[62:63], v[62:63], v[64:65]
	v_mov_b32_e32 v64, v56
	v_mov_b32_e32 v65, v52
	v_pk_fma_f32 v[64:65], v[64:65], v[64:65], v[70:71]
	s_nop 0
	v_pk_add_f32 v[62:63], v[62:63], v[64:65]
	s_nop 0
	v_add_f32_e32 v62, v62, v63
	v_add_f32_e32 v62, v62, v78

; __device__ __forceinline__ u32x4 pack8(f32x4 a, f32x4 b) { u32x4 w; w.x = pk2(a[0], a[1]); w.y = pk2(a[2], a[3]); w.z = pk2(b[0], b[1]); w.w = pk2(b[2], b[3]); return w; }
; __device__ __forceinline__ float sq8(const f32x4& a, const f32x4& b) { return ((a[0] * a[0] + a[1] * a[1]) + (a[2] * a[2] + a[3] * a[3])) + ((b[0] * b[0] + b[1] * b[1]) + (b[2] * b[2] + b[3] * b[3])); }
;     __device__ __forceinline__ void operator()(const f32x4 (&acc)[2][2][4][2], const Unit& u, int ui, int wr, int wc, int fr, int fq, LAS unsigned char* lds) const {
;     ...
;                 for (int bj = 0; bj < 2; ++bj) {
;                     const int c = bj * 128 + wc * 32 + fq * 8;
;                     f32x4 v0 = acc[ai][bj][m][0] * rs, v1 = acc[ai][bj][m][1] * rs;
;                     if (pn < 6) { if (pn < 2) { v0 = v0 * QS_SB; v1 = v1 * QS_SB; } *(u32x4*)(QKV + (size_t)row * 1536 + pn * 256 + c) = pack8(v0, v1); }
;                     else if (pn == 6) { *(u32x4*)(CKV + (size_t)row * 256 + c) = pack8(v0, v1); sq += sq8(v0, v1); }
.LBB0_495:
	s_andn2_b64 vcc, exec, s[64:65]
	s_cbranch_vccnz .LBB0_497
	v_lshl_add_u64 v[68:69], s[38:39], 0, v[68:69]
	v_cvt_pk_bf16_f32 v62, v54, v55
	v_cvt_pk_bf16_f32 v63, v56, v57
	v_cvt_pk_bf16_f32 v64, v50, v51
	v_cvt_pk_bf16_f32 v65, v52, v53
	v_lshl_add_u64 v[68:69], v[68:69], 0, v[0:1]
	global_store_dwordx4 v[68:69], v[62:65], off offset:256 nt
	v_mov_b32_e32 v68, v57
	v_mov_b32_e32 v69, v53
	v_mov_b32_e32 v64, v55
	v_mov_b32_e32 v65, v51
	v_mov_b32_e32 v62, v54
	v_mov_b32_e32 v63, v50
	v_pk_mul_f32 v[64:65], v[64:65], v[64:65]
	v_pk_mul_f32 v[68:69], v[68:69], v[68:69]
	v_pk_fma_f32 v[62:63], v[62:63], v[62:63], v[64:65]
	v_mov_b32_e32 v64, v56
	v_mov_b32_e32 v65, v52
	v_pk_fma_f32 v[64:65], v[64:65], v[64:65], v[68:69]
	s_nop 0
	v_pk_add_f32 v[62:63], v[62:63], v[64:65]
	s_nop 0
	v_add_f32_e32 v62, v62, v63
	v_add_f32_e32 v62, v62, v78

; __device__ __forceinline__ u32x4 pack8(f32x4 a, f32x4 b) { u32x4 w; w.x = pk2(a[0], a[1]); w.y = pk2(a[2], a[3]); w.z = pk2(b[0], b[1]); w.w = pk2(b[2], b[3]); return w; }
;     __device__ __forceinline__ void operator()(const f32x4 (&acc)[2][2][4][2], const Unit& u, int ui, int wr, int wc, int fr, int fq, LAS unsigned char* lds) const {
;     ...
;                 for (int bj = 0; bj < 2; ++bj) {
;                     const int c = bj * 128 + wc * 32 + fq * 8;
;                     f32x4 v0 = acc[ai][bj][m][0] * rs, v1 = acc[ai][bj][m][1] * rs;
;                     if (pn < 6) { if (pn < 2) { v0 = v0 * QS_SB; v1 = v1 * QS_SB; } *(u32x4*)(QKV + (size_t)row * 1536 + pn * 256 + c) = pack8(v0, v1); }
.LBB0_498:
	v_pk_mul_f32 v[62:63], v[56:57], s[96:97] op_sel_hi:[1,0]
	v_pk_mul_f32 v[64:65], v[54:55], s[96:97] op_sel_hi:[1,0]
	v_pk_mul_f32 v[68:69], v[52:53], s[96:97] op_sel_hi:[1,0]
	v_pk_mul_f32 v[70:71], v[50:51], s[96:97] op_sel_hi:[1,0]
	v_cndmask_b32_e64 v53, v53, v69, s[12:13]
	v_cndmask_b32_e64 v68, v52, v68, s[12:13]
	v_cndmask_b32_e64 v52, v51, v71, s[12:13]
	v_cndmask_b32_e64 v69, v50, v70, s[12:13]
	v_cndmask_b32_e64 v51, v57, v63, s[12:13]
	v_cndmask_b32_e64 v56, v56, v62, s[12:13]
	v_cndmask_b32_e64 v50, v55, v65, s[12:13]
	v_cndmask_b32_e64 v54, v54, v64, s[12:13]
	v_cvt_pk_bf16_f32 v50, v54, v50
	v_cvt_pk_bf16_f32 v51, v56, v51
	v_cvt_pk_bf16_f32 v52, v69, v52
	v_cvt_pk_bf16_f32 v53, v68, v53
	v_lshl_add_u64 v[54:55], v[58:59], 0, v[0:1]
	v_mov_b32_e32 v62, v78
	global_store_dwordx4 v[54:55], v[50:53], off offset:256 nt
	s_and_b64 vcc, exec, s[20:21]
	s_cbranch_vccnz .LBB0_502

; __device__ __forceinline__ u32x4 pack8(f32x4 a, f32x4 b) { u32x4 w; w.x = pk2(a[0], a[1]); w.y = pk2(a[2], a[3]); w.z = pk2(b[0], b[1]); w.w = pk2(b[2], b[3]); return w; }
; __device__ __forceinline__ float sq8(const f32x4& a, const f32x4& b) { return ((a[0] * a[0] + a[1] * a[1]) + (a[2] * a[2] + a[3] * a[3])) + ((b[0] * b[0] + b[1] * b[1]) + (b[2] * b[2] + b[3] * b[3])); }
; __device__ __forceinline__ f32x2 rtab_get(LAS unsigned char* lds, int ui, int r) { return ((const LAS f32x2*)(lds + RTAB_OFF))[(ui & 1) * 256 + r]; }
;     __device__ __forceinline__ void operator()(const f32x4 (&acc)[2][2][4][2], const Unit& u, int ui, int wr, int wc, int fr, int fq, LAS unsigned char* lds) const {
;     ...
;                 const int rr = ai * 128 + wr * 64 + m * 16 + fr, row = u.pm * 256 + rr; const float rs = rtab_get(lds, ui, rr)[0];
;                 float sq = 0.f;
; #pragma unroll
;                 for (int bj = 0; bj < 2; ++bj) {
;                     const int c = bj * 128 + wc * 32 + fq * 8;
;                     f32x4 v0 = acc[ai][bj][m][0] * rs, v1 = acc[ai][bj][m][1] * rs;
;                     if (pn < 6) { if (pn < 2) { v0 = v0 * QS_SB; v1 = v1 * QS_SB; } *(u32x4*)(QKV + (size_t)row * 1536 + pn * 256 + c) = pack8(v0, v1); }
;                     else if (pn == 6) { *(u32x4*)(CKV + (size_t)row * 256 + c) = pack8(v0, v1); sq += sq8(v0, v1); }
;                     else if (pn == 7) { *(u32x4*)(CQ + (size_t)row * 384 + c) = pack8(v0, v1); sq += sq8(v0, v1); }
;                     else if (bj == 0) { *(u32x4*)(CQ + (size_t)row * 384 + 256 + c) = pack8(v0, v1); sq += sq8(v0, v1); }
.LBB0_502:
	ds_read_b32 v56, v150 offset:1152
	v_add_u32_e32 v50, 0x90, v138
	v_ashrrev_i32_e32 v51, 31, v50
	v_mad_i64_i32 v[54:55], s[6:7], v50, s59, 0
	v_lshlrev_b64 v[52:53], 9, v[50:51]
	s_waitcnt lgkmcnt(0)
	v_pk_mul_f32 v[48:49], v[48:49], v[56:57] op_sel_hi:[1,0]
	v_pk_mul_f32 v[46:47], v[46:47], v[56:57] op_sel_hi:[1,0]
	v_pk_mul_f32 v[60:61], v[44:45], v[56:57] op_sel_hi:[1,0]
	v_pk_mul_f32 v[58:59], v[42:43], v[56:57] op_sel_hi:[1,0]
	s_and_b64 vcc, exec, s[18:19]
	s_mov_b64 s[64:65], -1
	s_cbranch_vccnz .LBB0_512
	v_cvt_pk_bf16_f32 v42, v46, v47
	v_cvt_pk_bf16_f32 v43, v48, v49
	v_cvt_pk_bf16_f32 v44, v58, v59
	v_cvt_pk_bf16_f32 v45, v60, v61
	s_cmp_lt_i32 s26, 7
	s_cbranch_scc1 .LBB0_509
	s_cmp_lg_u32 s26, 7
	s_cbranch_scc0 .LBB0_506
	v_lshl_add_u64 v[62:63], s[40:41], 0, v[54:55]
	v_lshl_add_u64 v[62:63], v[62:63], 0, v[0:1]
	v_mov_b32_e32 v64, v47
	v_mov_b32_e32 v65, v59
	global_store_dwordx4 v[62:63], v[42:45], off offset:512 nt
	v_mov_b32_e32 v62, v46
	v_mov_b32_e32 v63, v58
	v_pk_mul_f32 v[64:65], v[64:65], v[64:65]
	v_mov_b32_e32 v66, v49
	v_mov_b32_e32 v67, v61
	v_pk_fma_f32 v[62:63], v[62:63], v[62:63], v[64:65]
	v_mov_b32_e32 v64, v48
	v_mov_b32_e32 v65, v60
	v_pk_mul_f32 v[66:67], v[66:67], v[66:67]
	s_mov_b64 s[64:65], 0
	v_pk_fma_f32 v[64:65], v[64:65], v[64:65], v[66:67]
	s_nop 0
	v_pk_add_f32 v[62:63], v[62:63], v[64:65]
	s_nop 0
	v_add_f32_e32 v62, v62, v63
.LBB0_506:
	s_andn2_b64 vcc, exec, s[64:65]
	s_cbranch_vccnz .LBB0_508
	v_lshl_add_u64 v[62:63], s[40:41], 0, v[54:55]
	v_lshl_add_u64 v[62:63], v[62:63], 0, v[0:1]
	v_mov_b32_e32 v64, v47
	v_mov_b32_e32 v65, v59
	global_store_dwordx4 v[62:63], v[42:45], off nt
	v_mov_b32_e32 v62, v46
	v_mov_b32_e32 v63, v58
	v_pk_mul_f32 v[64:65], v[64:65], v[64:65]
	v_mov_b32_e32 v66, v49
	v_mov_b32_e32 v67, v61
	v_pk_fma_f32 v[62:63], v[62:63], v[62:63], v[64:65]
	v_mov_b32_e32 v64, v48
	v_mov_b32_e32 v65, v60
	v_pk_mul_f32 v[66:67], v[66:67], v[66:67]
	s_nop 0
	v_pk_fma_f32 v[64:65], v[64:65], v[64:65], v[66:67]
	s_nop 0
	v_pk_add_f32 v[62:63], v[62:63], v[64:65]
	s_nop 0
	v_add_f32_e32 v62, v62, v63

; __device__ __forceinline__ u32x4 pack8(f32x4 a, f32x4 b) { u32x4 w; w.x = pk2(a[0], a[1]); w.y = pk2(a[2], a[3]); w.z = pk2(b[0], b[1]); w.w = pk2(b[2], b[3]); return w; }
; __device__ __forceinline__ float sq8(const f32x4& a, const f32x4& b) { return ((a[0] * a[0] + a[1] * a[1]) + (a[2] * a[2] + a[3] * a[3])) + ((b[0] * b[0] + b[1] * b[1]) + (b[2] * b[2] + b[3] * b[3])); }
;     __device__ __forceinline__ void operator()(const f32x4 (&acc)[2][2][4][2], const Unit& u, int ui, int wr, int wc, int fr, int fq, LAS unsigned char* lds) const {
;     ...
;                 for (int bj = 0; bj < 2; ++bj) {
;                     const int c = bj * 128 + wc * 32 + fq * 8;
;                     f32x4 v0 = acc[ai][bj][m][0] * rs, v1 = acc[ai][bj][m][1] * rs;
;                     if (pn < 6) { if (pn < 2) { v0 = v0 * QS_SB; v1 = v1 * QS_SB; } *(u32x4*)(QKV + (size_t)row * 1536 + pn * 256 + c) = pack8(v0, v1); }
;                     else if (pn == 6) { *(u32x4*)(CKV + (size_t)row * 256 + c) = pack8(v0, v1); sq += sq8(v0, v1); }
.LBB0_509:
	s_andn2_b64 vcc, exec, s[64:65]
	s_cbranch_vccnz .LBB0_511
	v_lshl_add_u64 v[62:63], s[38:39], 0, v[52:53]
	v_lshl_add_u64 v[62:63], v[62:63], 0, v[0:1]
	global_store_dwordx4 v[62:63], v[42:45], off nt
	v_mov_b32_e32 v62, v49
	v_mov_b32_e32 v63, v61
	v_mov_b32_e32 v44, v47
	v_mov_b32_e32 v45, v59
	v_mov_b32_e32 v42, v46
	v_mov_b32_e32 v43, v58
	v_pk_mul_f32 v[44:45], v[44:45], v[44:45]
	v_pk_mul_f32 v[62:63], v[62:63], v[62:63]
	v_pk_fma_f32 v[42:43], v[42:43], v[42:43], v[44:45]
	v_mov_b32_e32 v44, v48
	v_mov_b32_e32 v45, v60
	v_pk_fma_f32 v[44:45], v[44:45], v[44:45], v[62:63]
	s_nop 0
	v_pk_add_f32 v[42:43], v[42:43], v[44:45]
	s_nop 0
	v_add_f32_e32 v62, v42, v43

; __device__ __forceinline__ u32x4 pack8(f32x4 a, f32x4 b) { u32x4 w; w.x = pk2(a[0], a[1]); w.y = pk2(a[2], a[3]); w.z = pk2(b[0], b[1]); w.w = pk2(b[2], b[3]); return w; }
;     __device__ __forceinline__ void operator()(const f32x4 (&acc)[2][2][4][2], const Unit& u, int ui, int wr, int wc, int fr, int fq, LAS unsigned char* lds) const {
;     ...
;                 for (int bj = 0; bj < 2; ++bj) {
;                     const int c = bj * 128 + wc * 32 + fq * 8;
;                     f32x4 v0 = acc[ai][bj][m][0] * rs, v1 = acc[ai][bj][m][1] * rs;
;                     if (pn < 6) { if (pn < 2) { v0 = v0 * QS_SB; v1 = v1 * QS_SB; } *(u32x4*)(QKV + (size_t)row * 1536 + pn * 256 + c) = pack8(v0, v1); }
.LBB0_512:
	v_mad_i64_i32 v[42:43], s[6:7], v50, s3, 0
	v_lshl_add_u64 v[42:43], s[36:37], 0, v[42:43]
	s_and_b64 vcc, exec, s[64:65]
	v_lshl_add_u64 v[42:43], s[62:63], 1, v[42:43]
	s_cbranch_vccz .LBB0_514
	v_pk_mul_f32 v[44:45], v[48:49], s[96:97] op_sel_hi:[1,0]
	v_pk_mul_f32 v[62:63], v[46:47], s[96:97] op_sel_hi:[1,0]
	v_pk_mul_f32 v[64:65], v[60:61], s[96:97] op_sel_hi:[1,0]
	v_pk_mul_f32 v[66:67], v[58:59], s[96:97] op_sel_hi:[1,0]
	v_cndmask_b32_e64 v57, v61, v65, s[12:13]
	v_cndmask_b32_e64 v60, v60, v64, s[12:13]
	v_cndmask_b32_e64 v59, v59, v67, s[12:13]
	v_cndmask_b32_e64 v58, v58, v66, s[12:13]
	v_cndmask_b32_e64 v45, v49, v45, s[12:13]
	v_cndmask_b32_e64 v48, v48, v44, s[12:13]
	v_cndmask_b32_e64 v44, v47, v63, s[12:13]
	v_cndmask_b32_e64 v46, v46, v62, s[12:13]
	v_cvt_pk_bf16_f32 v44, v46, v44
	v_cvt_pk_bf16_f32 v45, v48, v45
	v_cvt_pk_bf16_f32 v46, v58, v59
	v_cvt_pk_bf16_f32 v47, v60, v57
	v_lshl_add_u64 v[48:49], v[42:43], 0, v[0:1]
	v_mov_b32_e32 v62, 0
	global_store_dwordx4 v[48:49], v[44:47], off nt

; __device__ __forceinline__ float xor32(float x) { auto rr = __builtin_amdgcn_permlane32_swap(__float_as_uint(x), __float_as_uint(x), false, false); return __uint_as_float(((unsigned)(threadIdx.x & 32)) ? rr[0] : rr[1]); }
; __device__ __forceinline__ u32x4 pack8(f32x4 a, f32x4 b) { u32x4 w; w.x = pk2(a[0], a[1]); w.y = pk2(a[2], a[3]); w.z = pk2(b[0], b[1]); w.w = pk2(b[2], b[3]); return w; }
;     __device__ __forceinline__ void operator()(const f32x4 (&acc)[2][2][4][2], const Unit& u, int ui, int wr, int wc, int fr, int fq, LAS unsigned char* lds) const {
;     ...
;                     else if (wc == 0) {
;                         const int ib = 8 * (fq & 1);
;                         const f32x4 c0 = *(const f32x4*)(COS + (size_t)row * 16 + ib), c1 = *(const f32x4*)(COS + (size_t)row * 16 + ib + 4);
;                         const f32x4 s0 = *(const f32x4*)(SIN + (size_t)row * 16 + ib), s1 = *(const f32x4*)(SIN + (size_t)row * 16 + ib + 4);
;                         f32x4 p0, p1;
; #pragma unroll
;                         for (int i = 0; i < 4; ++i) { p0[i] = xor32(v0[i]); p1[i] = xor32(v1[i]); }
;                         const float sg = (fq < 2) ? -1.f : 1.f;
;                         const f32x4 o0 = v0 * c0 + p0 * s0 * sg, o1 = v1 * c1 + p1 * s1 * sg;
;                         *(u32x4*)(KR + (size_t)row * 32 + fq * 8) = pack8(o0, o1);
.LBB0_517:
	s_cmp_lt_i32 s26, 7
	s_cbranch_scc1 .LBB0_525
	s_cmp_lg_u32 s26, 7
	s_cbranch_scc0 .LBB0_522
	s_andn2_b64 vcc, exec, s[56:57]
	s_cbranch_vccnz .LBB0_521
	v_lshlrev_b64 v[64:65], 2, v[44:45]
	v_lshl_add_u64 v[46:47], s[44:45], 0, v[64:65]
	v_lshlrev_b32_e32 v66, 2, v128
	v_mov_b32_e32 v67, v1
	v_lshl_add_u64 v[64:65], s[46:47], 0, v[64:65]
	v_lshl_add_u64 v[56:57], v[46:47], 0, v[66:67]
	v_lshl_add_u64 v[68:69], v[64:65], 0, v[66:67]
	s_waitcnt vmcnt(10)
	v_mov_b32_e32 v46, v174
	v_mov_b32_e32 v47, v175
	v_mov_b32_e32 v48, v176
	v_mov_b32_e32 v49, v177
	v_mov_b32_e32 v56, v178
	v_mov_b32_e32 v57, v179
	v_mov_b32_e32 v58, v180
	v_mov_b32_e32 v59, v181
	v_mov_b32_e32 v64, v182
	v_mov_b32_e32 v65, v183
	v_mov_b32_e32 v66, v184
	v_mov_b32_e32 v67, v185
	v_mov_b32_e32 v68, v230
	v_mov_b32_e32 v69, v231
	v_mov_b32_e32 v70, v232
	v_mov_b32_e32 v71, v233
	global_load_dwordx4 v[174:177], v[206:207], off offset:3072
	global_load_dwordx4 v[178:181], v[206:207], off offset:3088
	global_load_dwordx4 v[182:185], v[208:209], off offset:3072
	global_load_dwordx4 v[230:233], v[208:209], off offset:3088
	v_mov_b32_e32 v63, v38
	v_mov_b32_e32 v72, v38
	s_nop 1
	v_permlane32_swap_b32_e32 v63, v72
	v_cndmask_b32_e64 v72, v63, v72, s[4:5]
	v_mov_b32_e32 v63, v34
	v_mov_b32_e32 v73, v34
	s_nop 1
	v_permlane32_swap_b32_e32 v63, v73
	v_cndmask_b32_e64 v74, v63, v73, s[4:5]
	v_mov_b32_e32 v63, v39
	v_mov_b32_e32 v73, v39
	s_nop 1
	v_permlane32_swap_b32_e32 v63, v73
	v_cndmask_b32_e64 v73, v63, v73, s[4:5]
	v_mov_b32_e32 v63, v35
	v_mov_b32_e32 v75, v35
	s_nop 1
	v_permlane32_swap_b32_e32 v63, v75
	v_cndmask_b32_e64 v75, v63, v75, s[4:5]
	v_mov_b32_e32 v63, v40
	v_mov_b32_e32 v76, v40
	s_nop 1
	v_permlane32_swap_b32_e32 v63, v76
	v_cndmask_b32_e64 v76, v63, v76, s[4:5]
	v_mov_b32_e32 v63, v36
	v_mov_b32_e32 v77, v36
	s_nop 1
	v_permlane32_swap_b32_e32 v63, v77
	v_cndmask_b32_e64 v78, v63, v77, s[4:5]
	v_mov_b32_e32 v63, v41
	v_mov_b32_e32 v77, v41
	s_nop 1
	v_permlane32_swap_b32_e32 v63, v77
	v_cndmask_b32_e64 v77, v63, v77, s[4:5]
	v_mov_b32_e32 v63, v37
	v_mov_b32_e32 v79, v37
	s_nop 1
	v_permlane32_swap_b32_e32 v63, v79
	v_cndmask_b32_e64 v79, v63, v79, s[4:5]
	v_lshlrev_b64 v[60:61], 6, v[50:51]
	s_waitcnt lgkmcnt(0)
	v_pk_mul_f32 v[66:67], v[66:67], v[76:77]
	v_pk_mul_f32 v[64:65], v[64:65], v[72:73]
	v_mov_b32_e32 v72, v114
	v_mov_b32_e32 v73, v114
	v_pk_mul_f32 v[64:65], v[114:115], v[64:65]
	v_pk_mul_f32 v[66:67], v[72:73], v[66:67]
	v_pk_fma_f32 v[46:47], v[38:39], v[46:47], v[64:65]
	v_pk_fma_f32 v[48:49], v[40:41], v[48:49], v[66:67]
	v_pk_mul_f32 v[64:65], v[70:71], v[78:79]
	v_pk_mul_f32 v[66:67], v[68:69], v[74:75]
	v_pk_mul_f32 v[64:65], v[72:73], v[64:65]
	v_pk_mul_f32 v[66:67], v[114:115], v[66:67]
	v_pk_fma_f32 v[58:59], v[36:37], v[58:59], v[64:65]
	v_pk_fma_f32 v[56:57], v[34:35], v[56:57], v[66:67]
	v_cvt_pk_bf16_f32 v46, v46, v47
	v_cvt_pk_bf16_f32 v47, v48, v49
	v_cvt_pk_bf16_f32 v48, v56, v57
	v_cvt_pk_bf16_f32 v49, v58, v59
	v_lshl_add_u64 v[56:57], s[42:43], 0, v[60:61]
	v_lshlrev_b32_e32 v58, 1, v149
	v_mov_b32_e32 v59, v1
	v_lshl_add_u64 v[56:57], v[56:57], 0, v[58:59]
	global_store_dwordx4 v[56:57], v[46:49], off nt

; __device__ __forceinline__ u32x4 pack8(f32x4 a, f32x4 b) { u32x4 w; w.x = pk2(a[0], a[1]); w.y = pk2(a[2], a[3]); w.z = pk2(b[0], b[1]); w.w = pk2(b[2], b[3]); return w; }
; __device__ __forceinline__ float sq8(const f32x4& a, const f32x4& b) { return ((a[0] * a[0] + a[1] * a[1]) + (a[2] * a[2] + a[3] * a[3])) + ((b[0] * b[0] + b[1] * b[1]) + (b[2] * b[2] + b[3] * b[3])); }
;     __device__ __forceinline__ void operator()(const f32x4 (&acc)[2][2][4][2], const Unit& u, int ui, int wr, int wc, int fr, int fq, LAS unsigned char* lds) const {
;     ...
;                 for (int bj = 0; bj < 2; ++bj) {
;                     const int c = bj * 128 + wc * 32 + fq * 8;
;                     f32x4 v0 = acc[ai][bj][m][0] * rs, v1 = acc[ai][bj][m][1] * rs;
;                     if (pn < 6) { if (pn < 2) { v0 = v0 * QS_SB; v1 = v1 * QS_SB; } *(u32x4*)(QKV + (size_t)row * 1536 + pn * 256 + c) = pack8(v0, v1); }
;                     else if (pn == 6) { *(u32x4*)(CKV + (size_t)row * 256 + c) = pack8(v0, v1); sq += sq8(v0, v1); }
;                     else if (pn == 7) { *(u32x4*)(CQ + (size_t)row * 384 + c) = pack8(v0, v1); sq += sq8(v0, v1); }
.LBB0_522:
	s_andn2_b64 vcc, exec, s[64:65]
	v_mov_b32_e32 v46, v62
	s_cbranch_vccnz .LBB0_524
	v_lshl_add_u64 v[54:55], s[40:41], 0, v[54:55]
	v_cvt_pk_bf16_f32 v46, v38, v39
	v_cvt_pk_bf16_f32 v47, v40, v41
	v_cvt_pk_bf16_f32 v48, v34, v35
	v_cvt_pk_bf16_f32 v49, v36, v37
	v_lshl_add_u64 v[54:55], v[54:55], 0, v[0:1]
	global_store_dwordx4 v[54:55], v[46:49], off offset:256 nt
	v_mov_b32_e32 v54, v41
	v_mov_b32_e32 v55, v37
	v_mov_b32_e32 v48, v39
	v_mov_b32_e32 v49, v35
	v_mov_b32_e32 v46, v38
	v_mov_b32_e32 v47, v34
	v_pk_mul_f32 v[48:49], v[48:49], v[48:49]
	v_pk_mul_f32 v[54:55], v[54:55], v[54:55]
	v_pk_fma_f32 v[46:47], v[46:47], v[46:47], v[48:49]
	v_mov_b32_e32 v48, v40
	v_mov_b32_e32 v49, v36
	v_pk_fma_f32 v[48:49], v[48:49], v[48:49], v[54:55]
	s_nop 0
	v_pk_add_f32 v[46:47], v[46:47], v[48:49]
	s_nop 0
	v_add_f32_e32 v46, v46, v47
	v_add_f32_e32 v46, v46, v62

; __device__ __forceinline__ u32x4 pack8(f32x4 a, f32x4 b) { u32x4 w; w.x = pk2(a[0], a[1]); w.y = pk2(a[2], a[3]); w.z = pk2(b[0], b[1]); w.w = pk2(b[2], b[3]); return w; }
; __device__ __forceinline__ float sq8(const f32x4& a, const f32x4& b) { return ((a[0] * a[0] + a[1] * a[1]) + (a[2] * a[2] + a[3] * a[3])) + ((b[0] * b[0] + b[1] * b[1]) + (b[2] * b[2] + b[3] * b[3])); }
;     __device__ __forceinline__ void operator()(const f32x4 (&acc)[2][2][4][2], const Unit& u, int ui, int wr, int wc, int fr, int fq, LAS unsigned char* lds) const {
;     ...
;                 for (int bj = 0; bj < 2; ++bj) {
;                     const int c = bj * 128 + wc * 32 + fq * 8;
;                     f32x4 v0 = acc[ai][bj][m][0] * rs, v1 = acc[ai][bj][m][1] * rs;
;                     if (pn < 6) { if (pn < 2) { v0 = v0 * QS_SB; v1 = v1 * QS_SB; } *(u32x4*)(QKV + (size_t)row * 1536 + pn * 256 + c) = pack8(v0, v1); }
;                     else if (pn == 6) { *(u32x4*)(CKV + (size_t)row * 256 + c) = pack8(v0, v1); sq += sq8(v0, v1); }
.LBB0_525:
	s_andn2_b64 vcc, exec, s[64:65]
	s_cbranch_vccnz .LBB0_527
	v_lshl_add_u64 v[52:53], s[38:39], 0, v[52:53]
	v_cvt_pk_bf16_f32 v46, v38, v39
	v_cvt_pk_bf16_f32 v47, v40, v41
	v_cvt_pk_bf16_f32 v48, v34, v35
	v_cvt_pk_bf16_f32 v49, v36, v37
	v_lshl_add_u64 v[52:53], v[52:53], 0, v[0:1]
	global_store_dwordx4 v[52:53], v[46:49], off offset:256 nt
	v_mov_b32_e32 v52, v41
	v_mov_b32_e32 v53, v37
	v_mov_b32_e32 v48, v39
	v_mov_b32_e32 v49, v35
	v_mov_b32_e32 v46, v38
	v_mov_b32_e32 v47, v34
	v_pk_mul_f32 v[48:49], v[48:49], v[48:49]
	v_pk_mul_f32 v[52:53], v[52:53], v[52:53]
	v_pk_fma_f32 v[46:47], v[46:47], v[46:47], v[48:49]
	v_mov_b32_e32 v48, v40
	v_mov_b32_e32 v49, v36
	v_pk_fma_f32 v[48:49], v[48:49], v[48:49], v[52:53]
	s_nop 0
	v_pk_add_f32 v[46:47], v[46:47], v[48:49]
	s_nop 0
	v_add_f32_e32 v46, v46, v47
	v_add_f32_e32 v46, v46, v62

; __device__ __forceinline__ u32x4 pack8(f32x4 a, f32x4 b) { u32x4 w; w.x = pk2(a[0], a[1]); w.y = pk2(a[2], a[3]); w.z = pk2(b[0], b[1]); w.w = pk2(b[2], b[3]); return w; }
;     __device__ __forceinline__ void operator()(const f32x4 (&acc)[2][2][4][2], const Unit& u, int ui, int wr, int wc, int fr, int fq, LAS unsigned char* lds) const {
;     ...
;                 for (int bj = 0; bj < 2; ++bj) {
;                     const int c = bj * 128 + wc * 32 + fq * 8;
;                     f32x4 v0 = acc[ai][bj][m][0] * rs, v1 = acc[ai][bj][m][1] * rs;
;                     if (pn < 6) { if (pn < 2) { v0 = v0 * QS_SB; v1 = v1 * QS_SB; } *(u32x4*)(QKV + (size_t)row * 1536 + pn * 256 + c) = pack8(v0, v1); }
.LBB0_528:
	v_pk_mul_f32 v[46:47], v[40:41], s[96:97] op_sel_hi:[1,0]
	v_pk_mul_f32 v[48:49], v[38:39], s[96:97] op_sel_hi:[1,0]
	v_pk_mul_f32 v[52:53], v[36:37], s[96:97] op_sel_hi:[1,0]
	v_pk_mul_f32 v[54:55], v[34:35], s[96:97] op_sel_hi:[1,0]
	v_cndmask_b32_e64 v37, v37, v53, s[12:13]
	v_cndmask_b32_e64 v52, v36, v52, s[12:13]
	v_cndmask_b32_e64 v36, v35, v55, s[12:13]
	v_cndmask_b32_e64 v53, v34, v54, s[12:13]
	v_cndmask_b32_e64 v35, v41, v47, s[12:13]
	v_cndmask_b32_e64 v40, v40, v46, s[12:13]
	v_cndmask_b32_e64 v34, v39, v49, s[12:13]
	v_cndmask_b32_e64 v38, v38, v48, s[12:13]
	v_cvt_pk_bf16_f32 v34, v38, v34
	v_cvt_pk_bf16_f32 v35, v40, v35
	v_cvt_pk_bf16_f32 v36, v53, v36
	v_cvt_pk_bf16_f32 v37, v52, v37
	v_lshl_add_u64 v[38:39], v[42:43], 0, v[0:1]
	v_mov_b32_e32 v46, v62
	global_store_dwordx4 v[38:39], v[34:37], off offset:256 nt
	s_and_b64 vcc, exec, s[20:21]
	s_cbranch_vccnz .LBB0_532

; __device__ __forceinline__ u32x4 pack8(f32x4 a, f32x4 b) { u32x4 w; w.x = pk2(a[0], a[1]); w.y = pk2(a[2], a[3]); w.z = pk2(b[0], b[1]); w.w = pk2(b[2], b[3]); return w; }
; __device__ __forceinline__ float sq8(const f32x4& a, const f32x4& b) { return ((a[0] * a[0] + a[1] * a[1]) + (a[2] * a[2] + a[3] * a[3])) + ((b[0] * b[0] + b[1] * b[1]) + (b[2] * b[2] + b[3] * b[3])); }
; __device__ __forceinline__ f32x2 rtab_get(LAS unsigned char* lds, int ui, int r) { return ((const LAS f32x2*)(lds + RTAB_OFF))[(ui & 1) * 256 + r]; }
;     __device__ __forceinline__ void operator()(const f32x4 (&acc)[2][2][4][2], const Unit& u, int ui, int wr, int wc, int fr, int fq, LAS unsigned char* lds) const {
;     ...
;                 const int rr = ai * 128 + wr * 64 + m * 16 + fr, row = u.pm * 256 + rr; const float rs = rtab_get(lds, ui, rr)[0];
;                 float sq = 0.f;
; #pragma unroll
;                 for (int bj = 0; bj < 2; ++bj) {
;                     const int c = bj * 128 + wc * 32 + fq * 8;
;                     f32x4 v0 = acc[ai][bj][m][0] * rs, v1 = acc[ai][bj][m][1] * rs;
;                     if (pn < 6) { if (pn < 2) { v0 = v0 * QS_SB; v1 = v1 * QS_SB; } *(u32x4*)(QKV + (size_t)row * 1536 + pn * 256 + c) = pack8(v0, v1); }
;                     else if (pn == 6) { *(u32x4*)(CKV + (size_t)row * 256 + c) = pack8(v0, v1); sq += sq8(v0, v1); }
;                     else if (pn == 7) { *(u32x4*)(CQ + (size_t)row * 384 + c) = pack8(v0, v1); sq += sq8(v0, v1); }
;                     else if (bj == 0) { *(u32x4*)(CQ + (size_t)row * 384 + 256 + c) = pack8(v0, v1); sq += sq8(v0, v1); }
.LBB0_532:
	ds_read_b32 v40, v150 offset:1280
	v_add_u32_e32 v34, 0xa0, v138
	v_ashrrev_i32_e32 v35, 31, v34
	v_mad_i64_i32 v[38:39], s[6:7], v34, s59, 0
	v_lshlrev_b64 v[36:37], 9, v[34:35]
	s_waitcnt lgkmcnt(0)
	v_pk_mul_f32 v[32:33], v[32:33], v[40:41] op_sel_hi:[1,0]
	v_pk_mul_f32 v[30:31], v[30:31], v[40:41] op_sel_hi:[1,0]
	v_pk_mul_f32 v[44:45], v[28:29], v[40:41] op_sel_hi:[1,0]
	v_pk_mul_f32 v[42:43], v[26:27], v[40:41] op_sel_hi:[1,0]
	s_and_b64 vcc, exec, s[18:19]
	s_mov_b64 s[64:65], -1
	s_cbranch_vccnz .LBB0_542
	v_cvt_pk_bf16_f32 v26, v30, v31
	v_cvt_pk_bf16_f32 v27, v32, v33
	v_cvt_pk_bf16_f32 v28, v42, v43
	v_cvt_pk_bf16_f32 v29, v44, v45
	s_cmp_lt_i32 s26, 7
	s_cbranch_scc1 .LBB0_539
	s_cmp_lg_u32 s26, 7
	s_cbranch_scc0 .LBB0_536
	v_lshl_add_u64 v[46:47], s[40:41], 0, v[38:39]
	v_lshl_add_u64 v[46:47], v[46:47], 0, v[0:1]
	v_mov_b32_e32 v48, v31
	v_mov_b32_e32 v49, v43
	global_store_dwordx4 v[46:47], v[26:29], off offset:512 nt
	v_mov_b32_e32 v46, v30
	v_mov_b32_e32 v47, v42
	v_pk_mul_f32 v[48:49], v[48:49], v[48:49]
	v_mov_b32_e32 v50, v33
	v_mov_b32_e32 v51, v45
	v_pk_fma_f32 v[46:47], v[46:47], v[46:47], v[48:49]
	v_mov_b32_e32 v48, v32
	v_mov_b32_e32 v49, v44
	v_pk_mul_f32 v[50:51], v[50:51], v[50:51]
	s_mov_b64 s[64:65], 0
	v_pk_fma_f32 v[48:49], v[48:49], v[48:49], v[50:51]
	s_nop 0
	v_pk_add_f32 v[46:47], v[46:47], v[48:49]
	s_nop 0
	v_add_f32_e32 v46, v46, v47
.LBB0_536:
	s_andn2_b64 vcc, exec, s[64:65]
	s_cbranch_vccnz .LBB0_538
	v_lshl_add_u64 v[46:47], s[40:41], 0, v[38:39]
	v_lshl_add_u64 v[46:47], v[46:47], 0, v[0:1]
	v_mov_b32_e32 v48, v31
	v_mov_b32_e32 v49, v43
	global_store_dwordx4 v[46:47], v[26:29], off nt
	v_mov_b32_e32 v46, v30
	v_mov_b32_e32 v47, v42
	v_pk_mul_f32 v[48:49], v[48:49], v[48:49]
	v_mov_b32_e32 v50, v33
	v_mov_b32_e32 v51, v45
	v_pk_fma_f32 v[46:47], v[46:47], v[46:47], v[48:49]
	v_mov_b32_e32 v48, v32
	v_mov_b32_e32 v49, v44
	v_pk_mul_f32 v[50:51], v[50:51], v[50:51]
	s_nop 0
	v_pk_fma_f32 v[48:49], v[48:49], v[48:49], v[50:51]
	s_nop 0
	v_pk_add_f32 v[46:47], v[46:47], v[48:49]
	s_nop 0
	v_add_f32_e32 v46, v46, v47

; __device__ __forceinline__ u32x4 pack8(f32x4 a, f32x4 b) { u32x4 w; w.x = pk2(a[0], a[1]); w.y = pk2(a[2], a[3]); w.z = pk2(b[0], b[1]); w.w = pk2(b[2], b[3]); return w; }
; __device__ __forceinline__ float sq8(const f32x4& a, const f32x4& b) { return ((a[0] * a[0] + a[1] * a[1]) + (a[2] * a[2] + a[3] * a[3])) + ((b[0] * b[0] + b[1] * b[1]) + (b[2] * b[2] + b[3] * b[3])); }
;     __device__ __forceinline__ void operator()(const f32x4 (&acc)[2][2][4][2], const Unit& u, int ui, int wr, int wc, int fr, int fq, LAS unsigned char* lds) const {
;     ...
;                 for (int bj = 0; bj < 2; ++bj) {
;                     const int c = bj * 128 + wc * 32 + fq * 8;
;                     f32x4 v0 = acc[ai][bj][m][0] * rs, v1 = acc[ai][bj][m][1] * rs;
;                     if (pn < 6) { if (pn < 2) { v0 = v0 * QS_SB; v1 = v1 * QS_SB; } *(u32x4*)(QKV + (size_t)row * 1536 + pn * 256 + c) = pack8(v0, v1); }
;                     else if (pn == 6) { *(u32x4*)(CKV + (size_t)row * 256 + c) = pack8(v0, v1); sq += sq8(v0, v1); }
.LBB0_539:
	s_andn2_b64 vcc, exec, s[64:65]
	s_cbranch_vccnz .LBB0_541
	v_lshl_add_u64 v[46:47], s[38:39], 0, v[36:37]
	v_lshl_add_u64 v[46:47], v[46:47], 0, v[0:1]
	global_store_dwordx4 v[46:47], v[26:29], off nt
	v_mov_b32_e32 v46, v33
	v_mov_b32_e32 v47, v45
	v_mov_b32_e32 v28, v31
	v_mov_b32_e32 v29, v43
	v_mov_b32_e32 v26, v30
	v_mov_b32_e32 v27, v42
	v_pk_mul_f32 v[28:29], v[28:29], v[28:29]
	v_pk_mul_f32 v[46:47], v[46:47], v[46:47]
	v_pk_fma_f32 v[26:27], v[26:27], v[26:27], v[28:29]
	v_mov_b32_e32 v28, v32
	v_mov_b32_e32 v29, v44
	v_pk_fma_f32 v[28:29], v[28:29], v[28:29], v[46:47]
	s_nop 0
	v_pk_add_f32 v[26:27], v[26:27], v[28:29]
	s_nop 0
	v_add_f32_e32 v46, v26, v27

; __device__ __forceinline__ u32x4 pack8(f32x4 a, f32x4 b) { u32x4 w; w.x = pk2(a[0], a[1]); w.y = pk2(a[2], a[3]); w.z = pk2(b[0], b[1]); w.w = pk2(b[2], b[3]); return w; }
;     __device__ __forceinline__ void operator()(const f32x4 (&acc)[2][2][4][2], const Unit& u, int ui, int wr, int wc, int fr, int fq, LAS unsigned char* lds) const {
;     ...
;                 for (int bj = 0; bj < 2; ++bj) {
;                     const int c = bj * 128 + wc * 32 + fq * 8;
;                     f32x4 v0 = acc[ai][bj][m][0] * rs, v1 = acc[ai][bj][m][1] * rs;
;                     if (pn < 6) { if (pn < 2) { v0 = v0 * QS_SB; v1 = v1 * QS_SB; } *(u32x4*)(QKV + (size_t)row * 1536 + pn * 256 + c) = pack8(v0, v1); }
.LBB0_542:
	v_mad_i64_i32 v[26:27], s[6:7], v34, s3, 0
	v_lshl_add_u64 v[26:27], s[36:37], 0, v[26:27]
	s_and_b64 vcc, exec, s[64:65]
	v_lshl_add_u64 v[26:27], s[62:63], 1, v[26:27]
	s_cbranch_vccz .LBB0_544
	v_pk_mul_f32 v[28:29], v[32:33], s[96:97] op_sel_hi:[1,0]
	v_pk_mul_f32 v[46:47], v[30:31], s[96:97] op_sel_hi:[1,0]
	v_pk_mul_f32 v[48:49], v[44:45], s[96:97] op_sel_hi:[1,0]
	v_pk_mul_f32 v[50:51], v[42:43], s[96:97] op_sel_hi:[1,0]
	v_cndmask_b32_e64 v41, v45, v49, s[12:13]
	v_cndmask_b32_e64 v44, v44, v48, s[12:13]
	v_cndmask_b32_e64 v43, v43, v51, s[12:13]
	v_cndmask_b32_e64 v42, v42, v50, s[12:13]
	v_cndmask_b32_e64 v29, v33, v29, s[12:13]
	v_cndmask_b32_e64 v32, v32, v28, s[12:13]
	v_cndmask_b32_e64 v28, v31, v47, s[12:13]
	v_cndmask_b32_e64 v30, v30, v46, s[12:13]
	v_cvt_pk_bf16_f32 v28, v30, v28
	v_cvt_pk_bf16_f32 v29, v32, v29
	v_cvt_pk_bf16_f32 v30, v42, v43
	v_cvt_pk_bf16_f32 v31, v44, v41
	v_lshl_add_u64 v[32:33], v[26:27], 0, v[0:1]
	v_mov_b32_e32 v46, 0
	global_store_dwordx4 v[32:33], v[28:31], off nt

; __device__ __forceinline__ float xor32(float x) { auto rr = __builtin_amdgcn_permlane32_swap(__float_as_uint(x), __float_as_uint(x), false, false); return __uint_as_float(((unsigned)(threadIdx.x & 32)) ? rr[0] : rr[1]); }
; __device__ __forceinline__ u32x4 pack8(f32x4 a, f32x4 b) { u32x4 w; w.x = pk2(a[0], a[1]); w.y = pk2(a[2], a[3]); w.z = pk2(b[0], b[1]); w.w = pk2(b[2], b[3]); return w; }
;     __device__ __forceinline__ void operator()(const f32x4 (&acc)[2][2][4][2], const Unit& u, int ui, int wr, int wc, int fr, int fq, LAS unsigned char* lds) const {
;     ...
;                     else if (wc == 0) {
;                         const int ib = 8 * (fq & 1);
;                         const f32x4 c0 = *(const f32x4*)(COS + (size_t)row * 16 + ib), c1 = *(const f32x4*)(COS + (size_t)row * 16 + ib + 4);
;                         const f32x4 s0 = *(const f32x4*)(SIN + (size_t)row * 16 + ib), s1 = *(const f32x4*)(SIN + (size_t)row * 16 + ib + 4);
;                         f32x4 p0, p1;
; #pragma unroll
;                         for (int i = 0; i < 4; ++i) { p0[i] = xor32(v0[i]); p1[i] = xor32(v1[i]); }
;                         const float sg = (fq < 2) ? -1.f : 1.f;
;                         const f32x4 o0 = v0 * c0 + p0 * s0 * sg, o1 = v1 * c1 + p1 * s1 * sg;
;                         *(u32x4*)(KR + (size_t)row * 32 + fq * 8) = pack8(o0, o1);
.LBB0_547:
	s_cmp_lt_i32 s26, 7
	s_cbranch_scc1 .LBB0_555
	s_cmp_lg_u32 s26, 7
	s_cbranch_scc0 .LBB0_552
	s_andn2_b64 vcc, exec, s[56:57]
	s_cbranch_vccnz .LBB0_551
	v_lshlrev_b64 v[48:49], 2, v[28:29]
	v_lshl_add_u64 v[30:31], s[44:45], 0, v[48:49]
	v_lshlrev_b32_e32 v50, 2, v128
	v_mov_b32_e32 v51, v1
	v_lshl_add_u64 v[48:49], s[46:47], 0, v[48:49]
	v_lshl_add_u64 v[40:41], v[30:31], 0, v[50:51]
	v_lshl_add_u64 v[52:53], v[48:49], 0, v[50:51]
	s_waitcnt vmcnt(10)
	v_mov_b32_e32 v30, v214
	v_mov_b32_e32 v31, v215
	v_mov_b32_e32 v32, v216
	v_mov_b32_e32 v33, v217
	v_mov_b32_e32 v40, v218
	v_mov_b32_e32 v41, v219
	v_mov_b32_e32 v42, v220
	v_mov_b32_e32 v43, v221
	v_mov_b32_e32 v48, v222
	v_mov_b32_e32 v49, v223
	v_mov_b32_e32 v50, v224
	v_mov_b32_e32 v51, v225
	v_mov_b32_e32 v52, v226
	v_mov_b32_e32 v53, v227
	v_mov_b32_e32 v54, v228
	v_mov_b32_e32 v55, v229
	v_mov_b32_e32 v47, v22
	v_mov_b32_e32 v56, v22
	s_nop 1
	v_permlane32_swap_b32_e32 v47, v56
	v_cndmask_b32_e64 v56, v47, v56, s[4:5]
	v_mov_b32_e32 v47, v18
	v_mov_b32_e32 v57, v18
	s_nop 1
	v_permlane32_swap_b32_e32 v47, v57
	v_cndmask_b32_e64 v58, v47, v57, s[4:5]
	v_mov_b32_e32 v47, v23
	v_mov_b32_e32 v57, v23
	s_nop 1
	v_permlane32_swap_b32_e32 v47, v57
	v_cndmask_b32_e64 v57, v47, v57, s[4:5]
	v_mov_b32_e32 v47, v19
	v_mov_b32_e32 v59, v19
	s_nop 1
	v_permlane32_swap_b32_e32 v47, v59
	v_cndmask_b32_e64 v59, v47, v59, s[4:5]
	v_mov_b32_e32 v47, v24
	v_mov_b32_e32 v60, v24
	s_nop 1
	v_permlane32_swap_b32_e32 v47, v60
	v_cndmask_b32_e64 v60, v47, v60, s[4:5]
	v_mov_b32_e32 v47, v20
	v_mov_b32_e32 v61, v20
	s_nop 1
	v_permlane32_swap_b32_e32 v47, v61
	v_cndmask_b32_e64 v62, v47, v61, s[4:5]
	v_mov_b32_e32 v47, v25
	v_mov_b32_e32 v61, v25
	s_nop 1
	v_permlane32_swap_b32_e32 v47, v61
	v_cndmask_b32_e64 v61, v47, v61, s[4:5]
	v_mov_b32_e32 v47, v21
	v_mov_b32_e32 v63, v21
	s_nop 1
	v_permlane32_swap_b32_e32 v47, v63
	v_cndmask_b32_e64 v63, v47, v63, s[4:5]
	v_lshlrev_b64 v[44:45], 6, v[34:35]
	s_waitcnt lgkmcnt(0)
	v_pk_mul_f32 v[50:51], v[50:51], v[60:61]
	v_pk_mul_f32 v[48:49], v[48:49], v[56:57]
	v_mov_b32_e32 v56, v114
	v_mov_b32_e32 v57, v114
	v_pk_mul_f32 v[48:49], v[114:115], v[48:49]
	v_pk_mul_f32 v[50:51], v[56:57], v[50:51]
	v_pk_fma_f32 v[30:31], v[22:23], v[30:31], v[48:49]
	v_pk_fma_f32 v[32:33], v[24:25], v[32:33], v[50:51]
	v_pk_mul_f32 v[48:49], v[54:55], v[62:63]
	v_pk_mul_f32 v[50:51], v[52:53], v[58:59]
	v_pk_mul_f32 v[48:49], v[56:57], v[48:49]
	v_pk_mul_f32 v[50:51], v[114:115], v[50:51]
	v_pk_fma_f32 v[42:43], v[20:21], v[42:43], v[48:49]
	v_pk_fma_f32 v[40:41], v[18:19], v[40:41], v[50:51]
	v_cvt_pk_bf16_f32 v30, v30, v31
	v_cvt_pk_bf16_f32 v31, v32, v33
	v_cvt_pk_bf16_f32 v32, v40, v41
	v_cvt_pk_bf16_f32 v33, v42, v43
	v_lshl_add_u64 v[40:41], s[42:43], 0, v[44:45]
	v_lshlrev_b32_e32 v42, 1, v149
	v_mov_b32_e32 v43, v1
	v_lshl_add_u64 v[40:41], v[40:41], 0, v[42:43]
	global_store_dwordx4 v[40:41], v[30:33], off nt

; __device__ __forceinline__ u32x4 pack8(f32x4 a, f32x4 b) { u32x4 w; w.x = pk2(a[0], a[1]); w.y = pk2(a[2], a[3]); w.z = pk2(b[0], b[1]); w.w = pk2(b[2], b[3]); return w; }
; __device__ __forceinline__ float sq8(const f32x4& a, const f32x4& b) { return ((a[0] * a[0] + a[1] * a[1]) + (a[2] * a[2] + a[3] * a[3])) + ((b[0] * b[0] + b[1] * b[1]) + (b[2] * b[2] + b[3] * b[3])); }
;     __device__ __forceinline__ void operator()(const f32x4 (&acc)[2][2][4][2], const Unit& u, int ui, int wr, int wc, int fr, int fq, LAS unsigned char* lds) const {
;     ...
;                 for (int bj = 0; bj < 2; ++bj) {
;                     const int c = bj * 128 + wc * 32 + fq * 8;
;                     f32x4 v0 = acc[ai][bj][m][0] * rs, v1 = acc[ai][bj][m][1] * rs;
;                     if (pn < 6) { if (pn < 2) { v0 = v0 * QS_SB; v1 = v1 * QS_SB; } *(u32x4*)(QKV + (size_t)row * 1536 + pn * 256 + c) = pack8(v0, v1); }
;                     else if (pn == 6) { *(u32x4*)(CKV + (size_t)row * 256 + c) = pack8(v0, v1); sq += sq8(v0, v1); }
;                     else if (pn == 7) { *(u32x4*)(CQ + (size_t)row * 384 + c) = pack8(v0, v1); sq += sq8(v0, v1); }
.LBB0_552:
	s_andn2_b64 vcc, exec, s[64:65]
	v_mov_b32_e32 v30, v46
	s_cbranch_vccnz .LBB0_554
	v_lshl_add_u64 v[38:39], s[40:41], 0, v[38:39]
	v_cvt_pk_bf16_f32 v30, v22, v23
	v_cvt_pk_bf16_f32 v31, v24, v25
	v_cvt_pk_bf16_f32 v32, v18, v19
	v_cvt_pk_bf16_f32 v33, v20, v21
	v_lshl_add_u64 v[38:39], v[38:39], 0, v[0:1]
	global_store_dwordx4 v[38:39], v[30:33], off offset:256 nt
	v_mov_b32_e32 v38, v25
	v_mov_b32_e32 v39, v21
	v_mov_b32_e32 v32, v23
	v_mov_b32_e32 v33, v19
	v_mov_b32_e32 v30, v22
	v_mov_b32_e32 v31, v18
	v_pk_mul_f32 v[32:33], v[32:33], v[32:33]
	v_pk_mul_f32 v[38:39], v[38:39], v[38:39]
	v_pk_fma_f32 v[30:31], v[30:31], v[30:31], v[32:33]
	v_mov_b32_e32 v32, v24
	v_mov_b32_e32 v33, v20
	v_pk_fma_f32 v[32:33], v[32:33], v[32:33], v[38:39]
	s_nop 0
	v_pk_add_f32 v[30:31], v[30:31], v[32:33]
	s_nop 0
	v_add_f32_e32 v30, v30, v31
	v_add_f32_e32 v30, v30, v46

; __device__ __forceinline__ u32x4 pack8(f32x4 a, f32x4 b) { u32x4 w; w.x = pk2(a[0], a[1]); w.y = pk2(a[2], a[3]); w.z = pk2(b[0], b[1]); w.w = pk2(b[2], b[3]); return w; }
; __device__ __forceinline__ float sq8(const f32x4& a, const f32x4& b) { return ((a[0] * a[0] + a[1] * a[1]) + (a[2] * a[2] + a[3] * a[3])) + ((b[0] * b[0] + b[1] * b[1]) + (b[2] * b[2] + b[3] * b[3])); }
;     __device__ __forceinline__ void operator()(const f32x4 (&acc)[2][2][4][2], const Unit& u, int ui, int wr, int wc, int fr, int fq, LAS unsigned char* lds) const {
;     ...
;                 for (int bj = 0; bj < 2; ++bj) {
;                     const int c = bj * 128 + wc * 32 + fq * 8;
;                     f32x4 v0 = acc[ai][bj][m][0] * rs, v1 = acc[ai][bj][m][1] * rs;
;                     if (pn < 6) { if (pn < 2) { v0 = v0 * QS_SB; v1 = v1 * QS_SB; } *(u32x4*)(QKV + (size_t)row * 1536 + pn * 256 + c) = pack8(v0, v1); }
;                     else if (pn == 6) { *(u32x4*)(CKV + (size_t)row * 256 + c) = pack8(v0, v1); sq += sq8(v0, v1); }
.LBB0_555:
	s_andn2_b64 vcc, exec, s[64:65]
	s_cbranch_vccnz .LBB0_557
	v_lshl_add_u64 v[36:37], s[38:39], 0, v[36:37]
	v_cvt_pk_bf16_f32 v30, v22, v23
	v_cvt_pk_bf16_f32 v31, v24, v25
	v_cvt_pk_bf16_f32 v32, v18, v19
	v_cvt_pk_bf16_f32 v33, v20, v21
	v_lshl_add_u64 v[36:37], v[36:37], 0, v[0:1]
	global_store_dwordx4 v[36:37], v[30:33], off offset:256 nt
	v_mov_b32_e32 v36, v25
	v_mov_b32_e32 v37, v21
	v_mov_b32_e32 v32, v23
	v_mov_b32_e32 v33, v19
	v_mov_b32_e32 v30, v22
	v_mov_b32_e32 v31, v18
	v_pk_mul_f32 v[32:33], v[32:33], v[32:33]
	v_pk_mul_f32 v[36:37], v[36:37], v[36:37]
	v_pk_fma_f32 v[30:31], v[30:31], v[30:31], v[32:33]
	v_mov_b32_e32 v32, v24
	v_mov_b32_e32 v33, v20
	v_pk_fma_f32 v[32:33], v[32:33], v[32:33], v[36:37]
	s_nop 0
	v_pk_add_f32 v[30:31], v[30:31], v[32:33]
	s_nop 0
	v_add_f32_e32 v30, v30, v31
	v_add_f32_e32 v30, v30, v46

; __device__ __forceinline__ u32x4 pack8(f32x4 a, f32x4 b) { u32x4 w; w.x = pk2(a[0], a[1]); w.y = pk2(a[2], a[3]); w.z = pk2(b[0], b[1]); w.w = pk2(b[2], b[3]); return w; }
;     __device__ __forceinline__ void operator()(const f32x4 (&acc)[2][2][4][2], const Unit& u, int ui, int wr, int wc, int fr, int fq, LAS unsigned char* lds) const {
;     ...
;                 for (int bj = 0; bj < 2; ++bj) {
;                     const int c = bj * 128 + wc * 32 + fq * 8;
;                     f32x4 v0 = acc[ai][bj][m][0] * rs, v1 = acc[ai][bj][m][1] * rs;
;                     if (pn < 6) { if (pn < 2) { v0 = v0 * QS_SB; v1 = v1 * QS_SB; } *(u32x4*)(QKV + (size_t)row * 1536 + pn * 256 + c) = pack8(v0, v1); }
.LBB0_558:
	v_pk_mul_f32 v[30:31], v[24:25], s[96:97] op_sel_hi:[1,0]
	v_pk_mul_f32 v[32:33], v[22:23], s[96:97] op_sel_hi:[1,0]
	v_pk_mul_f32 v[36:37], v[20:21], s[96:97] op_sel_hi:[1,0]
	v_pk_mul_f32 v[38:39], v[18:19], s[96:97] op_sel_hi:[1,0]
	v_cndmask_b32_e64 v21, v21, v37, s[12:13]
	v_cndmask_b32_e64 v36, v20, v36, s[12:13]
	v_cndmask_b32_e64 v20, v19, v39, s[12:13]
	v_cndmask_b32_e64 v37, v18, v38, s[12:13]
	v_cndmask_b32_e64 v19, v25, v31, s[12:13]
	v_cndmask_b32_e64 v24, v24, v30, s[12:13]
	v_cndmask_b32_e64 v18, v23, v33, s[12:13]
	v_cndmask_b32_e64 v22, v22, v32, s[12:13]
	v_cvt_pk_bf16_f32 v18, v22, v18
	v_cvt_pk_bf16_f32 v19, v24, v19
	v_cvt_pk_bf16_f32 v20, v37, v20
	v_cvt_pk_bf16_f32 v21, v36, v21
	v_lshl_add_u64 v[22:23], v[26:27], 0, v[0:1]
	v_mov_b32_e32 v30, v46
	global_store_dwordx4 v[22:23], v[18:21], off offset:256 nt
	s_and_b64 vcc, exec, s[20:21]
	s_cbranch_vccnz .LBB0_562

; __device__ __forceinline__ u32x4 pack8(f32x4 a, f32x4 b) { u32x4 w; w.x = pk2(a[0], a[1]); w.y = pk2(a[2], a[3]); w.z = pk2(b[0], b[1]); w.w = pk2(b[2], b[3]); return w; }
; __device__ __forceinline__ float sq8(const f32x4& a, const f32x4& b) { return ((a[0] * a[0] + a[1] * a[1]) + (a[2] * a[2] + a[3] * a[3])) + ((b[0] * b[0] + b[1] * b[1]) + (b[2] * b[2] + b[3] * b[3])); }
; __device__ __forceinline__ f32x2 rtab_get(LAS unsigned char* lds, int ui, int r) { return ((const LAS f32x2*)(lds + RTAB_OFF))[(ui & 1) * 256 + r]; }
;     __device__ __forceinline__ void operator()(const f32x4 (&acc)[2][2][4][2], const Unit& u, int ui, int wr, int wc, int fr, int fq, LAS unsigned char* lds) const {
;     ...
;                 const int rr = ai * 128 + wr * 64 + m * 16 + fr, row = u.pm * 256 + rr; const float rs = rtab_get(lds, ui, rr)[0];
;                 float sq = 0.f;
; #pragma unroll
;                 for (int bj = 0; bj < 2; ++bj) {
;                     const int c = bj * 128 + wc * 32 + fq * 8;
;                     f32x4 v0 = acc[ai][bj][m][0] * rs, v1 = acc[ai][bj][m][1] * rs;
;                     if (pn < 6) { if (pn < 2) { v0 = v0 * QS_SB; v1 = v1 * QS_SB; } *(u32x4*)(QKV + (size_t)row * 1536 + pn * 256 + c) = pack8(v0, v1); }
;                     else if (pn == 6) { *(u32x4*)(CKV + (size_t)row * 256 + c) = pack8(v0, v1); sq += sq8(v0, v1); }
;                     else if (pn == 7) { *(u32x4*)(CQ + (size_t)row * 384 + c) = pack8(v0, v1); sq += sq8(v0, v1); }
;                     else if (bj == 0) { *(u32x4*)(CQ + (size_t)row * 384 + 256 + c) = pack8(v0, v1); sq += sq8(v0, v1); }
.LBB0_562:
	ds_read_b32 v24, v150 offset:1408
	v_add_u32_e32 v18, 0xb0, v138
	v_ashrrev_i32_e32 v19, 31, v18
	v_mad_i64_i32 v[22:23], s[6:7], v18, s59, 0
	v_lshlrev_b64 v[20:21], 9, v[18:19]
	s_waitcnt lgkmcnt(0)
	v_pk_mul_f32 v[16:17], v[16:17], v[24:25] op_sel_hi:[1,0]
	v_pk_mul_f32 v[14:15], v[14:15], v[24:25] op_sel_hi:[1,0]
	v_pk_mul_f32 v[28:29], v[12:13], v[24:25] op_sel_hi:[1,0]
	v_pk_mul_f32 v[26:27], v[10:11], v[24:25] op_sel_hi:[1,0]
	s_and_b64 vcc, exec, s[18:19]
	s_mov_b64 s[64:65], -1
	s_cbranch_vccnz .LBB0_572
	v_cvt_pk_bf16_f32 v10, v14, v15
	v_cvt_pk_bf16_f32 v11, v16, v17
	v_cvt_pk_bf16_f32 v12, v26, v27
	v_cvt_pk_bf16_f32 v13, v28, v29
	s_cmp_lt_i32 s26, 7
	s_cbranch_scc1 .LBB0_569
	s_cmp_lg_u32 s26, 7
	s_cbranch_scc0 .LBB0_566
	v_lshl_add_u64 v[30:31], s[40:41], 0, v[22:23]
	v_lshl_add_u64 v[30:31], v[30:31], 0, v[0:1]
	v_mov_b32_e32 v32, v15
	v_mov_b32_e32 v33, v27
	global_store_dwordx4 v[30:31], v[10:13], off offset:512 nt
	v_mov_b32_e32 v30, v14
	v_mov_b32_e32 v31, v26
	v_pk_mul_f32 v[32:33], v[32:33], v[32:33]
	v_mov_b32_e32 v34, v17
	v_mov_b32_e32 v35, v29
	v_pk_fma_f32 v[30:31], v[30:31], v[30:31], v[32:33]
	v_mov_b32_e32 v32, v16
	v_mov_b32_e32 v33, v28
	v_pk_mul_f32 v[34:35], v[34:35], v[34:35]
	s_mov_b64 s[64:65], 0
	v_pk_fma_f32 v[32:33], v[32:33], v[32:33], v[34:35]
	s_nop 0
	v_pk_add_f32 v[30:31], v[30:31], v[32:33]
	s_nop 0
	v_add_f32_e32 v30, v30, v31
.LBB0_566:
	s_andn2_b64 vcc, exec, s[64:65]
	s_cbranch_vccnz .LBB0_568
	v_lshl_add_u64 v[30:31], s[40:41], 0, v[22:23]
	v_lshl_add_u64 v[30:31], v[30:31], 0, v[0:1]
	v_mov_b32_e32 v32, v15
	v_mov_b32_e32 v33, v27
	global_store_dwordx4 v[30:31], v[10:13], off nt
	v_mov_b32_e32 v30, v14
	v_mov_b32_e32 v31, v26
	v_pk_mul_f32 v[32:33], v[32:33], v[32:33]
	v_mov_b32_e32 v34, v17
	v_mov_b32_e32 v35, v29
	v_pk_fma_f32 v[30:31], v[30:31], v[30:31], v[32:33]
	v_mov_b32_e32 v32, v16
	v_mov_b32_e32 v33, v28
	v_pk_mul_f32 v[34:35], v[34:35], v[34:35]
	s_nop 0
	v_pk_fma_f32 v[32:33], v[32:33], v[32:33], v[34:35]
	s_nop 0
	v_pk_add_f32 v[30:31], v[30:31], v[32:33]
	s_nop 0
	v_add_f32_e32 v30, v30, v31

; __device__ __forceinline__ u32x4 pack8(f32x4 a, f32x4 b) { u32x4 w; w.x = pk2(a[0], a[1]); w.y = pk2(a[2], a[3]); w.z = pk2(b[0], b[1]); w.w = pk2(b[2], b[3]); return w; }
; __device__ __forceinline__ float sq8(const f32x4& a, const f32x4& b) { return ((a[0] * a[0] + a[1] * a[1]) + (a[2] * a[2] + a[3] * a[3])) + ((b[0] * b[0] + b[1] * b[1]) + (b[2] * b[2] + b[3] * b[3])); }
;     __device__ __forceinline__ void operator()(const f32x4 (&acc)[2][2][4][2], const Unit& u, int ui, int wr, int wc, int fr, int fq, LAS unsigned char* lds) const {
;     ...
;                 for (int bj = 0; bj < 2; ++bj) {
;                     const int c = bj * 128 + wc * 32 + fq * 8;
;                     f32x4 v0 = acc[ai][bj][m][0] * rs, v1 = acc[ai][bj][m][1] * rs;
;                     if (pn < 6) { if (pn < 2) { v0 = v0 * QS_SB; v1 = v1 * QS_SB; } *(u32x4*)(QKV + (size_t)row * 1536 + pn * 256 + c) = pack8(v0, v1); }
;                     else if (pn == 6) { *(u32x4*)(CKV + (size_t)row * 256 + c) = pack8(v0, v1); sq += sq8(v0, v1); }
.LBB0_569:
	s_andn2_b64 vcc, exec, s[64:65]
	s_cbranch_vccnz .LBB0_571
	v_lshl_add_u64 v[30:31], s[38:39], 0, v[20:21]
	v_lshl_add_u64 v[30:31], v[30:31], 0, v[0:1]
	global_store_dwordx4 v[30:31], v[10:13], off nt
	v_mov_b32_e32 v30, v17
	v_mov_b32_e32 v31, v29
	v_mov_b32_e32 v12, v15
	v_mov_b32_e32 v13, v27
	v_mov_b32_e32 v10, v14
	v_mov_b32_e32 v11, v26
	v_pk_mul_f32 v[12:13], v[12:13], v[12:13]
	v_pk_mul_f32 v[30:31], v[30:31], v[30:31]
	v_pk_fma_f32 v[10:11], v[10:11], v[10:11], v[12:13]
	v_mov_b32_e32 v12, v16
	v_mov_b32_e32 v13, v28
	v_pk_fma_f32 v[12:13], v[12:13], v[12:13], v[30:31]
	s_nop 0
	v_pk_add_f32 v[10:11], v[10:11], v[12:13]
	s_nop 0
	v_add_f32_e32 v30, v10, v11

; __device__ __forceinline__ u32x4 pack8(f32x4 a, f32x4 b) { u32x4 w; w.x = pk2(a[0], a[1]); w.y = pk2(a[2], a[3]); w.z = pk2(b[0], b[1]); w.w = pk2(b[2], b[3]); return w; }
;     __device__ __forceinline__ void operator()(const f32x4 (&acc)[2][2][4][2], const Unit& u, int ui, int wr, int wc, int fr, int fq, LAS unsigned char* lds) const {
;     ...
;                 for (int bj = 0; bj < 2; ++bj) {
;                     const int c = bj * 128 + wc * 32 + fq * 8;
;                     f32x4 v0 = acc[ai][bj][m][0] * rs, v1 = acc[ai][bj][m][1] * rs;
;                     if (pn < 6) { if (pn < 2) { v0 = v0 * QS_SB; v1 = v1 * QS_SB; } *(u32x4*)(QKV + (size_t)row * 1536 + pn * 256 + c) = pack8(v0, v1); }
.LBB0_572:
	v_mad_i64_i32 v[10:11], s[6:7], v18, s3, 0
	v_lshl_add_u64 v[10:11], s[36:37], 0, v[10:11]
	s_and_b64 vcc, exec, s[64:65]
	v_lshl_add_u64 v[10:11], s[62:63], 1, v[10:11]
	s_cbranch_vccz .LBB0_574
	v_pk_mul_f32 v[12:13], v[16:17], s[96:97] op_sel_hi:[1,0]
	v_pk_mul_f32 v[30:31], v[14:15], s[96:97] op_sel_hi:[1,0]
	v_pk_mul_f32 v[32:33], v[28:29], s[96:97] op_sel_hi:[1,0]
	v_pk_mul_f32 v[34:35], v[26:27], s[96:97] op_sel_hi:[1,0]
	v_cndmask_b32_e64 v25, v29, v33, s[12:13]
	v_cndmask_b32_e64 v28, v28, v32, s[12:13]
	v_cndmask_b32_e64 v27, v27, v35, s[12:13]
	v_cndmask_b32_e64 v26, v26, v34, s[12:13]
	v_cndmask_b32_e64 v13, v17, v13, s[12:13]
	v_cndmask_b32_e64 v16, v16, v12, s[12:13]
	v_cndmask_b32_e64 v12, v15, v31, s[12:13]
	v_cndmask_b32_e64 v14, v14, v30, s[12:13]
	v_cvt_pk_bf16_f32 v12, v14, v12
	v_cvt_pk_bf16_f32 v13, v16, v13
	v_cvt_pk_bf16_f32 v14, v26, v27
	v_cvt_pk_bf16_f32 v15, v28, v25
	v_lshl_add_u64 v[16:17], v[10:11], 0, v[0:1]
	v_mov_b32_e32 v30, 0
	global_store_dwordx4 v[16:17], v[12:15], off nt

; __device__ __forceinline__ float xor32(float x) { auto rr = __builtin_amdgcn_permlane32_swap(__float_as_uint(x), __float_as_uint(x), false, false); return __uint_as_float(((unsigned)(threadIdx.x & 32)) ? rr[0] : rr[1]); }
; __device__ __forceinline__ u32x4 pack8(f32x4 a, f32x4 b) { u32x4 w; w.x = pk2(a[0], a[1]); w.y = pk2(a[2], a[3]); w.z = pk2(b[0], b[1]); w.w = pk2(b[2], b[3]); return w; }
;     __device__ __forceinline__ void operator()(const f32x4 (&acc)[2][2][4][2], const Unit& u, int ui, int wr, int wc, int fr, int fq, LAS unsigned char* lds) const {
;     ...
;                     else if (wc == 0) {
;                         const int ib = 8 * (fq & 1);
;                         const f32x4 c0 = *(const f32x4*)(COS + (size_t)row * 16 + ib), c1 = *(const f32x4*)(COS + (size_t)row * 16 + ib + 4);
;                         const f32x4 s0 = *(const f32x4*)(SIN + (size_t)row * 16 + ib), s1 = *(const f32x4*)(SIN + (size_t)row * 16 + ib + 4);
;                         f32x4 p0, p1;
; #pragma unroll
;                         for (int i = 0; i < 4; ++i) { p0[i] = xor32(v0[i]); p1[i] = xor32(v1[i]); }
;                         const float sg = (fq < 2) ? -1.f : 1.f;
;                         const f32x4 o0 = v0 * c0 + p0 * s0 * sg, o1 = v1 * c1 + p1 * s1 * sg;
;                         *(u32x4*)(KR + (size_t)row * 32 + fq * 8) = pack8(o0, o1);
.LBB0_577:
	s_cmp_lt_i32 s26, 7
	s_cbranch_scc1 .LBB0_585
	s_cmp_lg_u32 s26, 7
	s_cbranch_scc0 .LBB0_582
	s_andn2_b64 vcc, exec, s[56:57]
	s_cbranch_vccnz .LBB0_581
	v_lshlrev_b64 v[32:33], 2, v[12:13]
	v_lshl_add_u64 v[14:15], s[44:45], 0, v[32:33]
	v_lshlrev_b32_e32 v34, 2, v128
	v_mov_b32_e32 v35, v1
	v_lshl_add_u64 v[32:33], s[46:47], 0, v[32:33]
	v_lshl_add_u64 v[24:25], v[14:15], 0, v[34:35]
	v_lshl_add_u64 v[36:37], v[32:33], 0, v[34:35]
	s_waitcnt vmcnt(6)
	v_mov_b32_e32 v14, v174
	v_mov_b32_e32 v15, v175
	v_mov_b32_e32 v16, v176
	v_mov_b32_e32 v17, v177
	v_mov_b32_e32 v24, v178
	v_mov_b32_e32 v25, v179
	v_mov_b32_e32 v26, v180
	v_mov_b32_e32 v27, v181
	v_mov_b32_e32 v32, v182
	v_mov_b32_e32 v33, v183
	v_mov_b32_e32 v34, v184
	v_mov_b32_e32 v35, v185
	v_mov_b32_e32 v36, v230
	v_mov_b32_e32 v37, v231
	v_mov_b32_e32 v38, v232
	v_mov_b32_e32 v39, v233
	v_mov_b32_e32 v31, v6
	v_mov_b32_e32 v40, v6
	s_nop 1
	v_permlane32_swap_b32_e32 v31, v40
	v_cndmask_b32_e64 v40, v31, v40, s[4:5]
	v_mov_b32_e32 v31, v2
	v_mov_b32_e32 v41, v2
	s_nop 1
	v_permlane32_swap_b32_e32 v31, v41
	v_cndmask_b32_e64 v42, v31, v41, s[4:5]
	v_mov_b32_e32 v31, v7
	v_mov_b32_e32 v41, v7
	s_nop 1
	v_permlane32_swap_b32_e32 v31, v41
	v_cndmask_b32_e64 v41, v31, v41, s[4:5]
	v_mov_b32_e32 v31, v3
	v_mov_b32_e32 v43, v3
	s_nop 1
	v_permlane32_swap_b32_e32 v31, v43
	v_cndmask_b32_e64 v43, v31, v43, s[4:5]
	v_mov_b32_e32 v31, v8
	v_mov_b32_e32 v44, v8
	s_nop 1
	v_permlane32_swap_b32_e32 v31, v44
	v_cndmask_b32_e64 v44, v31, v44, s[4:5]
	v_mov_b32_e32 v31, v4
	v_mov_b32_e32 v45, v4
	s_nop 1
	v_permlane32_swap_b32_e32 v31, v45
	v_cndmask_b32_e64 v46, v31, v45, s[4:5]
	v_mov_b32_e32 v31, v9
	v_mov_b32_e32 v45, v9
	s_nop 1
	v_permlane32_swap_b32_e32 v31, v45
	v_cndmask_b32_e64 v45, v31, v45, s[4:5]
	v_mov_b32_e32 v31, v5
	v_mov_b32_e32 v47, v5
	s_nop 1
	v_permlane32_swap_b32_e32 v31, v47
	v_cndmask_b32_e64 v47, v31, v47, s[4:5]
	v_lshlrev_b64 v[28:29], 6, v[18:19]
	s_waitcnt lgkmcnt(0)
	v_pk_mul_f32 v[34:35], v[34:35], v[44:45]
	v_pk_mul_f32 v[32:33], v[32:33], v[40:41]
	v_mov_b32_e32 v40, v114
	v_mov_b32_e32 v41, v114
	v_pk_mul_f32 v[32:33], v[114:115], v[32:33]
	v_pk_mul_f32 v[34:35], v[40:41], v[34:35]
	v_pk_fma_f32 v[14:15], v[6:7], v[14:15], v[32:33]
	v_pk_fma_f32 v[16:17], v[8:9], v[16:17], v[34:35]
	v_pk_mul_f32 v[32:33], v[38:39], v[46:47]
	v_pk_mul_f32 v[34:35], v[36:37], v[42:43]
	v_pk_mul_f32 v[32:33], v[40:41], v[32:33]
	v_pk_mul_f32 v[34:35], v[114:115], v[34:35]
	v_pk_fma_f32 v[26:27], v[4:5], v[26:27], v[32:33]
	v_pk_fma_f32 v[24:25], v[2:3], v[24:25], v[34:35]
	v_cvt_pk_bf16_f32 v14, v14, v15
	v_cvt_pk_bf16_f32 v15, v16, v17
	v_cvt_pk_bf16_f32 v16, v24, v25
	v_cvt_pk_bf16_f32 v17, v26, v27
	v_lshl_add_u64 v[24:25], s[42:43], 0, v[28:29]
	v_lshlrev_b32_e32 v26, 1, v149
	v_mov_b32_e32 v27, v1
	v_lshl_add_u64 v[24:25], v[24:25], 0, v[26:27]
	global_store_dwordx4 v[24:25], v[14:17], off nt

; __device__ __forceinline__ u32x4 pack8(f32x4 a, f32x4 b) { u32x4 w; w.x = pk2(a[0], a[1]); w.y = pk2(a[2], a[3]); w.z = pk2(b[0], b[1]); w.w = pk2(b[2], b[3]); return w; }
; __device__ __forceinline__ float sq8(const f32x4& a, const f32x4& b) { return ((a[0] * a[0] + a[1] * a[1]) + (a[2] * a[2] + a[3] * a[3])) + ((b[0] * b[0] + b[1] * b[1]) + (b[2] * b[2] + b[3] * b[3])); }
;     __device__ __forceinline__ void operator()(const f32x4 (&acc)[2][2][4][2], const Unit& u, int ui, int wr, int wc, int fr, int fq, LAS unsigned char* lds) const {
;     ...
;                 for (int bj = 0; bj < 2; ++bj) {
;                     const int c = bj * 128 + wc * 32 + fq * 8;
;                     f32x4 v0 = acc[ai][bj][m][0] * rs, v1 = acc[ai][bj][m][1] * rs;
;                     if (pn < 6) { if (pn < 2) { v0 = v0 * QS_SB; v1 = v1 * QS_SB; } *(u32x4*)(QKV + (size_t)row * 1536 + pn * 256 + c) = pack8(v0, v1); }
;                     else if (pn == 6) { *(u32x4*)(CKV + (size_t)row * 256 + c) = pack8(v0, v1); sq += sq8(v0, v1); }
;                     else if (pn == 7) { *(u32x4*)(CQ + (size_t)row * 384 + c) = pack8(v0, v1); sq += sq8(v0, v1); }
.LBB0_582:
	s_andn2_b64 vcc, exec, s[18:19]
	v_mov_b32_e32 v14, v30
	s_cbranch_vccnz .LBB0_584
	v_lshl_add_u64 v[22:23], s[40:41], 0, v[22:23]
	v_cvt_pk_bf16_f32 v14, v6, v7
	v_cvt_pk_bf16_f32 v15, v8, v9
	v_cvt_pk_bf16_f32 v16, v2, v3
	v_cvt_pk_bf16_f32 v17, v4, v5
	v_lshl_add_u64 v[22:23], v[22:23], 0, v[0:1]
	global_store_dwordx4 v[22:23], v[14:17], off offset:256 nt
	v_mov_b32_e32 v22, v9
	v_mov_b32_e32 v23, v5
	v_mov_b32_e32 v16, v7
	v_mov_b32_e32 v17, v3
	v_mov_b32_e32 v14, v6
	v_mov_b32_e32 v15, v2
	v_pk_mul_f32 v[16:17], v[16:17], v[16:17]
	v_pk_mul_f32 v[22:23], v[22:23], v[22:23]
	v_pk_fma_f32 v[14:15], v[14:15], v[14:15], v[16:17]
	v_mov_b32_e32 v16, v8
	v_mov_b32_e32 v17, v4
	v_pk_fma_f32 v[16:17], v[16:17], v[16:17], v[22:23]
	s_nop 0
	v_pk_add_f32 v[14:15], v[14:15], v[16:17]
	s_nop 0
	v_add_f32_e32 v14, v14, v15
	v_add_f32_e32 v14, v14, v30

; __device__ __forceinline__ u32x4 pack8(f32x4 a, f32x4 b) { u32x4 w; w.x = pk2(a[0], a[1]); w.y = pk2(a[2], a[3]); w.z = pk2(b[0], b[1]); w.w = pk2(b[2], b[3]); return w; }
; __device__ __forceinline__ float sq8(const f32x4& a, const f32x4& b) { return ((a[0] * a[0] + a[1] * a[1]) + (a[2] * a[2] + a[3] * a[3])) + ((b[0] * b[0] + b[1] * b[1]) + (b[2] * b[2] + b[3] * b[3])); }
;     __device__ __forceinline__ void operator()(const f32x4 (&acc)[2][2][4][2], const Unit& u, int ui, int wr, int wc, int fr, int fq, LAS unsigned char* lds) const {
;     ...
;                 for (int bj = 0; bj < 2; ++bj) {
;                     const int c = bj * 128 + wc * 32 + fq * 8;
;                     f32x4 v0 = acc[ai][bj][m][0] * rs, v1 = acc[ai][bj][m][1] * rs;
;                     if (pn < 6) { if (pn < 2) { v0 = v0 * QS_SB; v1 = v1 * QS_SB; } *(u32x4*)(QKV + (size_t)row * 1536 + pn * 256 + c) = pack8(v0, v1); }
;                     else if (pn == 6) { *(u32x4*)(CKV + (size_t)row * 256 + c) = pack8(v0, v1); sq += sq8(v0, v1); }
.LBB0_585:
	s_andn2_b64 vcc, exec, s[18:19]
	s_cbranch_vccnz .LBB0_587
	v_lshl_add_u64 v[20:21], s[38:39], 0, v[20:21]
	v_cvt_pk_bf16_f32 v14, v6, v7
	v_cvt_pk_bf16_f32 v15, v8, v9
	v_cvt_pk_bf16_f32 v16, v2, v3
	v_cvt_pk_bf16_f32 v17, v4, v5
	v_lshl_add_u64 v[20:21], v[20:21], 0, v[0:1]
	global_store_dwordx4 v[20:21], v[14:17], off offset:256 nt
	v_mov_b32_e32 v20, v9
	v_mov_b32_e32 v21, v5
	v_mov_b32_e32 v16, v7
	v_mov_b32_e32 v17, v3
	v_mov_b32_e32 v14, v6
	v_mov_b32_e32 v15, v2
	v_pk_mul_f32 v[16:17], v[16:17], v[16:17]
	v_pk_mul_f32 v[20:21], v[20:21], v[20:21]
	v_pk_fma_f32 v[14:15], v[14:15], v[14:15], v[16:17]
	v_mov_b32_e32 v16, v8
	v_mov_b32_e32 v17, v4
	v_pk_fma_f32 v[16:17], v[16:17], v[16:17], v[20:21]
	s_nop 0
	v_pk_add_f32 v[14:15], v[14:15], v[16:17]
	s_nop 0
	v_add_f32_e32 v14, v14, v15
	v_add_f32_e32 v14, v14, v30

; __device__ __forceinline__ u32x4 pack8(f32x4 a, f32x4 b) { u32x4 w; w.x = pk2(a[0], a[1]); w.y = pk2(a[2], a[3]); w.z = pk2(b[0], b[1]); w.w = pk2(b[2], b[3]); return w; }
;     __device__ __forceinline__ void operator()(const f32x4 (&acc)[2][2][4][2], const Unit& u, int ui, int wr, int wc, int fr, int fq, LAS unsigned char* lds) const {
;     ...
;                 for (int bj = 0; bj < 2; ++bj) {
;                     const int c = bj * 128 + wc * 32 + fq * 8;
;                     f32x4 v0 = acc[ai][bj][m][0] * rs, v1 = acc[ai][bj][m][1] * rs;
;                     if (pn < 6) { if (pn < 2) { v0 = v0 * QS_SB; v1 = v1 * QS_SB; } *(u32x4*)(QKV + (size_t)row * 1536 + pn * 256 + c) = pack8(v0, v1); }
.LBB0_588:
	v_pk_mul_f32 v[14:15], v[8:9], s[96:97] op_sel_hi:[1,0]
	v_pk_mul_f32 v[16:17], v[6:7], s[96:97] op_sel_hi:[1,0]
	v_pk_mul_f32 v[20:21], v[4:5], s[96:97] op_sel_hi:[1,0]
	v_pk_mul_f32 v[22:23], v[2:3], s[96:97] op_sel_hi:[1,0]
	v_cndmask_b32_e64 v5, v5, v21, s[12:13]
	v_cndmask_b32_e64 v20, v4, v20, s[12:13]
	v_cndmask_b32_e64 v4, v3, v23, s[12:13]
	v_cndmask_b32_e64 v21, v2, v22, s[12:13]
	v_cndmask_b32_e64 v3, v9, v15, s[12:13]
	v_cndmask_b32_e64 v8, v8, v14, s[12:13]
	v_cndmask_b32_e64 v2, v7, v17, s[12:13]
	v_cndmask_b32_e64 v6, v6, v16, s[12:13]
	v_cvt_pk_bf16_f32 v2, v6, v2
	v_cvt_pk_bf16_f32 v3, v8, v3
	v_cvt_pk_bf16_f32 v4, v21, v4
	v_cvt_pk_bf16_f32 v5, v20, v5
	v_lshl_add_u64 v[6:7], v[10:11], 0, v[0:1]
	v_mov_b32_e32 v14, v30
	global_store_dwordx4 v[6:7], v[2:5], off offset:256 nt
	s_and_b64 vcc, exec, s[20:21]
	s_cbranch_vccnz .LBB0_592
